# LRU v4: backward-pass output through an LDS tile, stored as whole 128-byte rows
# baseline (speedup 1.0000x reference)
.LBB0_1451:
	s_load_dwordx4 s[0:3], s[8:9], 0x138
	s_waitcnt lgkmcnt(0)
	s_mov_b64 s[4:5], s[0:1]
	s_cmp_lt_i32 s4, 12
	s_cselect_b64 s[0:1], -1, 0
	s_cmp_gt_i32 s5, 11
	s_cselect_b64 s[2:3], -1, 0
	s_and_b64 s[0:1], s[0:1], s[2:3]
	s_andn2_b64 vcc, exec, s[0:1]
	s_cbranch_vccnz .LBB0_1535
	s_mov_b64 s[24:25], s[8:9]
	v_mbcnt_lo_u32_b32 v202, -1, 0
	v_mbcnt_hi_u32_b32 v202, -1, v202
	s_load_dword s0, s[8:9], 0x148
	s_waitcnt lgkmcnt(0)
	v_writelane_b32 v241, s0, 18
	s_nop 1
	v_writelane_b32 v241, s1, 19
	s_add_u32 s0, s8, 0x148
	s_addc_u32 s1, s9, 0
	v_writelane_b32 v241, s0, 34
	s_nop 1
	v_writelane_b32 v241, s1, 35
	v_readlane_b32 s0, v243, 0
	s_cmpk_gt_i32 s0, 0xff
	v_readlane_b32 s1, v243, 1
	s_cbranch_scc1 .LBB0_1482
	v_readlane_b32 s0, v243, 7
	v_readlane_b32 s1, v243, 8
	v_readlane_b32 s4, v243, 0
	v_readlane_b32 s6, v243, 12
	s_load_dwordx2 s[2:3], s[0:1], 0x130
	s_lshr_b32 s7, s6, 2
	s_and_b32 s8, s6, 3
	s_bfe_u32 s11, s4, 0x20003
	s_lshr_b32 s50, s4, 5
	s_lshl_b32 s50, s50, 3
	s_and_b32 s51, s4, 7
	s_or_b32 s50, s50, s51
	s_lshr_b32 s9, s50, 2
	s_and_b32 s10, s50, 3
	v_and_b32_e32 v160, 15, v202
	v_lshrrev_b32_e32 v161, 4, v202
	v_lshlrev_b32_e32 v209, 2, v202
	s_lshl_b32 s50, s7, 15
	v_xor_b32_e32 v178, v161, v160
	v_lshlrev_b32_e32 v178, 4, v178
	v_lshl_add_u32 v162, v160, 9, v178
	v_add_u32_e32 v162, s50, v162
	s_lshl_b32 s51, s11, 6
	s_lshl_b32 s52, s8, 4
	s_add_i32 s51, s51, s52
	v_add_u32_e32 v179, s51, v160
	v_lshrrev_b32_e32 v180, 3, v179
	v_and_b32_e32 v181, 7, v179
	v_lshlrev_b32_e32 v181, 1, v181
	v_lshlrev_b32_e32 v182, 2, v161
	v_add_u32_e32 v183, 0, v182
	v_xor_b32_e32 v184, v180, v183
	v_lshlrev_b32_e32 v184, 4, v184
	v_lshl_add_u32 v184, v183, 9, v184
	v_add3_u32 v165, v184, v181, s50
	v_add_u32_e32 v183, 1, v182
	v_xor_b32_e32 v184, v180, v183
	v_lshlrev_b32_e32 v184, 4, v184
	v_lshl_add_u32 v184, v183, 9, v184
	v_add3_u32 v166, v184, v181, s50
	v_add_u32_e32 v183, 2, v182
	v_xor_b32_e32 v184, v180, v183
	v_lshlrev_b32_e32 v184, 4, v184
	v_lshl_add_u32 v184, v183, 9, v184
	v_add3_u32 v167, v184, v181, s50
	v_add_u32_e32 v183, 3, v182
	v_xor_b32_e32 v184, v180, v183
	v_lshlrev_b32_e32 v184, 4, v184
	v_lshl_add_u32 v184, v183, 9, v184
	v_add3_u32 v168, v184, v181, s50
	v_lshrrev_b32_e32 v185, 5, v202
	v_and_b32_e32 v186, 31, v202
	s_lshl_b32 s51, s6, 4
	v_add_u32_e32 v187, 0, v185
	v_xor_b32_e32 v188, v186, v187
	v_lshlrev_b32_e32 v188, 4, v188
	v_add_u32_e32 v187, s51, v187
	v_lshl_add_u32 v211, v187, 11, v188
	v_add_u32_e32 v187, 2, v185
	v_xor_b32_e32 v188, v186, v187
	v_lshlrev_b32_e32 v188, 4, v188
	v_add_u32_e32 v187, s51, v187
	v_lshl_add_u32 v212, v187, 11, v188
	v_add_u32_e32 v187, 4, v185
	v_xor_b32_e32 v188, v186, v187
	v_lshlrev_b32_e32 v188, 4, v188
	v_add_u32_e32 v187, s51, v187
	v_lshl_add_u32 v213, v187, 11, v188
	v_add_u32_e32 v187, 6, v185
	v_xor_b32_e32 v188, v186, v187
	v_lshlrev_b32_e32 v188, 4, v188
	v_add_u32_e32 v187, s51, v187
	v_lshl_add_u32 v214, v187, 11, v188
	v_add_u32_e32 v187, 8, v185
	v_xor_b32_e32 v188, v186, v187
	v_lshlrev_b32_e32 v188, 4, v188
	v_add_u32_e32 v187, s51, v187
	v_lshl_add_u32 v215, v187, 11, v188
	v_add_u32_e32 v187, 10, v185
	v_xor_b32_e32 v188, v186, v187
	v_lshlrev_b32_e32 v188, 4, v188
	v_add_u32_e32 v187, s51, v187
	v_lshl_add_u32 v216, v187, 11, v188
	v_add_u32_e32 v187, 12, v185
	v_xor_b32_e32 v188, v186, v187
	v_lshlrev_b32_e32 v188, 4, v188
	v_add_u32_e32 v187, s51, v187
	v_lshl_add_u32 v217, v187, 11, v188
	v_add_u32_e32 v187, 14, v185
	v_xor_b32_e32 v188, v186, v187
	v_lshlrev_b32_e32 v188, 4, v188
	v_add_u32_e32 v187, s51, v187
	v_lshl_add_u32 v218, v187, 11, v188
	s_lshl_b32 s51, s6, 7
	s_add_i32 s51, s51, 0x20000
	v_lshl_add_u32 v207, v160, 3, s51
	s_lshl_b32 s51, s8, 7
	s_add_i32 s51, s51, 0x20000
	v_lshl_add_u32 v208, v160, 3, s51
	s_lshl_b32 s51, s7, 6
	v_add_u32_e32 v189, s51, v182
	s_lshl_b32 s51, s8, 4
	v_add_u32_e32 v190, s51, v160
	v_lshlrev_b32_e32 v190, 1, v190
	v_lshl_add_u32 v210, v189, 11, v190
	s_lshl_b32 s51, s7, 13
	s_add_i32 s51, s51, 0x20800
	v_lshlrev_b32_e32 v191, 9, v161
	s_lshl_b32 s52, s8, 5
	v_lshl_add_u32 v192, v160, 1, s52
	v_add3_u32 v169, v191, v192, s51
	v_lshrrev_b32_e32 v191, 3, v202
	v_and_b32_e32 v192, 7, v202
	s_lshl_b32 s52, s8, 4
	v_add_u32_e32 v191, s52, v191
	v_lshlrev_b32_e32 v192, 4, v192
	v_lshl_add_u32 v170, v191, 7, v192
	v_add_u32_e32 v170, s51, v170
	s_lshl_b32 s52, s7, 6
	v_add_u32_e32 v191, s52, v191
	v_lshl_add_u32 v171, v191, 11, v192
	v_add_u32_e32 v172, 0x4000, v171
	s_waitcnt lgkmcnt(0)
	s_lshl_b32 s50, s10, 9
	s_add_u32 s16, s2, s50
	s_addc_u32 s17, s3, 0
	s_add_u32 s16, s16, 0x1b900000
	s_addc_u32 s17, s17, 0
	s_lshl_b32 s50, s10, 9
	s_lshl_b32 s51, s11, 7
	s_add_i32 s50, s50, s51
	s_add_u32 s18, s2, s50
	s_addc_u32 s19, s3, 0
	s_add_u32 s18, s18, 0x13100000
	s_addc_u32 s19, s19, 0
	s_add_u32 s20, s2, s50
	s_addc_u32 s21, s3, 0
	s_add_u32 s20, s20, 0x29100000
	s_addc_u32 s21, s21, 0
	s_lshl_b32 s50, s4, 18
	s_add_u32 s22, s2, s50
	s_addc_u32 s23, s3, 0
	s_add_u32 s22, s22, 0x20100000
	s_addc_u32 s23, s23, 0
	s_lshl_b32 s50, s10, 10
	s_lshl_b32 s51, s11, 6
	s_add_i32 s50, s50, s51
	s_lshl_b32 s51, s8, 4
	s_add_i32 s50, s50, s51
	s_add_i32 s50, s50, 0
	s_lshl_b32 s50, s50, 9
	s_add_u32 s46, s2, s50
	s_addc_u32 s47, s3, 0
	s_add_u32 s46, s46, 0x1000000
	s_addc_u32 s47, s47, 0
	s_add_u32 s48, s46, 0x20000
	s_addc_u32 s49, s47, 0
	v_lshlrev_b32_e32 v178, 9, v160
	v_lshl_add_u32 v178, v161, 4, v178
	global_load_dwordx4 v[0:3], v178, s[46:47]
	global_load_dwordx4 v[4:7], v178, s[46:47] offset:64
	global_load_dwordx4 v[8:11], v178, s[46:47] offset:128
	global_load_dwordx4 v[12:15], v178, s[46:47] offset:192
	global_load_dwordx4 v[16:19], v178, s[46:47] offset:256
	global_load_dwordx4 v[20:23], v178, s[46:47] offset:320
	global_load_dwordx4 v[24:27], v178, s[46:47] offset:384
	global_load_dwordx4 v[28:31], v178, s[46:47] offset:448
	global_load_dwordx4 v[32:35], v178, s[48:49]
	global_load_dwordx4 v[36:39], v178, s[48:49] offset:64
	global_load_dwordx4 v[40:43], v178, s[48:49] offset:128
	global_load_dwordx4 v[44:47], v178, s[48:49] offset:192
	global_load_dwordx4 v[48:51], v178, s[48:49] offset:256
	global_load_dwordx4 v[52:55], v178, s[48:49] offset:320
	global_load_dwordx4 v[56:59], v178, s[48:49] offset:384
	global_load_dwordx4 v[60:63], v178, s[48:49] offset:448
	s_load_dwordx2 s[46:47], s[0:1], 0xa0
	s_load_dwordx2 s[48:49], s[0:1], 0xb0
	s_load_dwordx2 s[40:41], s[0:1], 0xb8
	s_lshl_b32 s50, s10, 8
	s_lshl_b32 s51, s11, 6
	s_add_i32 s50, s50, s51
	s_lshl_b32 s51, s8, 4
	s_add_i32 s50, s50, s51
	v_add_u32_e32 v179, s50, v160
	v_lshlrev_b32_e32 v179, 2, v179
	s_waitcnt lgkmcnt(0)
	global_load_dword v173, v179, s[46:47]
	global_load_dword v174, v179, s[48:49]
	global_load_dword v175, v179, s[40:41]
	v_cmp_le_u32_e64 s[34:35], 16, v202
	v_cmp_le_u32_e64 s[36:37], 32, v202
	v_add_u32_e32 v204, -16, v202
	v_add_u32_e32 v205, -32, v202
	v_add_u32_e32 v206, 48, v160
	s_cmp_eq_u32 s7, 1
	s_cselect_b64 s[38:39], -1, 0
	v_and_b32_e32 v204, 63, v204
	v_lshlrev_b32_e32 v204, 2, v204
	v_and_b32_e32 v205, 63, v205
	v_lshlrev_b32_e32 v205, 2, v205
	v_and_b32_e32 v206, 63, v206
	v_lshlrev_b32_e32 v206, 2, v206
	v_mov_b32_e32 v176, 0
	s_mov_b32 s53, 0xbfb8aa3b
	s_waitcnt vmcnt(0)
	v_mul_f32_e32 v173, s53, v173
	v_mul_f32_e32 v174, s53, v174
	v_mul_f32_e32 v175, s53, v175
	v_exp_f32_e32 v175, v175
	s_nop 0
	v_add_f32_e32 v180, 1.0, v175
	v_log_f32_e32 v180, v180
	v_mov_b32_e32 v181, 0x3eaaaaab
	v_fma_f32 v181, v175, v181, -0.5
	v_fma_f32 v181, v175, v181, 1.0
	v_mul_f32_e32 v181, v175, v181
	v_mul_f32_e32 v181, 0x3fb8aa3b, v181
	v_cmp_gt_f32_e32 vcc, 0x3cf5c28f, v175
	s_nop 1
	v_cndmask_b32_e32 v175, v180, v181, vcc
	v_mul_f32_e32 v175, 0xc1000000, v175
	s_mov_b32 s13, 0
	s_barrier
	s_cmp_lt_u32 s13, 2
	s_lshl_b32 s50, s13, 7
	s_lshl_b32 s51, s9, 8
	s_add_i32 s51, s51, 0x8000
	s_add_i32 s51, s51, s50
	s_lshl_b32 s59, s9, 11
	s_add_i32 s59, s59, s50
	s_addk_i32 s59, 0xff00
	s_cmp_lt_u32 s13, 2
	s_cselect_b32 s59, s51, s59
	s_lshl_b32 s52, s59, 11
	s_add_u32 s46, s16, s52
	s_addc_u32 s47, s17, 0
	s_lshl_b32 s52, s6, 13
	s_mov_b32 m0, s52
	s_add_i32 s52, s52, 0x400
	global_load_lds_dwordx4 v211, s[46:47]
	s_mov_b32 m0, s52
	s_add_i32 s52, s52, 0x400
	global_load_lds_dwordx4 v212, s[46:47]
	s_mov_b32 m0, s52
	s_add_i32 s52, s52, 0x400
	global_load_lds_dwordx4 v213, s[46:47]
	s_mov_b32 m0, s52
	s_add_i32 s52, s52, 0x400
	global_load_lds_dwordx4 v214, s[46:47]
	s_mov_b32 m0, s52
	s_add_i32 s52, s52, 0x400
	global_load_lds_dwordx4 v215, s[46:47]
	s_mov_b32 m0, s52
	s_add_i32 s52, s52, 0x400
	global_load_lds_dwordx4 v216, s[46:47]
	s_mov_b32 m0, s52
	s_add_i32 s52, s52, 0x400
	global_load_lds_dwordx4 v217, s[46:47]
	s_mov_b32 m0, s52
	s_nop 0
	global_load_lds_dwordx4 v218, s[46:47]
	s_waitcnt vmcnt(0)
	s_barrier
	s_cmp_eq_u32 s13, 17
	s_cbranch_scc1 .Lmylru_nodma_1
	s_add_i32 s58, s13, 1
	s_cmp_lt_u32 s58, 2
	s_lshl_b32 s50, s58, 7
	s_lshl_b32 s51, s9, 8
	s_add_i32 s51, s51, 0x8000
	s_add_i32 s51, s51, s50
	s_lshl_b32 s59, s9, 11
	s_add_i32 s59, s59, s50
	s_addk_i32 s59, 0xff00
	s_cmp_lt_u32 s58, 2
	s_cselect_b32 s59, s51, s59
	s_lshl_b32 s52, s59, 11
	s_add_u32 s46, s16, s52
	s_addc_u32 s47, s17, 0
	s_lshl_b32 s52, s6, 13
	s_add_i32 s52, s52, 0x10000
	s_mov_b32 m0, s52
	s_add_i32 s52, s52, 0x400
	global_load_lds_dwordx4 v211, s[46:47]
	s_mov_b32 m0, s52
	s_add_i32 s52, s52, 0x400
	global_load_lds_dwordx4 v212, s[46:47]
	s_mov_b32 m0, s52
	s_add_i32 s52, s52, 0x400
	global_load_lds_dwordx4 v213, s[46:47]
	s_mov_b32 m0, s52
	s_add_i32 s52, s52, 0x400
	global_load_lds_dwordx4 v214, s[46:47]
	s_mov_b32 m0, s52
	s_add_i32 s52, s52, 0x400
	global_load_lds_dwordx4 v215, s[46:47]
	s_mov_b32 m0, s52
	s_add_i32 s52, s52, 0x400
	global_load_lds_dwordx4 v216, s[46:47]
	s_mov_b32 m0, s52
	s_add_i32 s52, s52, 0x400
	global_load_lds_dwordx4 v217, s[46:47]
	s_mov_b32 m0, s52
	s_nop 0
	global_load_lds_dwordx4 v218, s[46:47]
.Lmylru_nodma_1:
	v_mov_b32_e32 v163, v162
	ds_read_b128 v[96:99], v163
	ds_read_b128 v[100:103], v163 offset:8192
	ds_read_b128 v[104:107], v163 offset:16384
	ds_read_b128 v[108:111], v163 offset:24576
	v_xor_b32_e32 v164, 0x40, v163
	ds_read_b128 v[112:115], v164
	ds_read_b128 v[116:119], v164 offset:8192
	ds_read_b128 v[120:123], v164 offset:16384
	ds_read_b128 v[124:127], v164 offset:24576
	s_waitcnt lgkmcnt(7)
	v_mfma_f32_16x16x32_bf16 v[64:67], v[96:99], v[0:3], 0
	v_mfma_f32_16x16x32_bf16 v[68:71], v[96:99], v[32:35], 0
	v_xor_b32_e32 v164, 0x80, v163
	ds_read_b128 v[96:99], v164
	s_waitcnt lgkmcnt(7)
	v_mfma_f32_16x16x32_bf16 v[72:75], v[100:103], v[0:3], 0
	v_mfma_f32_16x16x32_bf16 v[76:79], v[100:103], v[32:35], 0
	ds_read_b128 v[100:103], v164 offset:8192
	s_waitcnt lgkmcnt(7)
	v_mfma_f32_16x16x32_bf16 v[80:83], v[104:107], v[0:3], 0
	v_mfma_f32_16x16x32_bf16 v[84:87], v[104:107], v[32:35], 0
	ds_read_b128 v[104:107], v164 offset:16384
	s_waitcnt lgkmcnt(7)
	v_mfma_f32_16x16x32_bf16 v[88:91], v[108:111], v[0:3], 0
	v_mfma_f32_16x16x32_bf16 v[92:95], v[108:111], v[32:35], 0
	ds_read_b128 v[108:111], v164 offset:24576
	s_waitcnt lgkmcnt(7)
	v_mfma_f32_16x16x32_bf16 v[64:67], v[112:115], v[4:7], v[64:67]
	v_mfma_f32_16x16x32_bf16 v[68:71], v[112:115], v[36:39], v[68:71]
	v_xor_b32_e32 v164, 0xc0, v163
	ds_read_b128 v[112:115], v164
	s_waitcnt lgkmcnt(7)
	v_mfma_f32_16x16x32_bf16 v[72:75], v[116:119], v[4:7], v[72:75]
	v_mfma_f32_16x16x32_bf16 v[76:79], v[116:119], v[36:39], v[76:79]
	ds_read_b128 v[116:119], v164 offset:8192
	s_waitcnt lgkmcnt(7)
	v_mfma_f32_16x16x32_bf16 v[80:83], v[120:123], v[4:7], v[80:83]
	v_mfma_f32_16x16x32_bf16 v[84:87], v[120:123], v[36:39], v[84:87]
	ds_read_b128 v[120:123], v164 offset:16384
	s_waitcnt lgkmcnt(7)
	v_mfma_f32_16x16x32_bf16 v[88:91], v[124:127], v[4:7], v[88:91]
	v_mfma_f32_16x16x32_bf16 v[92:95], v[124:127], v[36:39], v[92:95]
	ds_read_b128 v[124:127], v164 offset:24576
	s_waitcnt lgkmcnt(7)
	v_mfma_f32_16x16x32_bf16 v[64:67], v[96:99], v[8:11], v[64:67]
	v_mfma_f32_16x16x32_bf16 v[68:71], v[96:99], v[40:43], v[68:71]
	v_xor_b32_e32 v164, 0x100, v163
	ds_read_b128 v[96:99], v164
	s_waitcnt lgkmcnt(7)
	v_mfma_f32_16x16x32_bf16 v[72:75], v[100:103], v[8:11], v[72:75]
	v_mfma_f32_16x16x32_bf16 v[76:79], v[100:103], v[40:43], v[76:79]
	ds_read_b128 v[100:103], v164 offset:8192
	s_waitcnt lgkmcnt(7)
	v_mfma_f32_16x16x32_bf16 v[80:83], v[104:107], v[8:11], v[80:83]
	v_mfma_f32_16x16x32_bf16 v[84:87], v[104:107], v[40:43], v[84:87]
	ds_read_b128 v[104:107], v164 offset:16384
	s_waitcnt lgkmcnt(7)
	v_mfma_f32_16x16x32_bf16 v[88:91], v[108:111], v[8:11], v[88:91]
	v_mfma_f32_16x16x32_bf16 v[92:95], v[108:111], v[40:43], v[92:95]
	ds_read_b128 v[108:111], v164 offset:24576
	s_waitcnt lgkmcnt(7)
	v_mfma_f32_16x16x32_bf16 v[64:67], v[112:115], v[12:15], v[64:67]
	v_mfma_f32_16x16x32_bf16 v[68:71], v[112:115], v[44:47], v[68:71]
	v_xor_b32_e32 v164, 0x140, v163
	ds_read_b128 v[112:115], v164
	s_waitcnt lgkmcnt(7)
	v_mfma_f32_16x16x32_bf16 v[72:75], v[116:119], v[12:15], v[72:75]
	v_mfma_f32_16x16x32_bf16 v[76:79], v[116:119], v[44:47], v[76:79]
	ds_read_b128 v[116:119], v164 offset:8192
	s_waitcnt lgkmcnt(7)
	v_mfma_f32_16x16x32_bf16 v[80:83], v[120:123], v[12:15], v[80:83]
	v_mfma_f32_16x16x32_bf16 v[84:87], v[120:123], v[44:47], v[84:87]
	ds_read_b128 v[120:123], v164 offset:16384
	s_waitcnt lgkmcnt(7)
	v_mfma_f32_16x16x32_bf16 v[88:91], v[124:127], v[12:15], v[88:91]
	v_mfma_f32_16x16x32_bf16 v[92:95], v[124:127], v[44:47], v[92:95]
	ds_read_b128 v[124:127], v164 offset:24576
	s_waitcnt lgkmcnt(7)
	v_mfma_f32_16x16x32_bf16 v[64:67], v[96:99], v[16:19], v[64:67]
	v_mfma_f32_16x16x32_bf16 v[68:71], v[96:99], v[48:51], v[68:71]
	v_xor_b32_e32 v164, 0x180, v163
	ds_read_b128 v[96:99], v164
	s_waitcnt lgkmcnt(7)
	v_mfma_f32_16x16x32_bf16 v[72:75], v[100:103], v[16:19], v[72:75]
	v_mfma_f32_16x16x32_bf16 v[76:79], v[100:103], v[48:51], v[76:79]
	ds_read_b128 v[100:103], v164 offset:8192
	s_waitcnt lgkmcnt(7)
	v_mfma_f32_16x16x32_bf16 v[80:83], v[104:107], v[16:19], v[80:83]
	v_mfma_f32_16x16x32_bf16 v[84:87], v[104:107], v[48:51], v[84:87]
	ds_read_b128 v[104:107], v164 offset:16384
	s_waitcnt lgkmcnt(7)
	v_mfma_f32_16x16x32_bf16 v[88:91], v[108:111], v[16:19], v[88:91]
	v_mfma_f32_16x16x32_bf16 v[92:95], v[108:111], v[48:51], v[92:95]
	ds_read_b128 v[108:111], v164 offset:24576
	s_waitcnt lgkmcnt(7)
	v_mfma_f32_16x16x32_bf16 v[64:67], v[112:115], v[20:23], v[64:67]
	v_mfma_f32_16x16x32_bf16 v[68:71], v[112:115], v[52:55], v[68:71]
	v_xor_b32_e32 v164, 0x1c0, v163
	ds_read_b128 v[112:115], v164
	s_waitcnt lgkmcnt(7)
	v_mfma_f32_16x16x32_bf16 v[72:75], v[116:119], v[20:23], v[72:75]
	v_mfma_f32_16x16x32_bf16 v[76:79], v[116:119], v[52:55], v[76:79]
	ds_read_b128 v[116:119], v164 offset:8192
	s_waitcnt lgkmcnt(7)
	v_mfma_f32_16x16x32_bf16 v[80:83], v[120:123], v[20:23], v[80:83]
	v_mfma_f32_16x16x32_bf16 v[84:87], v[120:123], v[52:55], v[84:87]
	ds_read_b128 v[120:123], v164 offset:16384
	s_waitcnt lgkmcnt(7)
	v_mfma_f32_16x16x32_bf16 v[88:91], v[124:127], v[20:23], v[88:91]
	v_mfma_f32_16x16x32_bf16 v[92:95], v[124:127], v[52:55], v[92:95]
	ds_read_b128 v[124:127], v164 offset:24576
	s_waitcnt lgkmcnt(7)
	v_mfma_f32_16x16x32_bf16 v[64:67], v[96:99], v[24:27], v[64:67]
	v_mfma_f32_16x16x32_bf16 v[68:71], v[96:99], v[56:59], v[68:71]
	s_waitcnt lgkmcnt(6)
	v_mfma_f32_16x16x32_bf16 v[72:75], v[100:103], v[24:27], v[72:75]
	v_mfma_f32_16x16x32_bf16 v[76:79], v[100:103], v[56:59], v[76:79]
	s_waitcnt lgkmcnt(5)
	v_mfma_f32_16x16x32_bf16 v[80:83], v[104:107], v[24:27], v[80:83]
	v_mfma_f32_16x16x32_bf16 v[84:87], v[104:107], v[56:59], v[84:87]
	s_waitcnt lgkmcnt(4)
	v_mfma_f32_16x16x32_bf16 v[88:91], v[108:111], v[24:27], v[88:91]
	v_mfma_f32_16x16x32_bf16 v[92:95], v[108:111], v[56:59], v[92:95]
	s_waitcnt lgkmcnt(3)
	v_mfma_f32_16x16x32_bf16 v[64:67], v[112:115], v[28:31], v[64:67]
	v_mfma_f32_16x16x32_bf16 v[68:71], v[112:115], v[60:63], v[68:71]
	s_waitcnt lgkmcnt(2)
	v_mfma_f32_16x16x32_bf16 v[72:75], v[116:119], v[28:31], v[72:75]
	v_mfma_f32_16x16x32_bf16 v[76:79], v[116:119], v[60:63], v[76:79]
	s_waitcnt lgkmcnt(1)
	v_mfma_f32_16x16x32_bf16 v[80:83], v[120:123], v[28:31], v[80:83]
	v_mfma_f32_16x16x32_bf16 v[84:87], v[120:123], v[60:63], v[84:87]
	s_waitcnt lgkmcnt(0)
	v_mfma_f32_16x16x32_bf16 v[88:91], v[124:127], v[28:31], v[88:91]
	v_mfma_f32_16x16x32_bf16 v[92:95], v[124:127], v[60:63], v[92:95]
	v_mov_b32_e32 v198, v165
	v_mov_b32_e32 v199, v166
	v_mov_b32_e32 v200, v167
	v_mov_b32_e32 v201, v168
	ds_read_u16 v144, v198
	ds_read_u16 v145, v199
	ds_read_u16 v146, v200
	ds_read_u16 v147, v201
	ds_read_u16 v148, v198 offset:8192
	ds_read_u16 v149, v199 offset:8192
	ds_read_u16 v150, v200 offset:8192
	ds_read_u16 v151, v201 offset:8192
	ds_read_u16 v152, v198 offset:16384
	ds_read_u16 v153, v199 offset:16384
	ds_read_u16 v154, v200 offset:16384
	ds_read_u16 v155, v201 offset:16384
	ds_read_u16 v156, v198 offset:24576
	ds_read_u16 v157, v199 offset:24576
	ds_read_u16 v158, v200 offset:24576
	ds_read_u16 v159, v201 offset:24576
	s_nop 7
	v_fma_f32 v178, v64, s53, v173
	v_fma_f32 v179, v65, s53, v173
	v_fma_f32 v180, v66, s53, v173
	v_fma_f32 v181, v67, s53, v173
	v_fma_f32 v182, v72, s53, v173
	v_fma_f32 v183, v73, s53, v173
	v_fma_f32 v184, v74, s53, v173
	v_fma_f32 v185, v75, s53, v173
	v_fma_f32 v186, v68, s53, v174
	v_fma_f32 v187, v69, s53, v174
	v_fma_f32 v188, v70, s53, v174
	v_fma_f32 v189, v71, s53, v174
	v_fma_f32 v190, v76, s53, v174
	v_fma_f32 v191, v77, s53, v174
	v_fma_f32 v192, v78, s53, v174
	v_fma_f32 v193, v79, s53, v174
	v_exp_f32_e32 v178, v178
	v_exp_f32_e32 v179, v179
	v_exp_f32_e32 v180, v180
	v_exp_f32_e32 v181, v181
	v_exp_f32_e32 v182, v182
	v_exp_f32_e32 v183, v183
	v_exp_f32_e32 v184, v184
	v_exp_f32_e32 v185, v185
	v_exp_f32_e32 v186, v186
	v_exp_f32_e32 v187, v187
	v_exp_f32_e32 v188, v188
	v_exp_f32_e32 v189, v189
	v_exp_f32_e32 v190, v190
	v_exp_f32_e32 v191, v191
	v_exp_f32_e32 v192, v192
	v_exp_f32_e32 v193, v193
	v_add_f32_e32 v178, 1.0, v178
	v_add_f32_e32 v179, 1.0, v179
	v_add_f32_e32 v180, 1.0, v180
	v_add_f32_e32 v181, 1.0, v181
	v_add_f32_e32 v182, 1.0, v182
	v_add_f32_e32 v183, 1.0, v183
	v_add_f32_e32 v184, 1.0, v184
	v_add_f32_e32 v185, 1.0, v185
	v_add_f32_e32 v186, 1.0, v186
	v_add_f32_e32 v187, 1.0, v187
	v_add_f32_e32 v188, 1.0, v188
	v_add_f32_e32 v189, 1.0, v189
	v_add_f32_e32 v190, 1.0, v190
	v_add_f32_e32 v191, 1.0, v191
	v_add_f32_e32 v192, 1.0, v192
	v_add_f32_e32 v193, 1.0, v193
	v_rcp_f32_e32 v178, v178
	v_rcp_f32_e32 v179, v179
	v_rcp_f32_e32 v180, v180
	v_rcp_f32_e32 v181, v181
	v_rcp_f32_e32 v182, v182
	v_rcp_f32_e32 v183, v183
	v_rcp_f32_e32 v184, v184
	v_rcp_f32_e32 v185, v185
	v_rcp_f32_e32 v186, v186
	v_rcp_f32_e32 v187, v187
	v_rcp_f32_e32 v188, v188
	v_rcp_f32_e32 v189, v189
	v_rcp_f32_e32 v190, v190
	v_rcp_f32_e32 v191, v191
	v_rcp_f32_e32 v192, v192
	v_rcp_f32_e32 v193, v193
	v_mul_f32_e32 v178, v175, v178
	v_mul_f32_e32 v179, v175, v179
	v_mul_f32_e32 v180, v175, v180
	v_mul_f32_e32 v181, v175, v181
	v_mul_f32_e32 v182, v175, v182
	v_mul_f32_e32 v183, v175, v183
	v_mul_f32_e32 v184, v175, v184
	v_mul_f32_e32 v185, v175, v185
	v_exp_f32_e32 v96, v178
	v_exp_f32_e32 v97, v179
	v_exp_f32_e32 v98, v180
	v_exp_f32_e32 v99, v181
	v_exp_f32_e32 v100, v182
	v_exp_f32_e32 v101, v183
	v_exp_f32_e32 v102, v184
	v_exp_f32_e32 v103, v185
	s_nop 0
	v_fma_f32 v194, -v96, v96, 1.0
	v_fma_f32 v195, -v97, v97, 1.0
	v_fma_f32 v196, -v98, v98, 1.0
	v_fma_f32 v197, -v99, v99, 1.0
	v_fma_f32 v198, -v100, v100, 1.0
	v_fma_f32 v199, -v101, v101, 1.0
	v_fma_f32 v200, -v102, v102, 1.0
	v_fma_f32 v201, -v103, v103, 1.0
	v_max_f32_e32 v194, 0, v194
	v_max_f32_e32 v195, 0, v195
	v_max_f32_e32 v196, 0, v196
	v_max_f32_e32 v197, 0, v197
	v_max_f32_e32 v198, 0, v198
	v_max_f32_e32 v199, 0, v199
	v_max_f32_e32 v200, 0, v200
	v_max_f32_e32 v201, 0, v201
	v_sqrt_f32_e32 v194, v194
	v_sqrt_f32_e32 v195, v195
	v_sqrt_f32_e32 v196, v196
	v_sqrt_f32_e32 v197, v197
	v_sqrt_f32_e32 v198, v198
	v_sqrt_f32_e32 v199, v199
	v_sqrt_f32_e32 v200, v200
	v_sqrt_f32_e32 v201, v201
	s_waitcnt lgkmcnt(8)
	v_lshlrev_b32_e32 v144, 16, v144
	v_lshlrev_b32_e32 v145, 16, v145
	v_lshlrev_b32_e32 v146, 16, v146
	v_lshlrev_b32_e32 v147, 16, v147
	v_lshlrev_b32_e32 v148, 16, v148
	v_lshlrev_b32_e32 v149, 16, v149
	v_lshlrev_b32_e32 v150, 16, v150
	v_lshlrev_b32_e32 v151, 16, v151
	v_mul_f32_e32 v194, v194, v186
	v_mul_f32_e32 v195, v195, v187
	v_mul_f32_e32 v196, v196, v188
	v_mul_f32_e32 v197, v197, v189
	v_mul_f32_e32 v198, v198, v190
	v_mul_f32_e32 v199, v199, v191
	v_mul_f32_e32 v200, v200, v192
	v_mul_f32_e32 v201, v201, v193
	v_mul_f32_e32 v144, v194, v144
	v_mul_f32_e32 v145, v195, v145
	v_mul_f32_e32 v146, v196, v146
	v_mul_f32_e32 v147, v197, v147
	v_mul_f32_e32 v148, v198, v148
	v_mul_f32_e32 v149, v199, v149
	v_mul_f32_e32 v150, v200, v150
	v_mul_f32_e32 v151, v201, v151
	v_fma_f32 v178, v80, s53, v173
	v_fma_f32 v179, v81, s53, v173
	v_fma_f32 v180, v82, s53, v173
	v_fma_f32 v181, v83, s53, v173
	v_fma_f32 v182, v88, s53, v173
	v_fma_f32 v183, v89, s53, v173
	v_fma_f32 v184, v90, s53, v173
	v_fma_f32 v185, v91, s53, v173
	v_fma_f32 v186, v84, s53, v174
	v_fma_f32 v187, v85, s53, v174
	v_fma_f32 v188, v86, s53, v174
	v_fma_f32 v189, v87, s53, v174
	v_fma_f32 v190, v92, s53, v174
	v_fma_f32 v191, v93, s53, v174
	v_fma_f32 v192, v94, s53, v174
	v_fma_f32 v193, v95, s53, v174
	v_exp_f32_e32 v178, v178
	v_exp_f32_e32 v179, v179
	v_exp_f32_e32 v180, v180
	v_exp_f32_e32 v181, v181
	v_exp_f32_e32 v182, v182
	v_exp_f32_e32 v183, v183
	v_exp_f32_e32 v184, v184
	v_exp_f32_e32 v185, v185
	v_exp_f32_e32 v186, v186
	v_exp_f32_e32 v187, v187
	v_exp_f32_e32 v188, v188
	v_exp_f32_e32 v189, v189
	v_exp_f32_e32 v190, v190
	v_exp_f32_e32 v191, v191
	v_exp_f32_e32 v192, v192
	v_exp_f32_e32 v193, v193
	v_add_f32_e32 v178, 1.0, v178
	v_add_f32_e32 v179, 1.0, v179
	v_add_f32_e32 v180, 1.0, v180
	v_add_f32_e32 v181, 1.0, v181
	v_add_f32_e32 v182, 1.0, v182
	v_add_f32_e32 v183, 1.0, v183
	v_add_f32_e32 v184, 1.0, v184
	v_add_f32_e32 v185, 1.0, v185
	v_add_f32_e32 v186, 1.0, v186
	v_add_f32_e32 v187, 1.0, v187
	v_add_f32_e32 v188, 1.0, v188
	v_add_f32_e32 v189, 1.0, v189
	v_add_f32_e32 v190, 1.0, v190
	v_add_f32_e32 v191, 1.0, v191
	v_add_f32_e32 v192, 1.0, v192
	v_add_f32_e32 v193, 1.0, v193
	v_rcp_f32_e32 v178, v178
	v_rcp_f32_e32 v179, v179
	v_rcp_f32_e32 v180, v180
	v_rcp_f32_e32 v181, v181
	v_rcp_f32_e32 v182, v182
	v_rcp_f32_e32 v183, v183
	v_rcp_f32_e32 v184, v184
	v_rcp_f32_e32 v185, v185
	v_rcp_f32_e32 v186, v186
	v_rcp_f32_e32 v187, v187
	v_rcp_f32_e32 v188, v188
	v_rcp_f32_e32 v189, v189
	v_rcp_f32_e32 v190, v190
	v_rcp_f32_e32 v191, v191
	v_rcp_f32_e32 v192, v192
	v_rcp_f32_e32 v193, v193
	v_mul_f32_e32 v178, v175, v178
	v_mul_f32_e32 v179, v175, v179
	v_mul_f32_e32 v180, v175, v180
	v_mul_f32_e32 v181, v175, v181
	v_mul_f32_e32 v182, v175, v182
	v_mul_f32_e32 v183, v175, v183
	v_mul_f32_e32 v184, v175, v184
	v_mul_f32_e32 v185, v175, v185
	v_exp_f32_e32 v104, v178
	v_exp_f32_e32 v105, v179
	v_exp_f32_e32 v106, v180
	v_exp_f32_e32 v107, v181
	v_exp_f32_e32 v108, v182
	v_exp_f32_e32 v109, v183
	v_exp_f32_e32 v110, v184
	v_exp_f32_e32 v111, v185
	s_nop 0
	v_fma_f32 v194, -v104, v104, 1.0
	v_fma_f32 v195, -v105, v105, 1.0
	v_fma_f32 v196, -v106, v106, 1.0
	v_fma_f32 v197, -v107, v107, 1.0
	v_fma_f32 v198, -v108, v108, 1.0
	v_fma_f32 v199, -v109, v109, 1.0
	v_fma_f32 v200, -v110, v110, 1.0
	v_fma_f32 v201, -v111, v111, 1.0
	v_max_f32_e32 v194, 0, v194
	v_max_f32_e32 v195, 0, v195
	v_max_f32_e32 v196, 0, v196
	v_max_f32_e32 v197, 0, v197
	v_max_f32_e32 v198, 0, v198
	v_max_f32_e32 v199, 0, v199
	v_max_f32_e32 v200, 0, v200
	v_max_f32_e32 v201, 0, v201
	v_sqrt_f32_e32 v194, v194
	v_sqrt_f32_e32 v195, v195
	v_sqrt_f32_e32 v196, v196
	v_sqrt_f32_e32 v197, v197
	v_sqrt_f32_e32 v198, v198
	v_sqrt_f32_e32 v199, v199
	v_sqrt_f32_e32 v200, v200
	v_sqrt_f32_e32 v201, v201
	s_waitcnt lgkmcnt(0)
	v_lshlrev_b32_e32 v152, 16, v152
	v_lshlrev_b32_e32 v153, 16, v153
	v_lshlrev_b32_e32 v154, 16, v154
	v_lshlrev_b32_e32 v155, 16, v155
	v_lshlrev_b32_e32 v156, 16, v156
	v_lshlrev_b32_e32 v157, 16, v157
	v_lshlrev_b32_e32 v158, 16, v158
	v_lshlrev_b32_e32 v159, 16, v159
	v_mul_f32_e32 v194, v194, v186
	v_mul_f32_e32 v195, v195, v187
	v_mul_f32_e32 v196, v196, v188
	v_mul_f32_e32 v197, v197, v189
	v_mul_f32_e32 v198, v198, v190
	v_mul_f32_e32 v199, v199, v191
	v_mul_f32_e32 v200, v200, v192
	v_mul_f32_e32 v201, v201, v193
	v_mul_f32_e32 v152, v194, v152
	v_mul_f32_e32 v153, v195, v153
	v_mul_f32_e32 v154, v196, v154
	v_mul_f32_e32 v155, v197, v155
	v_mul_f32_e32 v156, v198, v156
	v_mul_f32_e32 v157, v199, v157
	v_mul_f32_e32 v158, v200, v158
	v_mul_f32_e32 v159, v201, v159
	v_fma_f32 v145, v97, v144, v145
	v_fma_f32 v149, v101, v148, v149
	v_fma_f32 v153, v105, v152, v153
	v_fma_f32 v157, v109, v156, v157
	v_mul_f32_e32 v97, v97, v96
	v_mul_f32_e32 v101, v101, v100
	v_mul_f32_e32 v105, v105, v104
	v_mul_f32_e32 v109, v109, v108
	v_fma_f32 v146, v98, v145, v146
	v_fma_f32 v150, v102, v149, v150
	v_fma_f32 v154, v106, v153, v154
	v_fma_f32 v158, v110, v157, v158
	v_mul_f32_e32 v98, v98, v97
	v_mul_f32_e32 v102, v102, v101
	v_mul_f32_e32 v106, v106, v105
	v_mul_f32_e32 v110, v110, v109
	v_fma_f32 v147, v99, v146, v147
	v_fma_f32 v151, v103, v150, v151
	v_fma_f32 v155, v107, v154, v155
	v_fma_f32 v159, v111, v158, v159
	v_mul_f32_e32 v99, v99, v98
	v_mul_f32_e32 v103, v103, v102
	v_mul_f32_e32 v107, v107, v106
	v_mul_f32_e32 v111, v111, v110
	ds_bpermute_b32 v178, v204, v99
	ds_bpermute_b32 v182, v204, v147
	ds_bpermute_b32 v179, v204, v103
	ds_bpermute_b32 v183, v204, v151
	ds_bpermute_b32 v180, v204, v107
	ds_bpermute_b32 v184, v204, v155
	ds_bpermute_b32 v181, v204, v111
	ds_bpermute_b32 v185, v204, v159
	s_waitcnt lgkmcnt(0)
	v_fma_f32 v186, v182, v99, v147
	v_cndmask_b32_e64 v178, 1.0, v178, s[34:35]
	v_fma_f32 v187, v183, v103, v151
	v_cndmask_b32_e64 v179, 1.0, v179, s[34:35]
	v_fma_f32 v188, v184, v107, v155
	v_cndmask_b32_e64 v180, 1.0, v180, s[34:35]
	v_fma_f32 v189, v185, v111, v159
	v_cndmask_b32_e64 v181, 1.0, v181, s[34:35]
	v_cndmask_b32_e64 v223, v147, v186, s[34:35]
	v_mul_f32_e32 v219, v99, v178
	v_cndmask_b32_e64 v224, v151, v187, s[34:35]
	v_mul_f32_e32 v220, v103, v179
	v_cndmask_b32_e64 v225, v155, v188, s[34:35]
	v_mul_f32_e32 v221, v107, v180
	v_cndmask_b32_e64 v226, v159, v189, s[34:35]
	v_mul_f32_e32 v222, v111, v181
	ds_bpermute_b32 v178, v205, v219
	ds_bpermute_b32 v182, v205, v223
	ds_bpermute_b32 v179, v205, v220
	ds_bpermute_b32 v183, v205, v224
	ds_bpermute_b32 v180, v205, v221
	ds_bpermute_b32 v184, v205, v225
	ds_bpermute_b32 v181, v205, v222
	ds_bpermute_b32 v185, v205, v226
	s_waitcnt lgkmcnt(0)
	v_fma_f32 v186, v182, v219, v223
	v_cndmask_b32_e64 v178, 1.0, v178, s[36:37]
	v_fma_f32 v187, v183, v220, v224
	v_cndmask_b32_e64 v179, 1.0, v179, s[36:37]
	v_fma_f32 v188, v184, v221, v225
	v_cndmask_b32_e64 v180, 1.0, v180, s[36:37]
	v_fma_f32 v189, v185, v222, v226
	v_cndmask_b32_e64 v181, 1.0, v181, s[36:37]
	v_cndmask_b32_e64 v223, v223, v186, s[36:37]
	v_mul_f32_e32 v219, v219, v178
	v_cndmask_b32_e64 v224, v224, v187, s[36:37]
	v_mul_f32_e32 v220, v220, v179
	v_cndmask_b32_e64 v225, v225, v188, s[36:37]
	v_mul_f32_e32 v221, v221, v180
	v_cndmask_b32_e64 v226, v226, v189, s[36:37]
	v_mul_f32_e32 v222, v222, v181
	ds_bpermute_b32 v227, v204, v219
	ds_bpermute_b32 v231, v204, v223
	ds_bpermute_b32 v235, v206, v219
	ds_bpermute_b32 v239, v206, v223
	ds_bpermute_b32 v228, v204, v220
	ds_bpermute_b32 v232, v204, v224
	ds_bpermute_b32 v236, v206, v220
	ds_bpermute_b32 v244, v206, v224
	ds_bpermute_b32 v229, v204, v221
	ds_bpermute_b32 v233, v204, v225
	ds_bpermute_b32 v237, v206, v221
	ds_bpermute_b32 v245, v206, v225
	ds_bpermute_b32 v230, v204, v222
	ds_bpermute_b32 v234, v204, v226
	ds_bpermute_b32 v238, v206, v222
	ds_bpermute_b32 v246, v206, v226
	s_waitcnt lgkmcnt(0)
	v_cndmask_b32_e64 v227, 1.0, v227, s[34:35]
	v_cndmask_b32_e64 v231, 0, v231, s[34:35]
	v_cndmask_b32_e64 v228, 1.0, v228, s[34:35]
	v_cndmask_b32_e64 v232, 0, v232, s[34:35]
	v_cndmask_b32_e64 v229, 1.0, v229, s[34:35]
	v_cndmask_b32_e64 v233, 0, v233, s[34:35]
	v_cndmask_b32_e64 v230, 1.0, v230, s[34:35]
	v_cndmask_b32_e64 v234, 0, v234, s[34:35]
	v_mov_b32_e32 v190, v235
	v_mov_b32_e32 v194, v239
	v_mov_b32_e32 v198, v190
	v_mov_b32_e32 v201, v194
	v_fma_f32 v194, v194, v236, v244
	v_mul_f32_e32 v190, v190, v236
	v_mov_b32_e32 v199, v190
	v_mov_b32_e32 v177, v194
	v_fma_f32 v194, v194, v237, v245
	v_mul_f32_e32 v190, v190, v237
	v_mov_b32_e32 v200, v190
	v_mov_b32_e32 v203, v194
	v_fma_f32 v194, v194, v238, v246
	v_mul_f32_e32 v190, v190, v238
	v_mov_b32_e32 v191, v194
	ds_write_b64 v207, v[190:191]
	s_waitcnt lgkmcnt(0)
	s_barrier
	ds_read_b64 v[178:179], v208
	ds_read_b64 v[180:181], v208 offset:512
	s_waitcnt lgkmcnt(0)
	v_fma_f32 v182, v176, v178, v179
	v_cndmask_b32_e64 v183, v176, v182, s[38:39]
	v_fma_f32 v176, v182, v180, v181
	s_add_i32 s13, s13, 1
	s_waitcnt vmcnt(0)
	s_barrier
	s_cmp_eq_u32 s13, 17
	s_cbranch_scc1 .Lmylru_nodma_2
	s_add_i32 s58, s13, 1
	s_cmp_lt_u32 s58, 2
	s_lshl_b32 s50, s58, 7
	s_lshl_b32 s51, s9, 8
	s_add_i32 s51, s51, 0x8000
	s_add_i32 s51, s51, s50
	s_lshl_b32 s59, s9, 11
	s_add_i32 s59, s59, s50
	s_addk_i32 s59, 0xff00
	s_cmp_lt_u32 s58, 2
	s_cselect_b32 s59, s51, s59
	s_lshl_b32 s52, s59, 11
	s_add_u32 s46, s16, s52
	s_addc_u32 s47, s17, 0
	s_lshl_b32 s52, s6, 13
	s_mov_b32 m0, s52
	s_add_i32 s52, s52, 0x400
	global_load_lds_dwordx4 v211, s[46:47]
	s_mov_b32 m0, s52
	s_add_i32 s52, s52, 0x400
	global_load_lds_dwordx4 v212, s[46:47]
	s_mov_b32 m0, s52
	s_add_i32 s52, s52, 0x400
	global_load_lds_dwordx4 v213, s[46:47]
	s_mov_b32 m0, s52
	s_add_i32 s52, s52, 0x400
	global_load_lds_dwordx4 v214, s[46:47]
	s_mov_b32 m0, s52
	s_add_i32 s52, s52, 0x400
	global_load_lds_dwordx4 v215, s[46:47]
	s_mov_b32 m0, s52
	s_add_i32 s52, s52, 0x400
	global_load_lds_dwordx4 v216, s[46:47]
	s_mov_b32 m0, s52
	s_add_i32 s52, s52, 0x400
	global_load_lds_dwordx4 v217, s[46:47]
	s_mov_b32 m0, s52
	s_nop 0
	global_load_lds_dwordx4 v218, s[46:47]
.Lmylru_nodma_2:
	v_or_b32_e32 v163, 0x10000, v162
	ds_read_b128 v[96:99], v163
	ds_read_b128 v[100:103], v163 offset:8192
	ds_read_b128 v[104:107], v163 offset:16384
	ds_read_b128 v[108:111], v163 offset:24576
	v_xor_b32_e32 v164, 0x40, v163
	ds_read_b128 v[112:115], v164
	ds_read_b128 v[116:119], v164 offset:8192
	ds_read_b128 v[120:123], v164 offset:16384
	ds_read_b128 v[124:127], v164 offset:24576
	s_waitcnt lgkmcnt(7)
	v_mfma_f32_16x16x32_bf16 v[64:67], v[96:99], v[0:3], 0
	v_mfma_f32_16x16x32_bf16 v[68:71], v[96:99], v[32:35], 0
	v_xor_b32_e32 v164, 0x80, v163
	ds_read_b128 v[96:99], v164
	s_waitcnt lgkmcnt(7)
	v_mfma_f32_16x16x32_bf16 v[72:75], v[100:103], v[0:3], 0
	v_mfma_f32_16x16x32_bf16 v[76:79], v[100:103], v[32:35], 0
	ds_read_b128 v[100:103], v164 offset:8192
	s_waitcnt lgkmcnt(7)
	v_mfma_f32_16x16x32_bf16 v[80:83], v[104:107], v[0:3], 0
	v_mfma_f32_16x16x32_bf16 v[84:87], v[104:107], v[32:35], 0
	ds_read_b128 v[104:107], v164 offset:16384
	s_waitcnt lgkmcnt(7)
	v_mfma_f32_16x16x32_bf16 v[88:91], v[108:111], v[0:3], 0
	v_mfma_f32_16x16x32_bf16 v[92:95], v[108:111], v[32:35], 0
	ds_read_b128 v[108:111], v164 offset:24576
	s_waitcnt lgkmcnt(7)
	v_mfma_f32_16x16x32_bf16 v[64:67], v[112:115], v[4:7], v[64:67]
	v_mfma_f32_16x16x32_bf16 v[68:71], v[112:115], v[36:39], v[68:71]
	v_xor_b32_e32 v164, 0xc0, v163
	ds_read_b128 v[112:115], v164
	s_waitcnt lgkmcnt(7)
	v_mfma_f32_16x16x32_bf16 v[72:75], v[116:119], v[4:7], v[72:75]
	v_mfma_f32_16x16x32_bf16 v[76:79], v[116:119], v[36:39], v[76:79]
	ds_read_b128 v[116:119], v164 offset:8192
	s_waitcnt lgkmcnt(7)
	v_mfma_f32_16x16x32_bf16 v[80:83], v[120:123], v[4:7], v[80:83]
	v_mfma_f32_16x16x32_bf16 v[84:87], v[120:123], v[36:39], v[84:87]
	ds_read_b128 v[120:123], v164 offset:16384
	s_waitcnt lgkmcnt(7)
	v_mfma_f32_16x16x32_bf16 v[88:91], v[124:127], v[4:7], v[88:91]
	v_mfma_f32_16x16x32_bf16 v[92:95], v[124:127], v[36:39], v[92:95]
	ds_read_b128 v[124:127], v164 offset:24576
	s_waitcnt lgkmcnt(7)
	v_mfma_f32_16x16x32_bf16 v[64:67], v[96:99], v[8:11], v[64:67]
	v_mfma_f32_16x16x32_bf16 v[68:71], v[96:99], v[40:43], v[68:71]
	v_xor_b32_e32 v164, 0x100, v163
	ds_read_b128 v[96:99], v164
	s_waitcnt lgkmcnt(7)
	v_mfma_f32_16x16x32_bf16 v[72:75], v[100:103], v[8:11], v[72:75]
	v_mfma_f32_16x16x32_bf16 v[76:79], v[100:103], v[40:43], v[76:79]
	ds_read_b128 v[100:103], v164 offset:8192
	s_waitcnt lgkmcnt(7)
	v_mfma_f32_16x16x32_bf16 v[80:83], v[104:107], v[8:11], v[80:83]
	v_mfma_f32_16x16x32_bf16 v[84:87], v[104:107], v[40:43], v[84:87]
	ds_read_b128 v[104:107], v164 offset:16384
	s_waitcnt lgkmcnt(7)
	v_mfma_f32_16x16x32_bf16 v[88:91], v[108:111], v[8:11], v[88:91]
	v_mfma_f32_16x16x32_bf16 v[92:95], v[108:111], v[40:43], v[92:95]
	ds_read_b128 v[108:111], v164 offset:24576
	s_waitcnt lgkmcnt(7)
	v_mfma_f32_16x16x32_bf16 v[64:67], v[112:115], v[12:15], v[64:67]
	v_mfma_f32_16x16x32_bf16 v[68:71], v[112:115], v[44:47], v[68:71]
	v_xor_b32_e32 v164, 0x140, v163
	ds_read_b128 v[112:115], v164
	s_waitcnt lgkmcnt(7)
	v_mfma_f32_16x16x32_bf16 v[72:75], v[116:119], v[12:15], v[72:75]
	v_mfma_f32_16x16x32_bf16 v[76:79], v[116:119], v[44:47], v[76:79]
	ds_read_b128 v[116:119], v164 offset:8192
	s_waitcnt lgkmcnt(7)
	v_mfma_f32_16x16x32_bf16 v[80:83], v[120:123], v[12:15], v[80:83]
	v_mfma_f32_16x16x32_bf16 v[84:87], v[120:123], v[44:47], v[84:87]
	ds_read_b128 v[120:123], v164 offset:16384
	s_waitcnt lgkmcnt(7)
	v_mfma_f32_16x16x32_bf16 v[88:91], v[124:127], v[12:15], v[88:91]
	v_mfma_f32_16x16x32_bf16 v[92:95], v[124:127], v[44:47], v[92:95]
	ds_read_b128 v[124:127], v164 offset:24576
	s_waitcnt lgkmcnt(7)
	v_mfma_f32_16x16x32_bf16 v[64:67], v[96:99], v[16:19], v[64:67]
	v_mfma_f32_16x16x32_bf16 v[68:71], v[96:99], v[48:51], v[68:71]
	v_xor_b32_e32 v164, 0x180, v163
	ds_read_b128 v[96:99], v164
	s_waitcnt lgkmcnt(7)
	v_mfma_f32_16x16x32_bf16 v[72:75], v[100:103], v[16:19], v[72:75]
	v_mfma_f32_16x16x32_bf16 v[76:79], v[100:103], v[48:51], v[76:79]
	ds_read_b128 v[100:103], v164 offset:8192
	s_waitcnt lgkmcnt(7)
	v_mfma_f32_16x16x32_bf16 v[80:83], v[104:107], v[16:19], v[80:83]
	v_mfma_f32_16x16x32_bf16 v[84:87], v[104:107], v[48:51], v[84:87]
	ds_read_b128 v[104:107], v164 offset:16384
	s_waitcnt lgkmcnt(7)
	v_mfma_f32_16x16x32_bf16 v[88:91], v[108:111], v[16:19], v[88:91]
	v_mfma_f32_16x16x32_bf16 v[92:95], v[108:111], v[48:51], v[92:95]
	ds_read_b128 v[108:111], v164 offset:24576
	s_waitcnt lgkmcnt(7)
	v_mfma_f32_16x16x32_bf16 v[64:67], v[112:115], v[20:23], v[64:67]
	v_mfma_f32_16x16x32_bf16 v[68:71], v[112:115], v[52:55], v[68:71]
	v_xor_b32_e32 v164, 0x1c0, v163
	ds_read_b128 v[112:115], v164
	s_waitcnt lgkmcnt(7)
	v_mfma_f32_16x16x32_bf16 v[72:75], v[116:119], v[20:23], v[72:75]
	v_mfma_f32_16x16x32_bf16 v[76:79], v[116:119], v[52:55], v[76:79]
	ds_read_b128 v[116:119], v164 offset:8192
	s_waitcnt lgkmcnt(7)
	v_mfma_f32_16x16x32_bf16 v[80:83], v[120:123], v[20:23], v[80:83]
	v_mfma_f32_16x16x32_bf16 v[84:87], v[120:123], v[52:55], v[84:87]
	ds_read_b128 v[120:123], v164 offset:16384
	s_waitcnt lgkmcnt(7)
	v_mfma_f32_16x16x32_bf16 v[88:91], v[124:127], v[20:23], v[88:91]
	v_mfma_f32_16x16x32_bf16 v[92:95], v[124:127], v[52:55], v[92:95]
	ds_read_b128 v[124:127], v164 offset:24576
	s_waitcnt lgkmcnt(7)
	v_mfma_f32_16x16x32_bf16 v[64:67], v[96:99], v[24:27], v[64:67]
	v_mfma_f32_16x16x32_bf16 v[68:71], v[96:99], v[56:59], v[68:71]
	s_waitcnt lgkmcnt(6)
	v_mfma_f32_16x16x32_bf16 v[72:75], v[100:103], v[24:27], v[72:75]
	v_mfma_f32_16x16x32_bf16 v[76:79], v[100:103], v[56:59], v[76:79]
	s_waitcnt lgkmcnt(5)
	v_mfma_f32_16x16x32_bf16 v[80:83], v[104:107], v[24:27], v[80:83]
	v_mfma_f32_16x16x32_bf16 v[84:87], v[104:107], v[56:59], v[84:87]
	s_waitcnt lgkmcnt(4)
	v_mfma_f32_16x16x32_bf16 v[88:91], v[108:111], v[24:27], v[88:91]
	v_mfma_f32_16x16x32_bf16 v[92:95], v[108:111], v[56:59], v[92:95]
	s_waitcnt lgkmcnt(3)
	v_mfma_f32_16x16x32_bf16 v[64:67], v[112:115], v[28:31], v[64:67]
	v_mfma_f32_16x16x32_bf16 v[68:71], v[112:115], v[60:63], v[68:71]
	s_waitcnt lgkmcnt(2)
	v_mfma_f32_16x16x32_bf16 v[72:75], v[116:119], v[28:31], v[72:75]
	v_mfma_f32_16x16x32_bf16 v[76:79], v[116:119], v[60:63], v[76:79]
	s_waitcnt lgkmcnt(1)
	v_mfma_f32_16x16x32_bf16 v[80:83], v[120:123], v[28:31], v[80:83]
	v_mfma_f32_16x16x32_bf16 v[84:87], v[120:123], v[60:63], v[84:87]
	s_waitcnt lgkmcnt(0)
	v_mfma_f32_16x16x32_bf16 v[88:91], v[124:127], v[28:31], v[88:91]
	v_mfma_f32_16x16x32_bf16 v[92:95], v[124:127], v[60:63], v[92:95]
	v_or_b32_e32 v198, 0x10000, v165
	v_or_b32_e32 v199, 0x10000, v166
	v_or_b32_e32 v200, 0x10000, v167
	v_or_b32_e32 v201, 0x10000, v168
	ds_read_u16 v144, v198
	ds_read_u16 v145, v199
	ds_read_u16 v146, v200
	ds_read_u16 v147, v201
	ds_read_u16 v148, v198 offset:8192
	ds_read_u16 v149, v199 offset:8192
	ds_read_u16 v150, v200 offset:8192
	ds_read_u16 v151, v201 offset:8192
	ds_read_u16 v152, v198 offset:16384
	ds_read_u16 v153, v199 offset:16384
	ds_read_u16 v154, v200 offset:16384
	ds_read_u16 v155, v201 offset:16384
	ds_read_u16 v156, v198 offset:24576
	ds_read_u16 v157, v199 offset:24576
	ds_read_u16 v158, v200 offset:24576
	ds_read_u16 v159, v201 offset:24576
	s_nop 7
	v_fma_f32 v178, v64, s53, v173
	v_fma_f32 v179, v65, s53, v173
	v_fma_f32 v180, v66, s53, v173
	v_fma_f32 v181, v67, s53, v173
	v_fma_f32 v182, v72, s53, v173
	v_fma_f32 v183, v73, s53, v173
	v_fma_f32 v184, v74, s53, v173
	v_fma_f32 v185, v75, s53, v173
	v_fma_f32 v186, v68, s53, v174
	v_fma_f32 v187, v69, s53, v174
	v_fma_f32 v188, v70, s53, v174
	v_fma_f32 v189, v71, s53, v174
	v_fma_f32 v190, v76, s53, v174
	v_fma_f32 v191, v77, s53, v174
	v_fma_f32 v192, v78, s53, v174
	v_fma_f32 v193, v79, s53, v174
	v_exp_f32_e32 v178, v178
	v_exp_f32_e32 v179, v179
	v_exp_f32_e32 v180, v180
	v_exp_f32_e32 v181, v181
	v_exp_f32_e32 v182, v182
	v_exp_f32_e32 v183, v183
	v_exp_f32_e32 v184, v184
	v_exp_f32_e32 v185, v185
	v_exp_f32_e32 v186, v186
	v_exp_f32_e32 v187, v187
	v_exp_f32_e32 v188, v188
	v_exp_f32_e32 v189, v189
	v_exp_f32_e32 v190, v190
	v_exp_f32_e32 v191, v191
	v_exp_f32_e32 v192, v192
	v_exp_f32_e32 v193, v193
	v_add_f32_e32 v178, 1.0, v178
	v_add_f32_e32 v179, 1.0, v179
	v_add_f32_e32 v180, 1.0, v180
	v_add_f32_e32 v181, 1.0, v181
	v_add_f32_e32 v182, 1.0, v182
	v_add_f32_e32 v183, 1.0, v183
	v_add_f32_e32 v184, 1.0, v184
	v_add_f32_e32 v185, 1.0, v185
	v_add_f32_e32 v186, 1.0, v186
	v_add_f32_e32 v187, 1.0, v187
	v_add_f32_e32 v188, 1.0, v188
	v_add_f32_e32 v189, 1.0, v189
	v_add_f32_e32 v190, 1.0, v190
	v_add_f32_e32 v191, 1.0, v191
	v_add_f32_e32 v192, 1.0, v192
	v_add_f32_e32 v193, 1.0, v193
	v_rcp_f32_e32 v178, v178
	v_rcp_f32_e32 v179, v179
	v_rcp_f32_e32 v180, v180
	v_rcp_f32_e32 v181, v181
	v_rcp_f32_e32 v182, v182
	v_rcp_f32_e32 v183, v183
	v_rcp_f32_e32 v184, v184
	v_rcp_f32_e32 v185, v185
	v_rcp_f32_e32 v186, v186
	v_rcp_f32_e32 v187, v187
	v_rcp_f32_e32 v188, v188
	v_rcp_f32_e32 v189, v189
	v_rcp_f32_e32 v190, v190
	v_rcp_f32_e32 v191, v191
	v_rcp_f32_e32 v192, v192
	v_rcp_f32_e32 v193, v193
	v_mul_f32_e32 v178, v175, v178
	v_mul_f32_e32 v179, v175, v179
	v_mul_f32_e32 v180, v175, v180
	v_mul_f32_e32 v181, v175, v181
	v_mul_f32_e32 v182, v175, v182
	v_mul_f32_e32 v183, v175, v183
	v_mul_f32_e32 v184, v175, v184
	v_mul_f32_e32 v185, v175, v185
	v_exp_f32_e32 v96, v178
	v_exp_f32_e32 v97, v179
	v_exp_f32_e32 v98, v180
	v_exp_f32_e32 v99, v181
	v_exp_f32_e32 v100, v182
	v_exp_f32_e32 v101, v183
	v_exp_f32_e32 v102, v184
	v_exp_f32_e32 v103, v185
	s_nop 0
	v_fma_f32 v194, -v96, v96, 1.0
	v_fma_f32 v195, -v97, v97, 1.0
	v_fma_f32 v196, -v98, v98, 1.0
	v_fma_f32 v197, -v99, v99, 1.0
	v_fma_f32 v198, -v100, v100, 1.0
	v_fma_f32 v199, -v101, v101, 1.0
	v_fma_f32 v200, -v102, v102, 1.0
	v_fma_f32 v201, -v103, v103, 1.0
	v_max_f32_e32 v194, 0, v194
	v_max_f32_e32 v195, 0, v195
	v_max_f32_e32 v196, 0, v196
	v_max_f32_e32 v197, 0, v197
	v_max_f32_e32 v198, 0, v198
	v_max_f32_e32 v199, 0, v199
	v_max_f32_e32 v200, 0, v200
	v_max_f32_e32 v201, 0, v201
	v_sqrt_f32_e32 v194, v194
	v_sqrt_f32_e32 v195, v195
	v_sqrt_f32_e32 v196, v196
	v_sqrt_f32_e32 v197, v197
	v_sqrt_f32_e32 v198, v198
	v_sqrt_f32_e32 v199, v199
	v_sqrt_f32_e32 v200, v200
	v_sqrt_f32_e32 v201, v201
	s_waitcnt lgkmcnt(8)
	v_lshlrev_b32_e32 v144, 16, v144
	v_lshlrev_b32_e32 v145, 16, v145
	v_lshlrev_b32_e32 v146, 16, v146
	v_lshlrev_b32_e32 v147, 16, v147
	v_lshlrev_b32_e32 v148, 16, v148
	v_lshlrev_b32_e32 v149, 16, v149
	v_lshlrev_b32_e32 v150, 16, v150
	v_lshlrev_b32_e32 v151, 16, v151
	v_mul_f32_e32 v194, v194, v186
	v_mul_f32_e32 v195, v195, v187
	v_mul_f32_e32 v196, v196, v188
	v_mul_f32_e32 v197, v197, v189
	v_mul_f32_e32 v198, v198, v190
	v_mul_f32_e32 v199, v199, v191
	v_mul_f32_e32 v200, v200, v192
	v_mul_f32_e32 v201, v201, v193
	v_mul_f32_e32 v144, v194, v144
	v_mul_f32_e32 v145, v195, v145
	v_mul_f32_e32 v146, v196, v146
	v_mul_f32_e32 v147, v197, v147
	v_mul_f32_e32 v148, v198, v148
	v_mul_f32_e32 v149, v199, v149
	v_mul_f32_e32 v150, v200, v150
	v_mul_f32_e32 v151, v201, v151
	v_fma_f32 v178, v80, s53, v173
	v_fma_f32 v179, v81, s53, v173
	v_fma_f32 v180, v82, s53, v173
	v_fma_f32 v181, v83, s53, v173
	v_fma_f32 v182, v88, s53, v173
	v_fma_f32 v183, v89, s53, v173
	v_fma_f32 v184, v90, s53, v173
	v_fma_f32 v185, v91, s53, v173
	v_fma_f32 v186, v84, s53, v174
	v_fma_f32 v187, v85, s53, v174
	v_fma_f32 v188, v86, s53, v174
	v_fma_f32 v189, v87, s53, v174
	v_fma_f32 v190, v92, s53, v174
	v_fma_f32 v191, v93, s53, v174
	v_fma_f32 v192, v94, s53, v174
	v_fma_f32 v193, v95, s53, v174
	v_exp_f32_e32 v178, v178
	v_exp_f32_e32 v179, v179
	v_exp_f32_e32 v180, v180
	v_exp_f32_e32 v181, v181
	v_exp_f32_e32 v182, v182
	v_exp_f32_e32 v183, v183
	v_exp_f32_e32 v184, v184
	v_exp_f32_e32 v185, v185
	v_exp_f32_e32 v186, v186
	v_exp_f32_e32 v187, v187
	v_exp_f32_e32 v188, v188
	v_exp_f32_e32 v189, v189
	v_exp_f32_e32 v190, v190
	v_exp_f32_e32 v191, v191
	v_exp_f32_e32 v192, v192
	v_exp_f32_e32 v193, v193
	v_add_f32_e32 v178, 1.0, v178
	v_add_f32_e32 v179, 1.0, v179
	v_add_f32_e32 v180, 1.0, v180
	v_add_f32_e32 v181, 1.0, v181
	v_add_f32_e32 v182, 1.0, v182
	v_add_f32_e32 v183, 1.0, v183
	v_add_f32_e32 v184, 1.0, v184
	v_add_f32_e32 v185, 1.0, v185
	v_add_f32_e32 v186, 1.0, v186
	v_add_f32_e32 v187, 1.0, v187
	v_add_f32_e32 v188, 1.0, v188
	v_add_f32_e32 v189, 1.0, v189
	v_add_f32_e32 v190, 1.0, v190
	v_add_f32_e32 v191, 1.0, v191
	v_add_f32_e32 v192, 1.0, v192
	v_add_f32_e32 v193, 1.0, v193
	v_rcp_f32_e32 v178, v178
	v_rcp_f32_e32 v179, v179
	v_rcp_f32_e32 v180, v180
	v_rcp_f32_e32 v181, v181
	v_rcp_f32_e32 v182, v182
	v_rcp_f32_e32 v183, v183
	v_rcp_f32_e32 v184, v184
	v_rcp_f32_e32 v185, v185
	v_rcp_f32_e32 v186, v186
	v_rcp_f32_e32 v187, v187
	v_rcp_f32_e32 v188, v188
	v_rcp_f32_e32 v189, v189
	v_rcp_f32_e32 v190, v190
	v_rcp_f32_e32 v191, v191
	v_rcp_f32_e32 v192, v192
	v_rcp_f32_e32 v193, v193
	v_mul_f32_e32 v178, v175, v178
	v_mul_f32_e32 v179, v175, v179
	v_mul_f32_e32 v180, v175, v180
	v_mul_f32_e32 v181, v175, v181
	v_mul_f32_e32 v182, v175, v182
	v_mul_f32_e32 v183, v175, v183
	v_mul_f32_e32 v184, v175, v184
	v_mul_f32_e32 v185, v175, v185
	v_exp_f32_e32 v104, v178
	v_exp_f32_e32 v105, v179
	v_exp_f32_e32 v106, v180
	v_exp_f32_e32 v107, v181
	v_exp_f32_e32 v108, v182
	v_exp_f32_e32 v109, v183
	v_exp_f32_e32 v110, v184
	v_exp_f32_e32 v111, v185
	s_nop 0
	v_fma_f32 v194, -v104, v104, 1.0
	v_fma_f32 v195, -v105, v105, 1.0
	v_fma_f32 v196, -v106, v106, 1.0
	v_fma_f32 v197, -v107, v107, 1.0
	v_fma_f32 v198, -v108, v108, 1.0
	v_fma_f32 v199, -v109, v109, 1.0
	v_fma_f32 v200, -v110, v110, 1.0
	v_fma_f32 v201, -v111, v111, 1.0
	v_max_f32_e32 v194, 0, v194
	v_max_f32_e32 v195, 0, v195
	v_max_f32_e32 v196, 0, v196
	v_max_f32_e32 v197, 0, v197
	v_max_f32_e32 v198, 0, v198
	v_max_f32_e32 v199, 0, v199
	v_max_f32_e32 v200, 0, v200
	v_max_f32_e32 v201, 0, v201
	v_sqrt_f32_e32 v194, v194
	v_sqrt_f32_e32 v195, v195
	v_sqrt_f32_e32 v196, v196
	v_sqrt_f32_e32 v197, v197
	v_sqrt_f32_e32 v198, v198
	v_sqrt_f32_e32 v199, v199
	v_sqrt_f32_e32 v200, v200
	v_sqrt_f32_e32 v201, v201
	s_waitcnt lgkmcnt(0)
	v_lshlrev_b32_e32 v152, 16, v152
	v_lshlrev_b32_e32 v153, 16, v153
	v_lshlrev_b32_e32 v154, 16, v154
	v_lshlrev_b32_e32 v155, 16, v155
	v_lshlrev_b32_e32 v156, 16, v156
	v_lshlrev_b32_e32 v157, 16, v157
	v_lshlrev_b32_e32 v158, 16, v158
	v_lshlrev_b32_e32 v159, 16, v159
	v_mul_f32_e32 v194, v194, v186
	v_mul_f32_e32 v195, v195, v187
	v_mul_f32_e32 v196, v196, v188
	v_mul_f32_e32 v197, v197, v189
	v_mul_f32_e32 v198, v198, v190
	v_mul_f32_e32 v199, v199, v191
	v_mul_f32_e32 v200, v200, v192
	v_mul_f32_e32 v201, v201, v193
	v_mul_f32_e32 v152, v194, v152
	v_mul_f32_e32 v153, v195, v153
	v_mul_f32_e32 v154, v196, v154
	v_mul_f32_e32 v155, v197, v155
	v_mul_f32_e32 v156, v198, v156
	v_mul_f32_e32 v157, v199, v157
	v_mul_f32_e32 v158, v200, v158
	v_mul_f32_e32 v159, v201, v159
	v_fma_f32 v145, v97, v144, v145
	v_fma_f32 v149, v101, v148, v149
	v_fma_f32 v153, v105, v152, v153
	v_fma_f32 v157, v109, v156, v157
	v_mul_f32_e32 v97, v97, v96
	v_mul_f32_e32 v101, v101, v100
	v_mul_f32_e32 v105, v105, v104
	v_mul_f32_e32 v109, v109, v108
	v_fma_f32 v146, v98, v145, v146
	v_fma_f32 v150, v102, v149, v150
	v_fma_f32 v154, v106, v153, v154
	v_fma_f32 v158, v110, v157, v158
	v_mul_f32_e32 v98, v98, v97
	v_mul_f32_e32 v102, v102, v101
	v_mul_f32_e32 v106, v106, v105
	v_mul_f32_e32 v110, v110, v109
	v_fma_f32 v147, v99, v146, v147
	v_fma_f32 v151, v103, v150, v151
	v_fma_f32 v155, v107, v154, v155
	v_fma_f32 v159, v111, v158, v159
	v_mul_f32_e32 v99, v99, v98
	v_mul_f32_e32 v103, v103, v102
	v_mul_f32_e32 v107, v107, v106
	v_mul_f32_e32 v111, v111, v110
	ds_bpermute_b32 v178, v204, v99
	ds_bpermute_b32 v182, v204, v147
	ds_bpermute_b32 v179, v204, v103
	ds_bpermute_b32 v183, v204, v151
	ds_bpermute_b32 v180, v204, v107
	ds_bpermute_b32 v184, v204, v155
	ds_bpermute_b32 v181, v204, v111
	ds_bpermute_b32 v185, v204, v159
	s_waitcnt lgkmcnt(0)
	v_fma_f32 v186, v182, v99, v147
	v_cndmask_b32_e64 v178, 1.0, v178, s[34:35]
	v_fma_f32 v187, v183, v103, v151
	v_cndmask_b32_e64 v179, 1.0, v179, s[34:35]
	v_fma_f32 v188, v184, v107, v155
	v_cndmask_b32_e64 v180, 1.0, v180, s[34:35]
	v_fma_f32 v189, v185, v111, v159
	v_cndmask_b32_e64 v181, 1.0, v181, s[34:35]
	v_cndmask_b32_e64 v223, v147, v186, s[34:35]
	v_mul_f32_e32 v219, v99, v178
	v_cndmask_b32_e64 v224, v151, v187, s[34:35]
	v_mul_f32_e32 v220, v103, v179
	v_cndmask_b32_e64 v225, v155, v188, s[34:35]
	v_mul_f32_e32 v221, v107, v180
	v_cndmask_b32_e64 v226, v159, v189, s[34:35]
	v_mul_f32_e32 v222, v111, v181
	ds_bpermute_b32 v178, v205, v219
	ds_bpermute_b32 v182, v205, v223
	ds_bpermute_b32 v179, v205, v220
	ds_bpermute_b32 v183, v205, v224
	ds_bpermute_b32 v180, v205, v221
	ds_bpermute_b32 v184, v205, v225
	ds_bpermute_b32 v181, v205, v222
	ds_bpermute_b32 v185, v205, v226
	s_waitcnt lgkmcnt(0)
	v_fma_f32 v186, v182, v219, v223
	v_cndmask_b32_e64 v178, 1.0, v178, s[36:37]
	v_fma_f32 v187, v183, v220, v224
	v_cndmask_b32_e64 v179, 1.0, v179, s[36:37]
	v_fma_f32 v188, v184, v221, v225
	v_cndmask_b32_e64 v180, 1.0, v180, s[36:37]
	v_fma_f32 v189, v185, v222, v226
	v_cndmask_b32_e64 v181, 1.0, v181, s[36:37]
	v_cndmask_b32_e64 v223, v223, v186, s[36:37]
	v_mul_f32_e32 v219, v219, v178
	v_cndmask_b32_e64 v224, v224, v187, s[36:37]
	v_mul_f32_e32 v220, v220, v179
	v_cndmask_b32_e64 v225, v225, v188, s[36:37]
	v_mul_f32_e32 v221, v221, v180
	v_cndmask_b32_e64 v226, v226, v189, s[36:37]
	v_mul_f32_e32 v222, v222, v181
	ds_bpermute_b32 v227, v204, v219
	ds_bpermute_b32 v231, v204, v223
	ds_bpermute_b32 v235, v206, v219
	ds_bpermute_b32 v239, v206, v223
	ds_bpermute_b32 v228, v204, v220
	ds_bpermute_b32 v232, v204, v224
	ds_bpermute_b32 v236, v206, v220
	ds_bpermute_b32 v244, v206, v224
	ds_bpermute_b32 v229, v204, v221
	ds_bpermute_b32 v233, v204, v225
	ds_bpermute_b32 v237, v206, v221
	ds_bpermute_b32 v245, v206, v225
	ds_bpermute_b32 v230, v204, v222
	ds_bpermute_b32 v234, v204, v226
	ds_bpermute_b32 v238, v206, v222
	ds_bpermute_b32 v246, v206, v226
	s_waitcnt lgkmcnt(0)
	v_cndmask_b32_e64 v227, 1.0, v227, s[34:35]
	v_cndmask_b32_e64 v231, 0, v231, s[34:35]
	v_cndmask_b32_e64 v228, 1.0, v228, s[34:35]
	v_cndmask_b32_e64 v232, 0, v232, s[34:35]
	v_cndmask_b32_e64 v229, 1.0, v229, s[34:35]
	v_cndmask_b32_e64 v233, 0, v233, s[34:35]
	v_cndmask_b32_e64 v230, 1.0, v230, s[34:35]
	v_cndmask_b32_e64 v234, 0, v234, s[34:35]
	v_mov_b32_e32 v190, v235
	v_mov_b32_e32 v194, v239
	v_mov_b32_e32 v198, v190
	v_mov_b32_e32 v201, v194
	v_fma_f32 v194, v194, v236, v244
	v_mul_f32_e32 v190, v190, v236
	v_mov_b32_e32 v199, v190
	v_mov_b32_e32 v177, v194
	v_fma_f32 v194, v194, v237, v245
	v_mul_f32_e32 v190, v190, v237
	v_mov_b32_e32 v200, v190
	v_mov_b32_e32 v203, v194
	v_fma_f32 v194, v194, v238, v246
	v_mul_f32_e32 v190, v190, v238
	v_mov_b32_e32 v191, v194
	ds_write_b64 v207, v[190:191] offset:1024
	s_waitcnt lgkmcnt(0)
	s_barrier
	ds_read_b64 v[178:179], v208 offset:1024
	ds_read_b64 v[180:181], v208 offset:1536
	s_waitcnt lgkmcnt(0)
	v_fma_f32 v182, v176, v178, v179
	v_cndmask_b32_e64 v183, v176, v182, s[38:39]
	v_fma_f32 v176, v182, v180, v181
	s_add_i32 s13, s13, 1
	s_mov_b32 s60, 8

.Lmylru_nodma_3:
	v_mov_b32_e32 v163, v162
	ds_read_b128 v[96:99], v163
	ds_read_b128 v[100:103], v163 offset:8192
	ds_read_b128 v[104:107], v163 offset:16384
	ds_read_b128 v[108:111], v163 offset:24576
	v_xor_b32_e32 v164, 0x40, v163
	ds_read_b128 v[112:115], v164
	ds_read_b128 v[116:119], v164 offset:8192
	ds_read_b128 v[120:123], v164 offset:16384
	ds_read_b128 v[124:127], v164 offset:24576
	s_waitcnt lgkmcnt(7)
	v_mfma_f32_16x16x32_bf16 v[64:67], v[96:99], v[0:3], 0
	v_mfma_f32_16x16x32_bf16 v[68:71], v[96:99], v[32:35], 0
	v_xor_b32_e32 v164, 0x80, v163
	ds_read_b128 v[96:99], v164
	s_waitcnt lgkmcnt(7)
	v_mfma_f32_16x16x32_bf16 v[72:75], v[100:103], v[0:3], 0
	v_mfma_f32_16x16x32_bf16 v[76:79], v[100:103], v[32:35], 0
	ds_read_b128 v[100:103], v164 offset:8192
	s_waitcnt lgkmcnt(7)
	v_mfma_f32_16x16x32_bf16 v[80:83], v[104:107], v[0:3], 0
	v_mfma_f32_16x16x32_bf16 v[84:87], v[104:107], v[32:35], 0
	ds_read_b128 v[104:107], v164 offset:16384
	s_waitcnt lgkmcnt(7)
	v_mfma_f32_16x16x32_bf16 v[88:91], v[108:111], v[0:3], 0
	v_mfma_f32_16x16x32_bf16 v[92:95], v[108:111], v[32:35], 0
	ds_read_b128 v[108:111], v164 offset:24576
	s_waitcnt lgkmcnt(7)
	v_mfma_f32_16x16x32_bf16 v[64:67], v[112:115], v[4:7], v[64:67]
	v_mfma_f32_16x16x32_bf16 v[68:71], v[112:115], v[36:39], v[68:71]
	v_xor_b32_e32 v164, 0xc0, v163
	ds_read_b128 v[112:115], v164
	s_waitcnt lgkmcnt(7)
	v_mfma_f32_16x16x32_bf16 v[72:75], v[116:119], v[4:7], v[72:75]
	v_mfma_f32_16x16x32_bf16 v[76:79], v[116:119], v[36:39], v[76:79]
	ds_read_b128 v[116:119], v164 offset:8192
	s_waitcnt lgkmcnt(7)
	v_mfma_f32_16x16x32_bf16 v[80:83], v[120:123], v[4:7], v[80:83]
	v_mfma_f32_16x16x32_bf16 v[84:87], v[120:123], v[36:39], v[84:87]
	ds_read_b128 v[120:123], v164 offset:16384
	s_waitcnt lgkmcnt(7)
	v_mfma_f32_16x16x32_bf16 v[88:91], v[124:127], v[4:7], v[88:91]
	v_mfma_f32_16x16x32_bf16 v[92:95], v[124:127], v[36:39], v[92:95]
	ds_read_b128 v[124:127], v164 offset:24576
	s_waitcnt lgkmcnt(7)
	v_mfma_f32_16x16x32_bf16 v[64:67], v[96:99], v[8:11], v[64:67]
	v_mfma_f32_16x16x32_bf16 v[68:71], v[96:99], v[40:43], v[68:71]
	v_xor_b32_e32 v164, 0x100, v163
	ds_read_b128 v[96:99], v164
	s_waitcnt lgkmcnt(7)
	v_mfma_f32_16x16x32_bf16 v[72:75], v[100:103], v[8:11], v[72:75]
	v_mfma_f32_16x16x32_bf16 v[76:79], v[100:103], v[40:43], v[76:79]
	ds_read_b128 v[100:103], v164 offset:8192
	s_waitcnt lgkmcnt(7)
	v_mfma_f32_16x16x32_bf16 v[80:83], v[104:107], v[8:11], v[80:83]
	v_mfma_f32_16x16x32_bf16 v[84:87], v[104:107], v[40:43], v[84:87]
	ds_read_b128 v[104:107], v164 offset:16384
	s_waitcnt lgkmcnt(7)
	v_mfma_f32_16x16x32_bf16 v[88:91], v[108:111], v[8:11], v[88:91]
	v_mfma_f32_16x16x32_bf16 v[92:95], v[108:111], v[40:43], v[92:95]
	ds_read_b128 v[108:111], v164 offset:24576
	s_waitcnt lgkmcnt(7)
	v_mfma_f32_16x16x32_bf16 v[64:67], v[112:115], v[12:15], v[64:67]
	v_mfma_f32_16x16x32_bf16 v[68:71], v[112:115], v[44:47], v[68:71]
	v_xor_b32_e32 v164, 0x140, v163
	ds_read_b128 v[112:115], v164
	s_waitcnt lgkmcnt(7)
	v_mfma_f32_16x16x32_bf16 v[72:75], v[116:119], v[12:15], v[72:75]
	v_mfma_f32_16x16x32_bf16 v[76:79], v[116:119], v[44:47], v[76:79]
	ds_read_b128 v[116:119], v164 offset:8192
	s_waitcnt lgkmcnt(7)
	v_mfma_f32_16x16x32_bf16 v[80:83], v[120:123], v[12:15], v[80:83]
	v_mfma_f32_16x16x32_bf16 v[84:87], v[120:123], v[44:47], v[84:87]
	ds_read_b128 v[120:123], v164 offset:16384
	s_waitcnt lgkmcnt(7)
	v_mfma_f32_16x16x32_bf16 v[88:91], v[124:127], v[12:15], v[88:91]
	v_mfma_f32_16x16x32_bf16 v[92:95], v[124:127], v[44:47], v[92:95]
	ds_read_b128 v[124:127], v164 offset:24576
	s_waitcnt lgkmcnt(7)
	v_mfma_f32_16x16x32_bf16 v[64:67], v[96:99], v[16:19], v[64:67]
	v_mfma_f32_16x16x32_bf16 v[68:71], v[96:99], v[48:51], v[68:71]
	v_xor_b32_e32 v164, 0x180, v163
	ds_read_b128 v[96:99], v164
	s_waitcnt lgkmcnt(7)
	v_mfma_f32_16x16x32_bf16 v[72:75], v[100:103], v[16:19], v[72:75]
	v_mfma_f32_16x16x32_bf16 v[76:79], v[100:103], v[48:51], v[76:79]
	ds_read_b128 v[100:103], v164 offset:8192
	s_waitcnt lgkmcnt(7)
	v_mfma_f32_16x16x32_bf16 v[80:83], v[104:107], v[16:19], v[80:83]
	v_mfma_f32_16x16x32_bf16 v[84:87], v[104:107], v[48:51], v[84:87]
	ds_read_b128 v[104:107], v164 offset:16384
	s_waitcnt lgkmcnt(7)
	v_mfma_f32_16x16x32_bf16 v[88:91], v[108:111], v[16:19], v[88:91]
	v_mfma_f32_16x16x32_bf16 v[92:95], v[108:111], v[48:51], v[92:95]
	ds_read_b128 v[108:111], v164 offset:24576
	s_waitcnt lgkmcnt(7)
	v_mfma_f32_16x16x32_bf16 v[64:67], v[112:115], v[20:23], v[64:67]
	v_mfma_f32_16x16x32_bf16 v[68:71], v[112:115], v[52:55], v[68:71]
	v_xor_b32_e32 v164, 0x1c0, v163
	ds_read_b128 v[112:115], v164
	s_waitcnt lgkmcnt(7)
	v_mfma_f32_16x16x32_bf16 v[72:75], v[116:119], v[20:23], v[72:75]
	v_mfma_f32_16x16x32_bf16 v[76:79], v[116:119], v[52:55], v[76:79]
	ds_read_b128 v[116:119], v164 offset:8192
	s_waitcnt lgkmcnt(7)
	v_mfma_f32_16x16x32_bf16 v[80:83], v[120:123], v[20:23], v[80:83]
	v_mfma_f32_16x16x32_bf16 v[84:87], v[120:123], v[52:55], v[84:87]
	ds_read_b128 v[120:123], v164 offset:16384
	s_waitcnt lgkmcnt(7)
	v_mfma_f32_16x16x32_bf16 v[88:91], v[124:127], v[20:23], v[88:91]
	v_mfma_f32_16x16x32_bf16 v[92:95], v[124:127], v[52:55], v[92:95]
	ds_read_b128 v[124:127], v164 offset:24576
	s_waitcnt lgkmcnt(7)
	v_mfma_f32_16x16x32_bf16 v[64:67], v[96:99], v[24:27], v[64:67]
	v_mfma_f32_16x16x32_bf16 v[68:71], v[96:99], v[56:59], v[68:71]
	s_waitcnt lgkmcnt(6)
	v_mfma_f32_16x16x32_bf16 v[72:75], v[100:103], v[24:27], v[72:75]
	v_mfma_f32_16x16x32_bf16 v[76:79], v[100:103], v[56:59], v[76:79]
	s_waitcnt lgkmcnt(5)
	v_mfma_f32_16x16x32_bf16 v[80:83], v[104:107], v[24:27], v[80:83]
	v_mfma_f32_16x16x32_bf16 v[84:87], v[104:107], v[56:59], v[84:87]
	s_waitcnt lgkmcnt(4)
	v_mfma_f32_16x16x32_bf16 v[88:91], v[108:111], v[24:27], v[88:91]
	v_mfma_f32_16x16x32_bf16 v[92:95], v[108:111], v[56:59], v[92:95]
	s_waitcnt lgkmcnt(3)
	v_mfma_f32_16x16x32_bf16 v[64:67], v[112:115], v[28:31], v[64:67]
	v_mfma_f32_16x16x32_bf16 v[68:71], v[112:115], v[60:63], v[68:71]
	s_waitcnt lgkmcnt(2)
	v_mfma_f32_16x16x32_bf16 v[72:75], v[116:119], v[28:31], v[72:75]
	v_mfma_f32_16x16x32_bf16 v[76:79], v[116:119], v[60:63], v[76:79]
	s_waitcnt lgkmcnt(1)
	v_mfma_f32_16x16x32_bf16 v[80:83], v[120:123], v[28:31], v[80:83]
	v_mfma_f32_16x16x32_bf16 v[84:87], v[120:123], v[60:63], v[84:87]
	s_waitcnt lgkmcnt(0)
	v_mfma_f32_16x16x32_bf16 v[88:91], v[124:127], v[28:31], v[88:91]
	v_mfma_f32_16x16x32_bf16 v[92:95], v[124:127], v[60:63], v[92:95]
	v_mov_b32_e32 v198, v165
	v_mov_b32_e32 v199, v166
	v_mov_b32_e32 v200, v167
	v_mov_b32_e32 v201, v168
	ds_read_u16 v144, v198
	ds_read_u16 v145, v199
	ds_read_u16 v146, v200
	ds_read_u16 v147, v201
	ds_read_u16 v148, v198 offset:8192
	ds_read_u16 v149, v199 offset:8192
	ds_read_u16 v150, v200 offset:8192
	ds_read_u16 v151, v201 offset:8192
	ds_read_u16 v152, v198 offset:16384
	ds_read_u16 v153, v199 offset:16384
	ds_read_u16 v154, v200 offset:16384
	ds_read_u16 v155, v201 offset:16384
	ds_read_u16 v156, v198 offset:24576
	ds_read_u16 v157, v199 offset:24576
	ds_read_u16 v158, v200 offset:24576
	ds_read_u16 v159, v201 offset:24576
	s_nop 7
	v_fma_f32 v178, v64, s53, v173
	v_fma_f32 v179, v65, s53, v173
	v_fma_f32 v180, v66, s53, v173
	v_fma_f32 v181, v67, s53, v173
	v_fma_f32 v182, v72, s53, v173
	v_fma_f32 v183, v73, s53, v173
	v_fma_f32 v184, v74, s53, v173
	v_fma_f32 v185, v75, s53, v173
	v_fma_f32 v186, v68, s53, v174
	v_fma_f32 v187, v69, s53, v174
	v_fma_f32 v188, v70, s53, v174
	v_fma_f32 v189, v71, s53, v174
	v_fma_f32 v190, v76, s53, v174
	v_fma_f32 v191, v77, s53, v174
	v_fma_f32 v192, v78, s53, v174
	v_fma_f32 v193, v79, s53, v174
	v_exp_f32_e32 v178, v178
	v_exp_f32_e32 v179, v179
	v_exp_f32_e32 v180, v180
	v_exp_f32_e32 v181, v181
	v_exp_f32_e32 v182, v182
	v_exp_f32_e32 v183, v183
	v_exp_f32_e32 v184, v184
	v_exp_f32_e32 v185, v185
	v_exp_f32_e32 v186, v186
	v_exp_f32_e32 v187, v187
	v_exp_f32_e32 v188, v188
	v_exp_f32_e32 v189, v189
	v_exp_f32_e32 v190, v190
	v_exp_f32_e32 v191, v191
	v_exp_f32_e32 v192, v192
	v_exp_f32_e32 v193, v193
	v_add_f32_e32 v178, 1.0, v178
	v_add_f32_e32 v179, 1.0, v179
	v_add_f32_e32 v180, 1.0, v180
	v_add_f32_e32 v181, 1.0, v181
	v_add_f32_e32 v182, 1.0, v182
	v_add_f32_e32 v183, 1.0, v183
	v_add_f32_e32 v184, 1.0, v184
	v_add_f32_e32 v185, 1.0, v185
	v_add_f32_e32 v186, 1.0, v186
	v_add_f32_e32 v187, 1.0, v187
	v_add_f32_e32 v188, 1.0, v188
	v_add_f32_e32 v189, 1.0, v189
	v_add_f32_e32 v190, 1.0, v190
	v_add_f32_e32 v191, 1.0, v191
	v_add_f32_e32 v192, 1.0, v192
	v_add_f32_e32 v193, 1.0, v193
	v_rcp_f32_e32 v178, v178
	v_rcp_f32_e32 v179, v179
	v_rcp_f32_e32 v180, v180
	v_rcp_f32_e32 v181, v181
	v_rcp_f32_e32 v182, v182
	v_rcp_f32_e32 v183, v183
	v_rcp_f32_e32 v184, v184
	v_rcp_f32_e32 v185, v185
	v_rcp_f32_e32 v186, v186
	v_rcp_f32_e32 v187, v187
	v_rcp_f32_e32 v188, v188
	v_rcp_f32_e32 v189, v189
	v_rcp_f32_e32 v190, v190
	v_rcp_f32_e32 v191, v191
	v_rcp_f32_e32 v192, v192
	v_rcp_f32_e32 v193, v193
	v_mul_f32_e32 v178, v175, v178
	v_mul_f32_e32 v179, v175, v179
	v_mul_f32_e32 v180, v175, v180
	v_mul_f32_e32 v181, v175, v181
	v_mul_f32_e32 v182, v175, v182
	v_mul_f32_e32 v183, v175, v183
	v_mul_f32_e32 v184, v175, v184
	v_mul_f32_e32 v185, v175, v185
	v_exp_f32_e32 v96, v178
	v_exp_f32_e32 v97, v179
	v_exp_f32_e32 v98, v180
	v_exp_f32_e32 v99, v181
	v_exp_f32_e32 v100, v182
	v_exp_f32_e32 v101, v183
	v_exp_f32_e32 v102, v184
	v_exp_f32_e32 v103, v185
	s_nop 0
	v_fma_f32 v194, -v96, v96, 1.0
	v_fma_f32 v195, -v97, v97, 1.0
	v_fma_f32 v196, -v98, v98, 1.0
	v_fma_f32 v197, -v99, v99, 1.0
	v_fma_f32 v198, -v100, v100, 1.0
	v_fma_f32 v199, -v101, v101, 1.0
	v_fma_f32 v200, -v102, v102, 1.0
	v_fma_f32 v201, -v103, v103, 1.0
	v_max_f32_e32 v194, 0, v194
	v_max_f32_e32 v195, 0, v195
	v_max_f32_e32 v196, 0, v196
	v_max_f32_e32 v197, 0, v197
	v_max_f32_e32 v198, 0, v198
	v_max_f32_e32 v199, 0, v199
	v_max_f32_e32 v200, 0, v200
	v_max_f32_e32 v201, 0, v201
	v_sqrt_f32_e32 v194, v194
	v_sqrt_f32_e32 v195, v195
	v_sqrt_f32_e32 v196, v196
	v_sqrt_f32_e32 v197, v197
	v_sqrt_f32_e32 v198, v198
	v_sqrt_f32_e32 v199, v199
	v_sqrt_f32_e32 v200, v200
	v_sqrt_f32_e32 v201, v201
	s_waitcnt lgkmcnt(8)
	v_lshlrev_b32_e32 v144, 16, v144
	v_lshlrev_b32_e32 v145, 16, v145
	v_lshlrev_b32_e32 v146, 16, v146
	v_lshlrev_b32_e32 v147, 16, v147
	v_lshlrev_b32_e32 v148, 16, v148
	v_lshlrev_b32_e32 v149, 16, v149
	v_lshlrev_b32_e32 v150, 16, v150
	v_lshlrev_b32_e32 v151, 16, v151
	v_mul_f32_e32 v194, v194, v186
	v_mul_f32_e32 v195, v195, v187
	v_mul_f32_e32 v196, v196, v188
	v_mul_f32_e32 v197, v197, v189
	v_mul_f32_e32 v198, v198, v190
	v_mul_f32_e32 v199, v199, v191
	v_mul_f32_e32 v200, v200, v192
	v_mul_f32_e32 v201, v201, v193
	v_mul_f32_e32 v144, v194, v144
	v_mul_f32_e32 v145, v195, v145
	v_mul_f32_e32 v146, v196, v146
	v_mul_f32_e32 v147, v197, v147
	v_mul_f32_e32 v148, v198, v148
	v_mul_f32_e32 v149, v199, v149
	v_mul_f32_e32 v150, v200, v150
	v_mul_f32_e32 v151, v201, v151
	v_fma_f32 v178, v80, s53, v173
	v_fma_f32 v179, v81, s53, v173
	v_fma_f32 v180, v82, s53, v173
	v_fma_f32 v181, v83, s53, v173
	v_fma_f32 v182, v88, s53, v173
	v_fma_f32 v183, v89, s53, v173
	v_fma_f32 v184, v90, s53, v173
	v_fma_f32 v185, v91, s53, v173
	v_fma_f32 v186, v84, s53, v174
	v_fma_f32 v187, v85, s53, v174
	v_fma_f32 v188, v86, s53, v174
	v_fma_f32 v189, v87, s53, v174
	v_fma_f32 v190, v92, s53, v174
	v_fma_f32 v191, v93, s53, v174
	v_fma_f32 v192, v94, s53, v174
	v_fma_f32 v193, v95, s53, v174
	v_exp_f32_e32 v178, v178
	v_exp_f32_e32 v179, v179
	v_exp_f32_e32 v180, v180
	v_exp_f32_e32 v181, v181
	v_exp_f32_e32 v182, v182
	v_exp_f32_e32 v183, v183
	v_exp_f32_e32 v184, v184
	v_exp_f32_e32 v185, v185
	v_exp_f32_e32 v186, v186
	v_exp_f32_e32 v187, v187
	v_exp_f32_e32 v188, v188
	v_exp_f32_e32 v189, v189
	v_exp_f32_e32 v190, v190
	v_exp_f32_e32 v191, v191
	v_exp_f32_e32 v192, v192
	v_exp_f32_e32 v193, v193
	v_add_f32_e32 v178, 1.0, v178
	v_add_f32_e32 v179, 1.0, v179
	v_add_f32_e32 v180, 1.0, v180
	v_add_f32_e32 v181, 1.0, v181
	v_add_f32_e32 v182, 1.0, v182
	v_add_f32_e32 v183, 1.0, v183
	v_add_f32_e32 v184, 1.0, v184
	v_add_f32_e32 v185, 1.0, v185
	v_add_f32_e32 v186, 1.0, v186
	v_add_f32_e32 v187, 1.0, v187
	v_add_f32_e32 v188, 1.0, v188
	v_add_f32_e32 v189, 1.0, v189
	v_add_f32_e32 v190, 1.0, v190
	v_add_f32_e32 v191, 1.0, v191
	v_add_f32_e32 v192, 1.0, v192
	v_add_f32_e32 v193, 1.0, v193
	v_rcp_f32_e32 v178, v178
	v_rcp_f32_e32 v179, v179
	v_rcp_f32_e32 v180, v180
	v_rcp_f32_e32 v181, v181
	v_rcp_f32_e32 v182, v182
	v_rcp_f32_e32 v183, v183
	v_rcp_f32_e32 v184, v184
	v_rcp_f32_e32 v185, v185
	v_rcp_f32_e32 v186, v186
	v_rcp_f32_e32 v187, v187
	v_rcp_f32_e32 v188, v188
	v_rcp_f32_e32 v189, v189
	v_rcp_f32_e32 v190, v190
	v_rcp_f32_e32 v191, v191
	v_rcp_f32_e32 v192, v192
	v_rcp_f32_e32 v193, v193
	v_mul_f32_e32 v178, v175, v178
	v_mul_f32_e32 v179, v175, v179
	v_mul_f32_e32 v180, v175, v180
	v_mul_f32_e32 v181, v175, v181
	v_mul_f32_e32 v182, v175, v182
	v_mul_f32_e32 v183, v175, v183
	v_mul_f32_e32 v184, v175, v184
	v_mul_f32_e32 v185, v175, v185
	v_exp_f32_e32 v104, v178
	v_exp_f32_e32 v105, v179
	v_exp_f32_e32 v106, v180
	v_exp_f32_e32 v107, v181
	v_exp_f32_e32 v108, v182
	v_exp_f32_e32 v109, v183
	v_exp_f32_e32 v110, v184
	v_exp_f32_e32 v111, v185
	s_nop 0
	v_fma_f32 v194, -v104, v104, 1.0
	v_fma_f32 v195, -v105, v105, 1.0
	v_fma_f32 v196, -v106, v106, 1.0
	v_fma_f32 v197, -v107, v107, 1.0
	v_fma_f32 v198, -v108, v108, 1.0
	v_fma_f32 v199, -v109, v109, 1.0
	v_fma_f32 v200, -v110, v110, 1.0
	v_fma_f32 v201, -v111, v111, 1.0
	v_max_f32_e32 v194, 0, v194
	v_max_f32_e32 v195, 0, v195
	v_max_f32_e32 v196, 0, v196
	v_max_f32_e32 v197, 0, v197
	v_max_f32_e32 v198, 0, v198
	v_max_f32_e32 v199, 0, v199
	v_max_f32_e32 v200, 0, v200
	v_max_f32_e32 v201, 0, v201
	v_sqrt_f32_e32 v194, v194
	v_sqrt_f32_e32 v195, v195
	v_sqrt_f32_e32 v196, v196
	v_sqrt_f32_e32 v197, v197
	v_sqrt_f32_e32 v198, v198
	v_sqrt_f32_e32 v199, v199
	v_sqrt_f32_e32 v200, v200
	v_sqrt_f32_e32 v201, v201
	s_waitcnt lgkmcnt(0)
	v_lshlrev_b32_e32 v152, 16, v152
	v_lshlrev_b32_e32 v153, 16, v153
	v_lshlrev_b32_e32 v154, 16, v154
	v_lshlrev_b32_e32 v155, 16, v155
	v_lshlrev_b32_e32 v156, 16, v156
	v_lshlrev_b32_e32 v157, 16, v157
	v_lshlrev_b32_e32 v158, 16, v158
	v_lshlrev_b32_e32 v159, 16, v159
	v_mul_f32_e32 v194, v194, v186
	v_mul_f32_e32 v195, v195, v187
	v_mul_f32_e32 v196, v196, v188
	v_mul_f32_e32 v197, v197, v189
	v_mul_f32_e32 v198, v198, v190
	v_mul_f32_e32 v199, v199, v191
	v_mul_f32_e32 v200, v200, v192
	v_mul_f32_e32 v201, v201, v193
	v_mul_f32_e32 v152, v194, v152
	v_mul_f32_e32 v153, v195, v153
	v_mul_f32_e32 v154, v196, v154
	v_mul_f32_e32 v155, v197, v155
	v_mul_f32_e32 v156, v198, v156
	v_mul_f32_e32 v157, v199, v157
	v_mul_f32_e32 v158, v200, v158
	v_mul_f32_e32 v159, v201, v159
	v_fma_f32 v145, v97, v144, v145
	v_fma_f32 v149, v101, v148, v149
	v_fma_f32 v153, v105, v152, v153
	v_fma_f32 v157, v109, v156, v157
	v_mul_f32_e32 v97, v97, v96
	v_mul_f32_e32 v101, v101, v100
	v_mul_f32_e32 v105, v105, v104
	v_mul_f32_e32 v109, v109, v108
	v_fma_f32 v146, v98, v145, v146
	v_fma_f32 v150, v102, v149, v150
	v_fma_f32 v154, v106, v153, v154
	v_fma_f32 v158, v110, v157, v158
	v_mul_f32_e32 v98, v98, v97
	v_mul_f32_e32 v102, v102, v101
	v_mul_f32_e32 v106, v106, v105
	v_mul_f32_e32 v110, v110, v109
	v_fma_f32 v147, v99, v146, v147
	v_fma_f32 v151, v103, v150, v151
	v_fma_f32 v155, v107, v154, v155
	v_fma_f32 v159, v111, v158, v159
	v_mul_f32_e32 v99, v99, v98
	v_mul_f32_e32 v103, v103, v102
	v_mul_f32_e32 v107, v107, v106
	v_mul_f32_e32 v111, v111, v110
	ds_bpermute_b32 v178, v204, v99
	ds_bpermute_b32 v182, v204, v147
	ds_bpermute_b32 v179, v204, v103
	ds_bpermute_b32 v183, v204, v151
	ds_bpermute_b32 v180, v204, v107
	ds_bpermute_b32 v184, v204, v155
	ds_bpermute_b32 v181, v204, v111
	ds_bpermute_b32 v185, v204, v159
	s_waitcnt lgkmcnt(0)
	v_fma_f32 v186, v182, v99, v147
	v_cndmask_b32_e64 v178, 1.0, v178, s[34:35]
	v_fma_f32 v187, v183, v103, v151
	v_cndmask_b32_e64 v179, 1.0, v179, s[34:35]
	v_fma_f32 v188, v184, v107, v155
	v_cndmask_b32_e64 v180, 1.0, v180, s[34:35]
	v_fma_f32 v189, v185, v111, v159
	v_cndmask_b32_e64 v181, 1.0, v181, s[34:35]
	v_cndmask_b32_e64 v223, v147, v186, s[34:35]
	v_mul_f32_e32 v219, v99, v178
	v_cndmask_b32_e64 v224, v151, v187, s[34:35]
	v_mul_f32_e32 v220, v103, v179
	v_cndmask_b32_e64 v225, v155, v188, s[34:35]
	v_mul_f32_e32 v221, v107, v180
	v_cndmask_b32_e64 v226, v159, v189, s[34:35]
	v_mul_f32_e32 v222, v111, v181
	ds_bpermute_b32 v178, v205, v219
	ds_bpermute_b32 v182, v205, v223
	ds_bpermute_b32 v179, v205, v220
	ds_bpermute_b32 v183, v205, v224
	ds_bpermute_b32 v180, v205, v221
	ds_bpermute_b32 v184, v205, v225
	ds_bpermute_b32 v181, v205, v222
	ds_bpermute_b32 v185, v205, v226
	s_waitcnt lgkmcnt(0)
	v_fma_f32 v186, v182, v219, v223
	v_cndmask_b32_e64 v178, 1.0, v178, s[36:37]
	v_fma_f32 v187, v183, v220, v224
	v_cndmask_b32_e64 v179, 1.0, v179, s[36:37]
	v_fma_f32 v188, v184, v221, v225
	v_cndmask_b32_e64 v180, 1.0, v180, s[36:37]
	v_fma_f32 v189, v185, v222, v226
	v_cndmask_b32_e64 v181, 1.0, v181, s[36:37]
	v_cndmask_b32_e64 v223, v223, v186, s[36:37]
	v_mul_f32_e32 v219, v219, v178
	v_cndmask_b32_e64 v224, v224, v187, s[36:37]
	v_mul_f32_e32 v220, v220, v179
	v_cndmask_b32_e64 v225, v225, v188, s[36:37]
	v_mul_f32_e32 v221, v221, v180
	v_cndmask_b32_e64 v226, v226, v189, s[36:37]
	v_mul_f32_e32 v222, v222, v181
	ds_bpermute_b32 v227, v204, v219
	ds_bpermute_b32 v231, v204, v223
	ds_bpermute_b32 v235, v206, v219
	ds_bpermute_b32 v239, v206, v223
	ds_bpermute_b32 v228, v204, v220
	ds_bpermute_b32 v232, v204, v224
	ds_bpermute_b32 v236, v206, v220
	ds_bpermute_b32 v244, v206, v224
	ds_bpermute_b32 v229, v204, v221
	ds_bpermute_b32 v233, v204, v225
	ds_bpermute_b32 v237, v206, v221
	ds_bpermute_b32 v245, v206, v225
	ds_bpermute_b32 v230, v204, v222
	ds_bpermute_b32 v234, v204, v226
	ds_bpermute_b32 v238, v206, v222
	ds_bpermute_b32 v246, v206, v226
	s_waitcnt lgkmcnt(0)
	v_cndmask_b32_e64 v227, 1.0, v227, s[34:35]
	v_cndmask_b32_e64 v231, 0, v231, s[34:35]
	v_cndmask_b32_e64 v228, 1.0, v228, s[34:35]
	v_cndmask_b32_e64 v232, 0, v232, s[34:35]
	v_cndmask_b32_e64 v229, 1.0, v229, s[34:35]
	v_cndmask_b32_e64 v233, 0, v233, s[34:35]
	v_cndmask_b32_e64 v230, 1.0, v230, s[34:35]
	v_cndmask_b32_e64 v234, 0, v234, s[34:35]
	v_mov_b32_e32 v190, v235
	v_mov_b32_e32 v194, v239
	v_mov_b32_e32 v198, v190
	v_mov_b32_e32 v201, v194
	v_fma_f32 v194, v194, v236, v244
	v_mul_f32_e32 v190, v190, v236
	v_mov_b32_e32 v199, v190
	v_mov_b32_e32 v177, v194
	v_fma_f32 v194, v194, v237, v245
	v_mul_f32_e32 v190, v190, v237
	v_mov_b32_e32 v200, v190
	v_mov_b32_e32 v203, v194
	v_fma_f32 v194, v194, v238, v246
	v_mul_f32_e32 v190, v190, v238
	v_mov_b32_e32 v191, v194
	ds_write_b64 v207, v[190:191]
	s_waitcnt lgkmcnt(0)
	s_barrier
	ds_read_b64 v[178:179], v208
	ds_read_b64 v[180:181], v208 offset:512
	s_waitcnt lgkmcnt(0)
	v_fma_f32 v182, v176, v178, v179
	v_cndmask_b32_e64 v183, v176, v182, s[38:39]
	v_fma_f32 v176, v182, v180, v181
	v_mov_b32_e32 v184, v183
	v_fma_f32 v185, v183, v198, v201
	v_fma_f32 v186, v183, v199, v177
	v_fma_f32 v187, v183, v200, v203
	v_fma_f32 v184, v184, v227, v231
	v_fma_f32 v185, v185, v228, v232
	v_fma_f32 v186, v186, v229, v233
	v_fma_f32 v187, v187, v230, v234
	v_fma_f32 v144, v184, v96, v144
	v_fma_f32 v148, v185, v100, v148
	v_fma_f32 v152, v186, v104, v152
	v_fma_f32 v156, v187, v108, v156
	v_fma_f32 v145, v184, v97, v145
	v_fma_f32 v149, v185, v101, v149
	v_fma_f32 v153, v186, v105, v153
	v_fma_f32 v157, v187, v109, v157
	v_fma_f32 v146, v184, v98, v146
	v_fma_f32 v150, v185, v102, v150
	v_fma_f32 v154, v186, v106, v154
	v_fma_f32 v158, v187, v110, v158
	v_fma_f32 v147, v184, v99, v147
	v_fma_f32 v151, v185, v103, v151
	v_fma_f32 v155, v186, v107, v155
	v_fma_f32 v159, v187, v111, v159
	v_cvt_pk_bf16_f32 v178, v144, v145
	v_cvt_pk_bf16_f32 v179, v146, v147
	v_cvt_pk_bf16_f32 v180, v148, v149
	v_cvt_pk_bf16_f32 v181, v150, v151
	v_cvt_pk_bf16_f32 v182, v152, v153
	v_cvt_pk_bf16_f32 v183, v154, v155
	v_cvt_pk_bf16_f32 v184, v156, v157
	v_cvt_pk_bf16_f32 v185, v158, v159
	global_store_dword v209, v178, s[44:45]
	global_store_dword v209, v179, s[44:45] offset:256
	global_store_dword v209, v180, s[44:45] offset:512
	global_store_dword v209, v181, s[44:45] offset:768
	global_store_dword v209, v182, s[44:45] offset:1024
	global_store_dword v209, v183, s[44:45] offset:1280
	global_store_dword v209, v184, s[44:45] offset:1536
	global_store_dword v209, v185, s[44:45] offset:1792
	s_add_i32 s13, s13, 1
	s_cmp_eq_u32 s13, 2
	s_cbranch_scc1 .Lmylru_t0_4
	s_waitcnt vmcnt(8)
	s_branch .Lmylru_t1_4

.Lmylru_nodma_4:
	v_or_b32_e32 v163, 0x10000, v162
	ds_read_b128 v[96:99], v163
	ds_read_b128 v[100:103], v163 offset:8192
	ds_read_b128 v[104:107], v163 offset:16384
	ds_read_b128 v[108:111], v163 offset:24576
	v_xor_b32_e32 v164, 0x40, v163
	ds_read_b128 v[112:115], v164
	ds_read_b128 v[116:119], v164 offset:8192
	ds_read_b128 v[120:123], v164 offset:16384
	ds_read_b128 v[124:127], v164 offset:24576
	s_waitcnt lgkmcnt(7)
	v_mfma_f32_16x16x32_bf16 v[64:67], v[96:99], v[0:3], 0
	v_mfma_f32_16x16x32_bf16 v[68:71], v[96:99], v[32:35], 0
	v_xor_b32_e32 v164, 0x80, v163
	ds_read_b128 v[96:99], v164
	s_waitcnt lgkmcnt(7)
	v_mfma_f32_16x16x32_bf16 v[72:75], v[100:103], v[0:3], 0
	v_mfma_f32_16x16x32_bf16 v[76:79], v[100:103], v[32:35], 0
	ds_read_b128 v[100:103], v164 offset:8192
	s_waitcnt lgkmcnt(7)
	v_mfma_f32_16x16x32_bf16 v[80:83], v[104:107], v[0:3], 0
	v_mfma_f32_16x16x32_bf16 v[84:87], v[104:107], v[32:35], 0
	ds_read_b128 v[104:107], v164 offset:16384
	s_waitcnt lgkmcnt(7)
	v_mfma_f32_16x16x32_bf16 v[88:91], v[108:111], v[0:3], 0
	v_mfma_f32_16x16x32_bf16 v[92:95], v[108:111], v[32:35], 0
	ds_read_b128 v[108:111], v164 offset:24576
	s_waitcnt lgkmcnt(7)
	v_mfma_f32_16x16x32_bf16 v[64:67], v[112:115], v[4:7], v[64:67]
	v_mfma_f32_16x16x32_bf16 v[68:71], v[112:115], v[36:39], v[68:71]
	v_xor_b32_e32 v164, 0xc0, v163
	ds_read_b128 v[112:115], v164
	s_waitcnt lgkmcnt(7)
	v_mfma_f32_16x16x32_bf16 v[72:75], v[116:119], v[4:7], v[72:75]
	v_mfma_f32_16x16x32_bf16 v[76:79], v[116:119], v[36:39], v[76:79]
	ds_read_b128 v[116:119], v164 offset:8192
	s_waitcnt lgkmcnt(7)
	v_mfma_f32_16x16x32_bf16 v[80:83], v[120:123], v[4:7], v[80:83]
	v_mfma_f32_16x16x32_bf16 v[84:87], v[120:123], v[36:39], v[84:87]
	ds_read_b128 v[120:123], v164 offset:16384
	s_waitcnt lgkmcnt(7)
	v_mfma_f32_16x16x32_bf16 v[88:91], v[124:127], v[4:7], v[88:91]
	v_mfma_f32_16x16x32_bf16 v[92:95], v[124:127], v[36:39], v[92:95]
	ds_read_b128 v[124:127], v164 offset:24576
	s_waitcnt lgkmcnt(7)
	v_mfma_f32_16x16x32_bf16 v[64:67], v[96:99], v[8:11], v[64:67]
	v_mfma_f32_16x16x32_bf16 v[68:71], v[96:99], v[40:43], v[68:71]
	v_xor_b32_e32 v164, 0x100, v163
	ds_read_b128 v[96:99], v164
	s_waitcnt lgkmcnt(7)
	v_mfma_f32_16x16x32_bf16 v[72:75], v[100:103], v[8:11], v[72:75]
	v_mfma_f32_16x16x32_bf16 v[76:79], v[100:103], v[40:43], v[76:79]
	ds_read_b128 v[100:103], v164 offset:8192
	s_waitcnt lgkmcnt(7)
	v_mfma_f32_16x16x32_bf16 v[80:83], v[104:107], v[8:11], v[80:83]
	v_mfma_f32_16x16x32_bf16 v[84:87], v[104:107], v[40:43], v[84:87]
	ds_read_b128 v[104:107], v164 offset:16384
	s_waitcnt lgkmcnt(7)
	v_mfma_f32_16x16x32_bf16 v[88:91], v[108:111], v[8:11], v[88:91]
	v_mfma_f32_16x16x32_bf16 v[92:95], v[108:111], v[40:43], v[92:95]
	ds_read_b128 v[108:111], v164 offset:24576
	s_waitcnt lgkmcnt(7)
	v_mfma_f32_16x16x32_bf16 v[64:67], v[112:115], v[12:15], v[64:67]
	v_mfma_f32_16x16x32_bf16 v[68:71], v[112:115], v[44:47], v[68:71]
	v_xor_b32_e32 v164, 0x140, v163
	ds_read_b128 v[112:115], v164
	s_waitcnt lgkmcnt(7)
	v_mfma_f32_16x16x32_bf16 v[72:75], v[116:119], v[12:15], v[72:75]
	v_mfma_f32_16x16x32_bf16 v[76:79], v[116:119], v[44:47], v[76:79]
	ds_read_b128 v[116:119], v164 offset:8192
	s_waitcnt lgkmcnt(7)
	v_mfma_f32_16x16x32_bf16 v[80:83], v[120:123], v[12:15], v[80:83]
	v_mfma_f32_16x16x32_bf16 v[84:87], v[120:123], v[44:47], v[84:87]
	ds_read_b128 v[120:123], v164 offset:16384
	s_waitcnt lgkmcnt(7)
	v_mfma_f32_16x16x32_bf16 v[88:91], v[124:127], v[12:15], v[88:91]
	v_mfma_f32_16x16x32_bf16 v[92:95], v[124:127], v[44:47], v[92:95]
	ds_read_b128 v[124:127], v164 offset:24576
	s_waitcnt lgkmcnt(7)
	v_mfma_f32_16x16x32_bf16 v[64:67], v[96:99], v[16:19], v[64:67]
	v_mfma_f32_16x16x32_bf16 v[68:71], v[96:99], v[48:51], v[68:71]
	v_xor_b32_e32 v164, 0x180, v163
	ds_read_b128 v[96:99], v164
	s_waitcnt lgkmcnt(7)
	v_mfma_f32_16x16x32_bf16 v[72:75], v[100:103], v[16:19], v[72:75]
	v_mfma_f32_16x16x32_bf16 v[76:79], v[100:103], v[48:51], v[76:79]
	ds_read_b128 v[100:103], v164 offset:8192
	s_waitcnt lgkmcnt(7)
	v_mfma_f32_16x16x32_bf16 v[80:83], v[104:107], v[16:19], v[80:83]
	v_mfma_f32_16x16x32_bf16 v[84:87], v[104:107], v[48:51], v[84:87]
	ds_read_b128 v[104:107], v164 offset:16384
	s_waitcnt lgkmcnt(7)
	v_mfma_f32_16x16x32_bf16 v[88:91], v[108:111], v[16:19], v[88:91]
	v_mfma_f32_16x16x32_bf16 v[92:95], v[108:111], v[48:51], v[92:95]
	ds_read_b128 v[108:111], v164 offset:24576
	s_waitcnt lgkmcnt(7)
	v_mfma_f32_16x16x32_bf16 v[64:67], v[112:115], v[20:23], v[64:67]
	v_mfma_f32_16x16x32_bf16 v[68:71], v[112:115], v[52:55], v[68:71]
	v_xor_b32_e32 v164, 0x1c0, v163
	ds_read_b128 v[112:115], v164
	s_waitcnt lgkmcnt(7)
	v_mfma_f32_16x16x32_bf16 v[72:75], v[116:119], v[20:23], v[72:75]
	v_mfma_f32_16x16x32_bf16 v[76:79], v[116:119], v[52:55], v[76:79]
	ds_read_b128 v[116:119], v164 offset:8192
	s_waitcnt lgkmcnt(7)
	v_mfma_f32_16x16x32_bf16 v[80:83], v[120:123], v[20:23], v[80:83]
	v_mfma_f32_16x16x32_bf16 v[84:87], v[120:123], v[52:55], v[84:87]
	ds_read_b128 v[120:123], v164 offset:16384
	s_waitcnt lgkmcnt(7)
	v_mfma_f32_16x16x32_bf16 v[88:91], v[124:127], v[20:23], v[88:91]
	v_mfma_f32_16x16x32_bf16 v[92:95], v[124:127], v[52:55], v[92:95]
	ds_read_b128 v[124:127], v164 offset:24576
	s_waitcnt lgkmcnt(7)
	v_mfma_f32_16x16x32_bf16 v[64:67], v[96:99], v[24:27], v[64:67]
	v_mfma_f32_16x16x32_bf16 v[68:71], v[96:99], v[56:59], v[68:71]
	s_waitcnt lgkmcnt(6)
	v_mfma_f32_16x16x32_bf16 v[72:75], v[100:103], v[24:27], v[72:75]
	v_mfma_f32_16x16x32_bf16 v[76:79], v[100:103], v[56:59], v[76:79]
	s_waitcnt lgkmcnt(5)
	v_mfma_f32_16x16x32_bf16 v[80:83], v[104:107], v[24:27], v[80:83]
	v_mfma_f32_16x16x32_bf16 v[84:87], v[104:107], v[56:59], v[84:87]
	s_waitcnt lgkmcnt(4)
	v_mfma_f32_16x16x32_bf16 v[88:91], v[108:111], v[24:27], v[88:91]
	v_mfma_f32_16x16x32_bf16 v[92:95], v[108:111], v[56:59], v[92:95]
	s_waitcnt lgkmcnt(3)
	v_mfma_f32_16x16x32_bf16 v[64:67], v[112:115], v[28:31], v[64:67]
	v_mfma_f32_16x16x32_bf16 v[68:71], v[112:115], v[60:63], v[68:71]
	s_waitcnt lgkmcnt(2)
	v_mfma_f32_16x16x32_bf16 v[72:75], v[116:119], v[28:31], v[72:75]
	v_mfma_f32_16x16x32_bf16 v[76:79], v[116:119], v[60:63], v[76:79]
	s_waitcnt lgkmcnt(1)
	v_mfma_f32_16x16x32_bf16 v[80:83], v[120:123], v[28:31], v[80:83]
	v_mfma_f32_16x16x32_bf16 v[84:87], v[120:123], v[60:63], v[84:87]
	s_waitcnt lgkmcnt(0)
	v_mfma_f32_16x16x32_bf16 v[88:91], v[124:127], v[28:31], v[88:91]
	v_mfma_f32_16x16x32_bf16 v[92:95], v[124:127], v[60:63], v[92:95]
	v_or_b32_e32 v198, 0x10000, v165
	v_or_b32_e32 v199, 0x10000, v166
	v_or_b32_e32 v200, 0x10000, v167
	v_or_b32_e32 v201, 0x10000, v168
	ds_read_u16 v144, v198
	ds_read_u16 v145, v199
	ds_read_u16 v146, v200
	ds_read_u16 v147, v201
	ds_read_u16 v148, v198 offset:8192
	ds_read_u16 v149, v199 offset:8192
	ds_read_u16 v150, v200 offset:8192
	ds_read_u16 v151, v201 offset:8192
	ds_read_u16 v152, v198 offset:16384
	ds_read_u16 v153, v199 offset:16384
	ds_read_u16 v154, v200 offset:16384
	ds_read_u16 v155, v201 offset:16384
	ds_read_u16 v156, v198 offset:24576
	ds_read_u16 v157, v199 offset:24576
	ds_read_u16 v158, v200 offset:24576
	ds_read_u16 v159, v201 offset:24576
	s_nop 7
	v_fma_f32 v178, v64, s53, v173
	v_fma_f32 v179, v65, s53, v173
	v_fma_f32 v180, v66, s53, v173
	v_fma_f32 v181, v67, s53, v173
	v_fma_f32 v182, v72, s53, v173
	v_fma_f32 v183, v73, s53, v173
	v_fma_f32 v184, v74, s53, v173
	v_fma_f32 v185, v75, s53, v173
	v_fma_f32 v186, v68, s53, v174
	v_fma_f32 v187, v69, s53, v174
	v_fma_f32 v188, v70, s53, v174
	v_fma_f32 v189, v71, s53, v174
	v_fma_f32 v190, v76, s53, v174
	v_fma_f32 v191, v77, s53, v174
	v_fma_f32 v192, v78, s53, v174
	v_fma_f32 v193, v79, s53, v174
	v_exp_f32_e32 v178, v178
	v_exp_f32_e32 v179, v179
	v_exp_f32_e32 v180, v180
	v_exp_f32_e32 v181, v181
	v_exp_f32_e32 v182, v182
	v_exp_f32_e32 v183, v183
	v_exp_f32_e32 v184, v184
	v_exp_f32_e32 v185, v185
	v_exp_f32_e32 v186, v186
	v_exp_f32_e32 v187, v187
	v_exp_f32_e32 v188, v188
	v_exp_f32_e32 v189, v189
	v_exp_f32_e32 v190, v190
	v_exp_f32_e32 v191, v191
	v_exp_f32_e32 v192, v192
	v_exp_f32_e32 v193, v193
	v_add_f32_e32 v178, 1.0, v178
	v_add_f32_e32 v179, 1.0, v179
	v_add_f32_e32 v180, 1.0, v180
	v_add_f32_e32 v181, 1.0, v181
	v_add_f32_e32 v182, 1.0, v182
	v_add_f32_e32 v183, 1.0, v183
	v_add_f32_e32 v184, 1.0, v184
	v_add_f32_e32 v185, 1.0, v185
	v_add_f32_e32 v186, 1.0, v186
	v_add_f32_e32 v187, 1.0, v187
	v_add_f32_e32 v188, 1.0, v188
	v_add_f32_e32 v189, 1.0, v189
	v_add_f32_e32 v190, 1.0, v190
	v_add_f32_e32 v191, 1.0, v191
	v_add_f32_e32 v192, 1.0, v192
	v_add_f32_e32 v193, 1.0, v193
	v_rcp_f32_e32 v178, v178
	v_rcp_f32_e32 v179, v179
	v_rcp_f32_e32 v180, v180
	v_rcp_f32_e32 v181, v181
	v_rcp_f32_e32 v182, v182
	v_rcp_f32_e32 v183, v183
	v_rcp_f32_e32 v184, v184
	v_rcp_f32_e32 v185, v185
	v_rcp_f32_e32 v186, v186
	v_rcp_f32_e32 v187, v187
	v_rcp_f32_e32 v188, v188
	v_rcp_f32_e32 v189, v189
	v_rcp_f32_e32 v190, v190
	v_rcp_f32_e32 v191, v191
	v_rcp_f32_e32 v192, v192
	v_rcp_f32_e32 v193, v193
	v_mul_f32_e32 v178, v175, v178
	v_mul_f32_e32 v179, v175, v179
	v_mul_f32_e32 v180, v175, v180
	v_mul_f32_e32 v181, v175, v181
	v_mul_f32_e32 v182, v175, v182
	v_mul_f32_e32 v183, v175, v183
	v_mul_f32_e32 v184, v175, v184
	v_mul_f32_e32 v185, v175, v185
	v_exp_f32_e32 v96, v178
	v_exp_f32_e32 v97, v179
	v_exp_f32_e32 v98, v180
	v_exp_f32_e32 v99, v181
	v_exp_f32_e32 v100, v182
	v_exp_f32_e32 v101, v183
	v_exp_f32_e32 v102, v184
	v_exp_f32_e32 v103, v185
	s_nop 0
	v_fma_f32 v194, -v96, v96, 1.0
	v_fma_f32 v195, -v97, v97, 1.0
	v_fma_f32 v196, -v98, v98, 1.0
	v_fma_f32 v197, -v99, v99, 1.0
	v_fma_f32 v198, -v100, v100, 1.0
	v_fma_f32 v199, -v101, v101, 1.0
	v_fma_f32 v200, -v102, v102, 1.0
	v_fma_f32 v201, -v103, v103, 1.0
	v_max_f32_e32 v194, 0, v194
	v_max_f32_e32 v195, 0, v195
	v_max_f32_e32 v196, 0, v196
	v_max_f32_e32 v197, 0, v197
	v_max_f32_e32 v198, 0, v198
	v_max_f32_e32 v199, 0, v199
	v_max_f32_e32 v200, 0, v200
	v_max_f32_e32 v201, 0, v201
	v_sqrt_f32_e32 v194, v194
	v_sqrt_f32_e32 v195, v195
	v_sqrt_f32_e32 v196, v196
	v_sqrt_f32_e32 v197, v197
	v_sqrt_f32_e32 v198, v198
	v_sqrt_f32_e32 v199, v199
	v_sqrt_f32_e32 v200, v200
	v_sqrt_f32_e32 v201, v201
	s_waitcnt lgkmcnt(8)
	v_lshlrev_b32_e32 v144, 16, v144
	v_lshlrev_b32_e32 v145, 16, v145
	v_lshlrev_b32_e32 v146, 16, v146
	v_lshlrev_b32_e32 v147, 16, v147
	v_lshlrev_b32_e32 v148, 16, v148
	v_lshlrev_b32_e32 v149, 16, v149
	v_lshlrev_b32_e32 v150, 16, v150
	v_lshlrev_b32_e32 v151, 16, v151
	v_mul_f32_e32 v194, v194, v186
	v_mul_f32_e32 v195, v195, v187
	v_mul_f32_e32 v196, v196, v188
	v_mul_f32_e32 v197, v197, v189
	v_mul_f32_e32 v198, v198, v190
	v_mul_f32_e32 v199, v199, v191
	v_mul_f32_e32 v200, v200, v192
	v_mul_f32_e32 v201, v201, v193
	v_mul_f32_e32 v144, v194, v144
	v_mul_f32_e32 v145, v195, v145
	v_mul_f32_e32 v146, v196, v146
	v_mul_f32_e32 v147, v197, v147
	v_mul_f32_e32 v148, v198, v148
	v_mul_f32_e32 v149, v199, v149
	v_mul_f32_e32 v150, v200, v150
	v_mul_f32_e32 v151, v201, v151
	v_fma_f32 v178, v80, s53, v173
	v_fma_f32 v179, v81, s53, v173
	v_fma_f32 v180, v82, s53, v173
	v_fma_f32 v181, v83, s53, v173
	v_fma_f32 v182, v88, s53, v173
	v_fma_f32 v183, v89, s53, v173
	v_fma_f32 v184, v90, s53, v173
	v_fma_f32 v185, v91, s53, v173
	v_fma_f32 v186, v84, s53, v174
	v_fma_f32 v187, v85, s53, v174
	v_fma_f32 v188, v86, s53, v174
	v_fma_f32 v189, v87, s53, v174
	v_fma_f32 v190, v92, s53, v174
	v_fma_f32 v191, v93, s53, v174
	v_fma_f32 v192, v94, s53, v174
	v_fma_f32 v193, v95, s53, v174
	v_exp_f32_e32 v178, v178
	v_exp_f32_e32 v179, v179
	v_exp_f32_e32 v180, v180
	v_exp_f32_e32 v181, v181
	v_exp_f32_e32 v182, v182
	v_exp_f32_e32 v183, v183
	v_exp_f32_e32 v184, v184
	v_exp_f32_e32 v185, v185
	v_exp_f32_e32 v186, v186
	v_exp_f32_e32 v187, v187
	v_exp_f32_e32 v188, v188
	v_exp_f32_e32 v189, v189
	v_exp_f32_e32 v190, v190
	v_exp_f32_e32 v191, v191
	v_exp_f32_e32 v192, v192
	v_exp_f32_e32 v193, v193
	v_add_f32_e32 v178, 1.0, v178
	v_add_f32_e32 v179, 1.0, v179
	v_add_f32_e32 v180, 1.0, v180
	v_add_f32_e32 v181, 1.0, v181
	v_add_f32_e32 v182, 1.0, v182
	v_add_f32_e32 v183, 1.0, v183
	v_add_f32_e32 v184, 1.0, v184
	v_add_f32_e32 v185, 1.0, v185
	v_add_f32_e32 v186, 1.0, v186
	v_add_f32_e32 v187, 1.0, v187
	v_add_f32_e32 v188, 1.0, v188
	v_add_f32_e32 v189, 1.0, v189
	v_add_f32_e32 v190, 1.0, v190
	v_add_f32_e32 v191, 1.0, v191
	v_add_f32_e32 v192, 1.0, v192
	v_add_f32_e32 v193, 1.0, v193
	v_rcp_f32_e32 v178, v178
	v_rcp_f32_e32 v179, v179
	v_rcp_f32_e32 v180, v180
	v_rcp_f32_e32 v181, v181
	v_rcp_f32_e32 v182, v182
	v_rcp_f32_e32 v183, v183
	v_rcp_f32_e32 v184, v184
	v_rcp_f32_e32 v185, v185
	v_rcp_f32_e32 v186, v186
	v_rcp_f32_e32 v187, v187
	v_rcp_f32_e32 v188, v188
	v_rcp_f32_e32 v189, v189
	v_rcp_f32_e32 v190, v190
	v_rcp_f32_e32 v191, v191
	v_rcp_f32_e32 v192, v192
	v_rcp_f32_e32 v193, v193
	v_mul_f32_e32 v178, v175, v178
	v_mul_f32_e32 v179, v175, v179
	v_mul_f32_e32 v180, v175, v180
	v_mul_f32_e32 v181, v175, v181
	v_mul_f32_e32 v182, v175, v182
	v_mul_f32_e32 v183, v175, v183
	v_mul_f32_e32 v184, v175, v184
	v_mul_f32_e32 v185, v175, v185
	v_exp_f32_e32 v104, v178
	v_exp_f32_e32 v105, v179
	v_exp_f32_e32 v106, v180
	v_exp_f32_e32 v107, v181
	v_exp_f32_e32 v108, v182
	v_exp_f32_e32 v109, v183
	v_exp_f32_e32 v110, v184
	v_exp_f32_e32 v111, v185
	s_nop 0
	v_fma_f32 v194, -v104, v104, 1.0
	v_fma_f32 v195, -v105, v105, 1.0
	v_fma_f32 v196, -v106, v106, 1.0
	v_fma_f32 v197, -v107, v107, 1.0
	v_fma_f32 v198, -v108, v108, 1.0
	v_fma_f32 v199, -v109, v109, 1.0
	v_fma_f32 v200, -v110, v110, 1.0
	v_fma_f32 v201, -v111, v111, 1.0
	v_max_f32_e32 v194, 0, v194
	v_max_f32_e32 v195, 0, v195
	v_max_f32_e32 v196, 0, v196
	v_max_f32_e32 v197, 0, v197
	v_max_f32_e32 v198, 0, v198
	v_max_f32_e32 v199, 0, v199
	v_max_f32_e32 v200, 0, v200
	v_max_f32_e32 v201, 0, v201
	v_sqrt_f32_e32 v194, v194
	v_sqrt_f32_e32 v195, v195
	v_sqrt_f32_e32 v196, v196
	v_sqrt_f32_e32 v197, v197
	v_sqrt_f32_e32 v198, v198
	v_sqrt_f32_e32 v199, v199
	v_sqrt_f32_e32 v200, v200
	v_sqrt_f32_e32 v201, v201
	s_waitcnt lgkmcnt(0)
	v_lshlrev_b32_e32 v152, 16, v152
	v_lshlrev_b32_e32 v153, 16, v153
	v_lshlrev_b32_e32 v154, 16, v154
	v_lshlrev_b32_e32 v155, 16, v155
	v_lshlrev_b32_e32 v156, 16, v156
	v_lshlrev_b32_e32 v157, 16, v157
	v_lshlrev_b32_e32 v158, 16, v158
	v_lshlrev_b32_e32 v159, 16, v159
	v_mul_f32_e32 v194, v194, v186
	v_mul_f32_e32 v195, v195, v187
	v_mul_f32_e32 v196, v196, v188
	v_mul_f32_e32 v197, v197, v189
	v_mul_f32_e32 v198, v198, v190
	v_mul_f32_e32 v199, v199, v191
	v_mul_f32_e32 v200, v200, v192
	v_mul_f32_e32 v201, v201, v193
	v_mul_f32_e32 v152, v194, v152
	v_mul_f32_e32 v153, v195, v153
	v_mul_f32_e32 v154, v196, v154
	v_mul_f32_e32 v155, v197, v155
	v_mul_f32_e32 v156, v198, v156
	v_mul_f32_e32 v157, v199, v157
	v_mul_f32_e32 v158, v200, v158
	v_mul_f32_e32 v159, v201, v159
	v_fma_f32 v145, v97, v144, v145
	v_fma_f32 v149, v101, v148, v149
	v_fma_f32 v153, v105, v152, v153
	v_fma_f32 v157, v109, v156, v157
	v_mul_f32_e32 v97, v97, v96
	v_mul_f32_e32 v101, v101, v100
	v_mul_f32_e32 v105, v105, v104
	v_mul_f32_e32 v109, v109, v108
	v_fma_f32 v146, v98, v145, v146
	v_fma_f32 v150, v102, v149, v150
	v_fma_f32 v154, v106, v153, v154
	v_fma_f32 v158, v110, v157, v158
	v_mul_f32_e32 v98, v98, v97
	v_mul_f32_e32 v102, v102, v101
	v_mul_f32_e32 v106, v106, v105
	v_mul_f32_e32 v110, v110, v109
	v_fma_f32 v147, v99, v146, v147
	v_fma_f32 v151, v103, v150, v151
	v_fma_f32 v155, v107, v154, v155
	v_fma_f32 v159, v111, v158, v159
	v_mul_f32_e32 v99, v99, v98
	v_mul_f32_e32 v103, v103, v102
	v_mul_f32_e32 v107, v107, v106
	v_mul_f32_e32 v111, v111, v110
	ds_bpermute_b32 v178, v204, v99
	ds_bpermute_b32 v182, v204, v147
	ds_bpermute_b32 v179, v204, v103
	ds_bpermute_b32 v183, v204, v151
	ds_bpermute_b32 v180, v204, v107
	ds_bpermute_b32 v184, v204, v155
	ds_bpermute_b32 v181, v204, v111
	ds_bpermute_b32 v185, v204, v159
	s_waitcnt lgkmcnt(0)
	v_fma_f32 v186, v182, v99, v147
	v_cndmask_b32_e64 v178, 1.0, v178, s[34:35]
	v_fma_f32 v187, v183, v103, v151
	v_cndmask_b32_e64 v179, 1.0, v179, s[34:35]
	v_fma_f32 v188, v184, v107, v155
	v_cndmask_b32_e64 v180, 1.0, v180, s[34:35]
	v_fma_f32 v189, v185, v111, v159
	v_cndmask_b32_e64 v181, 1.0, v181, s[34:35]
	v_cndmask_b32_e64 v223, v147, v186, s[34:35]
	v_mul_f32_e32 v219, v99, v178
	v_cndmask_b32_e64 v224, v151, v187, s[34:35]
	v_mul_f32_e32 v220, v103, v179
	v_cndmask_b32_e64 v225, v155, v188, s[34:35]
	v_mul_f32_e32 v221, v107, v180
	v_cndmask_b32_e64 v226, v159, v189, s[34:35]
	v_mul_f32_e32 v222, v111, v181
	ds_bpermute_b32 v178, v205, v219
	ds_bpermute_b32 v182, v205, v223
	ds_bpermute_b32 v179, v205, v220
	ds_bpermute_b32 v183, v205, v224
	ds_bpermute_b32 v180, v205, v221
	ds_bpermute_b32 v184, v205, v225
	ds_bpermute_b32 v181, v205, v222
	ds_bpermute_b32 v185, v205, v226
	s_waitcnt lgkmcnt(0)
	v_fma_f32 v186, v182, v219, v223
	v_cndmask_b32_e64 v178, 1.0, v178, s[36:37]
	v_fma_f32 v187, v183, v220, v224
	v_cndmask_b32_e64 v179, 1.0, v179, s[36:37]
	v_fma_f32 v188, v184, v221, v225
	v_cndmask_b32_e64 v180, 1.0, v180, s[36:37]
	v_fma_f32 v189, v185, v222, v226
	v_cndmask_b32_e64 v181, 1.0, v181, s[36:37]
	v_cndmask_b32_e64 v223, v223, v186, s[36:37]
	v_mul_f32_e32 v219, v219, v178
	v_cndmask_b32_e64 v224, v224, v187, s[36:37]
	v_mul_f32_e32 v220, v220, v179
	v_cndmask_b32_e64 v225, v225, v188, s[36:37]
	v_mul_f32_e32 v221, v221, v180
	v_cndmask_b32_e64 v226, v226, v189, s[36:37]
	v_mul_f32_e32 v222, v222, v181
	ds_bpermute_b32 v227, v204, v219
	ds_bpermute_b32 v231, v204, v223
	ds_bpermute_b32 v235, v206, v219
	ds_bpermute_b32 v239, v206, v223
	ds_bpermute_b32 v228, v204, v220
	ds_bpermute_b32 v232, v204, v224
	ds_bpermute_b32 v236, v206, v220
	ds_bpermute_b32 v244, v206, v224
	ds_bpermute_b32 v229, v204, v221
	ds_bpermute_b32 v233, v204, v225
	ds_bpermute_b32 v237, v206, v221
	ds_bpermute_b32 v245, v206, v225
	ds_bpermute_b32 v230, v204, v222
	ds_bpermute_b32 v234, v204, v226
	ds_bpermute_b32 v238, v206, v222
	ds_bpermute_b32 v246, v206, v226
	s_waitcnt lgkmcnt(0)
	v_cndmask_b32_e64 v227, 1.0, v227, s[34:35]
	v_cndmask_b32_e64 v231, 0, v231, s[34:35]
	v_cndmask_b32_e64 v228, 1.0, v228, s[34:35]
	v_cndmask_b32_e64 v232, 0, v232, s[34:35]
	v_cndmask_b32_e64 v229, 1.0, v229, s[34:35]
	v_cndmask_b32_e64 v233, 0, v233, s[34:35]
	v_cndmask_b32_e64 v230, 1.0, v230, s[34:35]
	v_cndmask_b32_e64 v234, 0, v234, s[34:35]
	v_mov_b32_e32 v190, v235
	v_mov_b32_e32 v194, v239
	v_mov_b32_e32 v198, v190
	v_mov_b32_e32 v201, v194
	v_fma_f32 v194, v194, v236, v244
	v_mul_f32_e32 v190, v190, v236
	v_mov_b32_e32 v199, v190
	v_mov_b32_e32 v177, v194
	v_fma_f32 v194, v194, v237, v245
	v_mul_f32_e32 v190, v190, v237
	v_mov_b32_e32 v200, v190
	v_mov_b32_e32 v203, v194
	v_fma_f32 v194, v194, v238, v246
	v_mul_f32_e32 v190, v190, v238
	v_mov_b32_e32 v191, v194
	ds_write_b64 v207, v[190:191] offset:1024
	s_waitcnt lgkmcnt(0)
	s_barrier
	ds_read_b64 v[178:179], v208 offset:1024
	ds_read_b64 v[180:181], v208 offset:1536
	s_waitcnt lgkmcnt(0)
	v_fma_f32 v182, v176, v178, v179
	v_cndmask_b32_e64 v183, v176, v182, s[38:39]
	v_fma_f32 v176, v182, v180, v181
	v_mov_b32_e32 v184, v183
	v_fma_f32 v185, v183, v198, v201
	v_fma_f32 v186, v183, v199, v177
	v_fma_f32 v187, v183, v200, v203
	v_fma_f32 v184, v184, v227, v231
	v_fma_f32 v185, v185, v228, v232
	v_fma_f32 v186, v186, v229, v233
	v_fma_f32 v187, v187, v230, v234
	v_fma_f32 v144, v184, v96, v144
	v_fma_f32 v148, v185, v100, v148
	v_fma_f32 v152, v186, v104, v152
	v_fma_f32 v156, v187, v108, v156
	v_fma_f32 v145, v184, v97, v145
	v_fma_f32 v149, v185, v101, v149
	v_fma_f32 v153, v186, v105, v153
	v_fma_f32 v157, v187, v109, v157
	v_fma_f32 v146, v184, v98, v146
	v_fma_f32 v150, v185, v102, v150
	v_fma_f32 v154, v186, v106, v154
	v_fma_f32 v158, v187, v110, v158
	v_fma_f32 v147, v184, v99, v147
	v_fma_f32 v151, v185, v103, v151
	v_fma_f32 v155, v186, v107, v155
	v_fma_f32 v159, v187, v111, v159
	v_cvt_pk_bf16_f32 v178, v144, v145
	v_cvt_pk_bf16_f32 v179, v146, v147
	v_cvt_pk_bf16_f32 v180, v148, v149
	v_cvt_pk_bf16_f32 v181, v150, v151
	v_cvt_pk_bf16_f32 v182, v152, v153
	v_cvt_pk_bf16_f32 v183, v154, v155
	v_cvt_pk_bf16_f32 v184, v156, v157
	v_cvt_pk_bf16_f32 v185, v158, v159
	global_store_dword v209, v178, s[44:45]
	global_store_dword v209, v179, s[44:45] offset:256
	global_store_dword v209, v180, s[44:45] offset:512
	global_store_dword v209, v181, s[44:45] offset:768
	global_store_dword v209, v182, s[44:45] offset:1024
	global_store_dword v209, v183, s[44:45] offset:1280
	global_store_dword v209, v184, s[44:45] offset:1536
	global_store_dword v209, v185, s[44:45] offset:1792
	s_add_i32 s13, s13, 1
	s_add_i32 s60, s60, -1
	s_cmp_lg_u32 s60, 0
	s_cbranch_scc1 .Lmylru_loop_0
	s_lshl_b32 s50, s10, 10
	s_lshl_b32 s51, s11, 6
	s_add_i32 s50, s50, s51
	s_lshl_b32 s51, s8, 4
	s_add_i32 s50, s50, s51
	s_add_i32 s50, s50, 512
	s_lshl_b32 s50, s50, 9
	s_add_u32 s46, s2, s50
	s_addc_u32 s47, s3, 0
	s_add_u32 s46, s46, 0x1000000
	s_addc_u32 s47, s47, 0
	s_add_u32 s48, s46, 0x20000
	s_addc_u32 s49, s47, 0
	v_lshlrev_b32_e32 v178, 9, v160
	v_lshl_add_u32 v178, v161, 4, v178
	global_load_dwordx4 v[0:3], v178, s[46:47]
	global_load_dwordx4 v[4:7], v178, s[46:47] offset:64
	global_load_dwordx4 v[8:11], v178, s[46:47] offset:128
	global_load_dwordx4 v[12:15], v178, s[46:47] offset:192
	global_load_dwordx4 v[16:19], v178, s[46:47] offset:256
	global_load_dwordx4 v[20:23], v178, s[46:47] offset:320
	global_load_dwordx4 v[24:27], v178, s[46:47] offset:384
	global_load_dwordx4 v[28:31], v178, s[46:47] offset:448
	global_load_dwordx4 v[32:35], v178, s[48:49]
	global_load_dwordx4 v[36:39], v178, s[48:49] offset:64
	global_load_dwordx4 v[40:43], v178, s[48:49] offset:128
	global_load_dwordx4 v[44:47], v178, s[48:49] offset:192
	global_load_dwordx4 v[48:51], v178, s[48:49] offset:256
	global_load_dwordx4 v[52:55], v178, s[48:49] offset:320
	global_load_dwordx4 v[56:59], v178, s[48:49] offset:384
	global_load_dwordx4 v[60:63], v178, s[48:49] offset:448
	s_load_dwordx2 s[46:47], s[0:1], 0xc8
	s_load_dwordx2 s[48:49], s[0:1], 0xd8
	s_load_dwordx2 s[40:41], s[0:1], 0xe0
	s_lshl_b32 s50, s10, 8
	s_lshl_b32 s51, s11, 6
	s_add_i32 s50, s50, s51
	s_lshl_b32 s51, s8, 4
	s_add_i32 s50, s50, s51
	v_add_u32_e32 v179, s50, v160
	v_lshlrev_b32_e32 v179, 2, v179
	s_waitcnt lgkmcnt(0)
	global_load_dword v173, v179, s[46:47]
	global_load_dword v174, v179, s[48:49]
	global_load_dword v175, v179, s[40:41]
	v_cmp_gt_u32_e64 s[34:35], 48, v202
	v_cmp_gt_u32_e64 s[36:37], 32, v202
	v_add_u32_e32 v204, 16, v202
	v_add_u32_e32 v205, 32, v202
	v_mov_b32_e32 v206, v160
	s_cmp_eq_u32 s7, 0
	s_cselect_b64 s[38:39], -1, 0
	v_and_b32_e32 v204, 63, v204
	v_lshlrev_b32_e32 v204, 2, v204
	v_and_b32_e32 v205, 63, v205
	v_lshlrev_b32_e32 v205, 2, v205
	v_and_b32_e32 v206, 63, v206
	v_lshlrev_b32_e32 v206, 2, v206
	v_mov_b32_e32 v176, 0
	s_mov_b32 s53, 0xbfb8aa3b
	s_waitcnt vmcnt(0)
	v_mul_f32_e32 v173, s53, v173
	v_mul_f32_e32 v174, s53, v174
	v_mul_f32_e32 v175, s53, v175
	v_exp_f32_e32 v175, v175
	s_nop 0
	v_add_f32_e32 v180, 1.0, v175
	v_log_f32_e32 v180, v180
	v_mov_b32_e32 v181, 0x3eaaaaab
	v_fma_f32 v181, v175, v181, -0.5
	v_fma_f32 v181, v175, v181, 1.0
	v_mul_f32_e32 v181, v175, v181
	v_mul_f32_e32 v181, 0x3fb8aa3b, v181
	v_cmp_gt_f32_e32 vcc, 0x3cf5c28f, v175
	s_nop 1
	v_cndmask_b32_e32 v175, v180, v181, vcc
	v_mul_f32_e32 v175, 0xc1000000, v175
	s_mov_b32 s13, 0
	s_barrier
	s_cmp_lt_u32 s13, 2
	s_sub_i32 s50, 1, s13
	s_lshl_b32 s50, s50, 7
	s_lshl_b32 s51, s9, 8
	s_add_i32 s51, s51, 0x8000
	s_add_i32 s51, s51, s50
	s_sub_i32 s50, 17, s13
	s_lshl_b32 s50, s50, 7
	s_lshl_b32 s59, s9, 11
	s_add_i32 s59, s59, s50
	s_cmp_lt_u32 s13, 2
	s_cselect_b32 s59, s51, s59
	s_lshl_b32 s52, s59, 11
	s_add_u32 s46, s16, s52
	s_addc_u32 s47, s17, 0
	s_lshl_b32 s52, s6, 13
	s_mov_b32 m0, s52
	s_add_i32 s52, s52, 0x400
	global_load_lds_dwordx4 v211, s[46:47]
	s_mov_b32 m0, s52
	s_add_i32 s52, s52, 0x400
	global_load_lds_dwordx4 v212, s[46:47]
	s_mov_b32 m0, s52
	s_add_i32 s52, s52, 0x400
	global_load_lds_dwordx4 v213, s[46:47]
	s_mov_b32 m0, s52
	s_add_i32 s52, s52, 0x400
	global_load_lds_dwordx4 v214, s[46:47]
	s_mov_b32 m0, s52
	s_add_i32 s52, s52, 0x400
	global_load_lds_dwordx4 v215, s[46:47]
	s_mov_b32 m0, s52
	s_add_i32 s52, s52, 0x400
	global_load_lds_dwordx4 v216, s[46:47]
	s_mov_b32 m0, s52
	s_add_i32 s52, s52, 0x400
	global_load_lds_dwordx4 v217, s[46:47]
	s_mov_b32 m0, s52
	s_nop 0
	global_load_lds_dwordx4 v218, s[46:47]
	s_waitcnt vmcnt(0)
	s_barrier
	s_cmp_eq_u32 s13, 17
	s_cbranch_scc1 .Lmylru_nodma_5
	s_add_i32 s58, s13, 1
	s_cmp_lt_u32 s58, 2
	s_sub_i32 s50, 1, s58
	s_lshl_b32 s50, s50, 7
	s_lshl_b32 s51, s9, 8
	s_add_i32 s51, s51, 0x8000
	s_add_i32 s51, s51, s50
	s_sub_i32 s50, 17, s58
	s_lshl_b32 s50, s50, 7
	s_lshl_b32 s59, s9, 11
	s_add_i32 s59, s59, s50
	s_cmp_lt_u32 s58, 2
	s_cselect_b32 s59, s51, s59
	s_lshl_b32 s52, s59, 11
	s_add_u32 s46, s16, s52
	s_addc_u32 s47, s17, 0
	s_lshl_b32 s52, s6, 13
	s_add_i32 s52, s52, 0x10000
	s_mov_b32 m0, s52
	s_add_i32 s52, s52, 0x400
	global_load_lds_dwordx4 v211, s[46:47]
	s_mov_b32 m0, s52
	s_add_i32 s52, s52, 0x400
	global_load_lds_dwordx4 v212, s[46:47]
	s_mov_b32 m0, s52
	s_add_i32 s52, s52, 0x400
	global_load_lds_dwordx4 v213, s[46:47]
	s_mov_b32 m0, s52
	s_add_i32 s52, s52, 0x400
	global_load_lds_dwordx4 v214, s[46:47]
	s_mov_b32 m0, s52
	s_add_i32 s52, s52, 0x400
	global_load_lds_dwordx4 v215, s[46:47]
	s_mov_b32 m0, s52
	s_add_i32 s52, s52, 0x400
	global_load_lds_dwordx4 v216, s[46:47]
	s_mov_b32 m0, s52
	s_add_i32 s52, s52, 0x400
	global_load_lds_dwordx4 v217, s[46:47]
	s_mov_b32 m0, s52
	s_nop 0
	global_load_lds_dwordx4 v218, s[46:47]
.Lmylru_nodma_5:
	v_mov_b32_e32 v163, v162
	ds_read_b128 v[96:99], v163
	ds_read_b128 v[100:103], v163 offset:8192
	ds_read_b128 v[104:107], v163 offset:16384
	ds_read_b128 v[108:111], v163 offset:24576
	v_xor_b32_e32 v164, 0x40, v163
	ds_read_b128 v[112:115], v164
	ds_read_b128 v[116:119], v164 offset:8192
	ds_read_b128 v[120:123], v164 offset:16384
	ds_read_b128 v[124:127], v164 offset:24576
	s_waitcnt lgkmcnt(7)
	v_mfma_f32_16x16x32_bf16 v[64:67], v[96:99], v[0:3], 0
	v_mfma_f32_16x16x32_bf16 v[68:71], v[96:99], v[32:35], 0
	v_xor_b32_e32 v164, 0x80, v163
	ds_read_b128 v[96:99], v164
	s_waitcnt lgkmcnt(7)
	v_mfma_f32_16x16x32_bf16 v[72:75], v[100:103], v[0:3], 0
	v_mfma_f32_16x16x32_bf16 v[76:79], v[100:103], v[32:35], 0
	ds_read_b128 v[100:103], v164 offset:8192
	s_waitcnt lgkmcnt(7)
	v_mfma_f32_16x16x32_bf16 v[80:83], v[104:107], v[0:3], 0
	v_mfma_f32_16x16x32_bf16 v[84:87], v[104:107], v[32:35], 0
	ds_read_b128 v[104:107], v164 offset:16384
	s_waitcnt lgkmcnt(7)
	v_mfma_f32_16x16x32_bf16 v[88:91], v[108:111], v[0:3], 0
	v_mfma_f32_16x16x32_bf16 v[92:95], v[108:111], v[32:35], 0
	ds_read_b128 v[108:111], v164 offset:24576
	s_waitcnt lgkmcnt(7)
	v_mfma_f32_16x16x32_bf16 v[64:67], v[112:115], v[4:7], v[64:67]
	v_mfma_f32_16x16x32_bf16 v[68:71], v[112:115], v[36:39], v[68:71]
	v_xor_b32_e32 v164, 0xc0, v163
	ds_read_b128 v[112:115], v164
	s_waitcnt lgkmcnt(7)
	v_mfma_f32_16x16x32_bf16 v[72:75], v[116:119], v[4:7], v[72:75]
	v_mfma_f32_16x16x32_bf16 v[76:79], v[116:119], v[36:39], v[76:79]
	ds_read_b128 v[116:119], v164 offset:8192
	s_waitcnt lgkmcnt(7)
	v_mfma_f32_16x16x32_bf16 v[80:83], v[120:123], v[4:7], v[80:83]
	v_mfma_f32_16x16x32_bf16 v[84:87], v[120:123], v[36:39], v[84:87]
	ds_read_b128 v[120:123], v164 offset:16384
	s_waitcnt lgkmcnt(7)
	v_mfma_f32_16x16x32_bf16 v[88:91], v[124:127], v[4:7], v[88:91]
	v_mfma_f32_16x16x32_bf16 v[92:95], v[124:127], v[36:39], v[92:95]
	ds_read_b128 v[124:127], v164 offset:24576
	s_waitcnt lgkmcnt(7)
	v_mfma_f32_16x16x32_bf16 v[64:67], v[96:99], v[8:11], v[64:67]
	v_mfma_f32_16x16x32_bf16 v[68:71], v[96:99], v[40:43], v[68:71]
	v_xor_b32_e32 v164, 0x100, v163
	ds_read_b128 v[96:99], v164
	s_waitcnt lgkmcnt(7)
	v_mfma_f32_16x16x32_bf16 v[72:75], v[100:103], v[8:11], v[72:75]
	v_mfma_f32_16x16x32_bf16 v[76:79], v[100:103], v[40:43], v[76:79]
	ds_read_b128 v[100:103], v164 offset:8192
	s_waitcnt lgkmcnt(7)
	v_mfma_f32_16x16x32_bf16 v[80:83], v[104:107], v[8:11], v[80:83]
	v_mfma_f32_16x16x32_bf16 v[84:87], v[104:107], v[40:43], v[84:87]
	ds_read_b128 v[104:107], v164 offset:16384
	s_waitcnt lgkmcnt(7)
	v_mfma_f32_16x16x32_bf16 v[88:91], v[108:111], v[8:11], v[88:91]
	v_mfma_f32_16x16x32_bf16 v[92:95], v[108:111], v[40:43], v[92:95]
	ds_read_b128 v[108:111], v164 offset:24576
	s_waitcnt lgkmcnt(7)
	v_mfma_f32_16x16x32_bf16 v[64:67], v[112:115], v[12:15], v[64:67]
	v_mfma_f32_16x16x32_bf16 v[68:71], v[112:115], v[44:47], v[68:71]
	v_xor_b32_e32 v164, 0x140, v163
	ds_read_b128 v[112:115], v164
	s_waitcnt lgkmcnt(7)
	v_mfma_f32_16x16x32_bf16 v[72:75], v[116:119], v[12:15], v[72:75]
	v_mfma_f32_16x16x32_bf16 v[76:79], v[116:119], v[44:47], v[76:79]
	ds_read_b128 v[116:119], v164 offset:8192
	s_waitcnt lgkmcnt(7)
	v_mfma_f32_16x16x32_bf16 v[80:83], v[120:123], v[12:15], v[80:83]
	v_mfma_f32_16x16x32_bf16 v[84:87], v[120:123], v[44:47], v[84:87]
	ds_read_b128 v[120:123], v164 offset:16384
	s_waitcnt lgkmcnt(7)
	v_mfma_f32_16x16x32_bf16 v[88:91], v[124:127], v[12:15], v[88:91]
	v_mfma_f32_16x16x32_bf16 v[92:95], v[124:127], v[44:47], v[92:95]
	ds_read_b128 v[124:127], v164 offset:24576
	s_waitcnt lgkmcnt(7)
	v_mfma_f32_16x16x32_bf16 v[64:67], v[96:99], v[16:19], v[64:67]
	v_mfma_f32_16x16x32_bf16 v[68:71], v[96:99], v[48:51], v[68:71]
	v_xor_b32_e32 v164, 0x180, v163
	ds_read_b128 v[96:99], v164
	s_waitcnt lgkmcnt(7)
	v_mfma_f32_16x16x32_bf16 v[72:75], v[100:103], v[16:19], v[72:75]
	v_mfma_f32_16x16x32_bf16 v[76:79], v[100:103], v[48:51], v[76:79]
	ds_read_b128 v[100:103], v164 offset:8192
	s_waitcnt lgkmcnt(7)
	v_mfma_f32_16x16x32_bf16 v[80:83], v[104:107], v[16:19], v[80:83]
	v_mfma_f32_16x16x32_bf16 v[84:87], v[104:107], v[48:51], v[84:87]
	ds_read_b128 v[104:107], v164 offset:16384
	s_waitcnt lgkmcnt(7)
	v_mfma_f32_16x16x32_bf16 v[88:91], v[108:111], v[16:19], v[88:91]
	v_mfma_f32_16x16x32_bf16 v[92:95], v[108:111], v[48:51], v[92:95]
	ds_read_b128 v[108:111], v164 offset:24576
	s_waitcnt lgkmcnt(7)
	v_mfma_f32_16x16x32_bf16 v[64:67], v[112:115], v[20:23], v[64:67]
	v_mfma_f32_16x16x32_bf16 v[68:71], v[112:115], v[52:55], v[68:71]
	v_xor_b32_e32 v164, 0x1c0, v163
	ds_read_b128 v[112:115], v164
	s_waitcnt lgkmcnt(7)
	v_mfma_f32_16x16x32_bf16 v[72:75], v[116:119], v[20:23], v[72:75]
	v_mfma_f32_16x16x32_bf16 v[76:79], v[116:119], v[52:55], v[76:79]
	ds_read_b128 v[116:119], v164 offset:8192
	s_waitcnt lgkmcnt(7)
	v_mfma_f32_16x16x32_bf16 v[80:83], v[120:123], v[20:23], v[80:83]
	v_mfma_f32_16x16x32_bf16 v[84:87], v[120:123], v[52:55], v[84:87]
	ds_read_b128 v[120:123], v164 offset:16384
	s_waitcnt lgkmcnt(7)
	v_mfma_f32_16x16x32_bf16 v[88:91], v[124:127], v[20:23], v[88:91]
	v_mfma_f32_16x16x32_bf16 v[92:95], v[124:127], v[52:55], v[92:95]
	ds_read_b128 v[124:127], v164 offset:24576
	s_waitcnt lgkmcnt(7)
	v_mfma_f32_16x16x32_bf16 v[64:67], v[96:99], v[24:27], v[64:67]
	v_mfma_f32_16x16x32_bf16 v[68:71], v[96:99], v[56:59], v[68:71]
	s_waitcnt lgkmcnt(6)
	v_mfma_f32_16x16x32_bf16 v[72:75], v[100:103], v[24:27], v[72:75]
	v_mfma_f32_16x16x32_bf16 v[76:79], v[100:103], v[56:59], v[76:79]
	s_waitcnt lgkmcnt(5)
	v_mfma_f32_16x16x32_bf16 v[80:83], v[104:107], v[24:27], v[80:83]
	v_mfma_f32_16x16x32_bf16 v[84:87], v[104:107], v[56:59], v[84:87]
	s_waitcnt lgkmcnt(4)
	v_mfma_f32_16x16x32_bf16 v[88:91], v[108:111], v[24:27], v[88:91]
	v_mfma_f32_16x16x32_bf16 v[92:95], v[108:111], v[56:59], v[92:95]
	s_waitcnt lgkmcnt(3)
	v_mfma_f32_16x16x32_bf16 v[64:67], v[112:115], v[28:31], v[64:67]
	v_mfma_f32_16x16x32_bf16 v[68:71], v[112:115], v[60:63], v[68:71]
	s_waitcnt lgkmcnt(2)
	v_mfma_f32_16x16x32_bf16 v[72:75], v[116:119], v[28:31], v[72:75]
	v_mfma_f32_16x16x32_bf16 v[76:79], v[116:119], v[60:63], v[76:79]
	s_waitcnt lgkmcnt(1)
	v_mfma_f32_16x16x32_bf16 v[80:83], v[120:123], v[28:31], v[80:83]
	v_mfma_f32_16x16x32_bf16 v[84:87], v[120:123], v[60:63], v[84:87]
	s_waitcnt lgkmcnt(0)
	v_mfma_f32_16x16x32_bf16 v[88:91], v[124:127], v[28:31], v[88:91]
	v_mfma_f32_16x16x32_bf16 v[92:95], v[124:127], v[60:63], v[92:95]
	v_mov_b32_e32 v198, v165
	v_mov_b32_e32 v199, v166
	v_mov_b32_e32 v200, v167
	v_mov_b32_e32 v201, v168
	ds_read_u16 v144, v198
	ds_read_u16 v145, v199
	ds_read_u16 v146, v200
	ds_read_u16 v147, v201
	ds_read_u16 v148, v198 offset:8192
	ds_read_u16 v149, v199 offset:8192
	ds_read_u16 v150, v200 offset:8192
	ds_read_u16 v151, v201 offset:8192
	ds_read_u16 v152, v198 offset:16384
	ds_read_u16 v153, v199 offset:16384
	ds_read_u16 v154, v200 offset:16384
	ds_read_u16 v155, v201 offset:16384
	ds_read_u16 v156, v198 offset:24576
	ds_read_u16 v157, v199 offset:24576
	ds_read_u16 v158, v200 offset:24576
	ds_read_u16 v159, v201 offset:24576
	s_nop 7
	v_fma_f32 v178, v64, s53, v173
	v_fma_f32 v179, v65, s53, v173
	v_fma_f32 v180, v66, s53, v173
	v_fma_f32 v181, v67, s53, v173
	v_fma_f32 v182, v72, s53, v173
	v_fma_f32 v183, v73, s53, v173
	v_fma_f32 v184, v74, s53, v173
	v_fma_f32 v185, v75, s53, v173
	v_fma_f32 v186, v68, s53, v174
	v_fma_f32 v187, v69, s53, v174
	v_fma_f32 v188, v70, s53, v174
	v_fma_f32 v189, v71, s53, v174
	v_fma_f32 v190, v76, s53, v174
	v_fma_f32 v191, v77, s53, v174
	v_fma_f32 v192, v78, s53, v174
	v_fma_f32 v193, v79, s53, v174
	v_exp_f32_e32 v178, v178
	v_exp_f32_e32 v179, v179
	v_exp_f32_e32 v180, v180
	v_exp_f32_e32 v181, v181
	v_exp_f32_e32 v182, v182
	v_exp_f32_e32 v183, v183
	v_exp_f32_e32 v184, v184
	v_exp_f32_e32 v185, v185
	v_exp_f32_e32 v186, v186
	v_exp_f32_e32 v187, v187
	v_exp_f32_e32 v188, v188
	v_exp_f32_e32 v189, v189
	v_exp_f32_e32 v190, v190
	v_exp_f32_e32 v191, v191
	v_exp_f32_e32 v192, v192
	v_exp_f32_e32 v193, v193
	v_add_f32_e32 v178, 1.0, v178
	v_add_f32_e32 v179, 1.0, v179
	v_add_f32_e32 v180, 1.0, v180
	v_add_f32_e32 v181, 1.0, v181
	v_add_f32_e32 v182, 1.0, v182
	v_add_f32_e32 v183, 1.0, v183
	v_add_f32_e32 v184, 1.0, v184
	v_add_f32_e32 v185, 1.0, v185
	v_add_f32_e32 v186, 1.0, v186
	v_add_f32_e32 v187, 1.0, v187
	v_add_f32_e32 v188, 1.0, v188
	v_add_f32_e32 v189, 1.0, v189
	v_add_f32_e32 v190, 1.0, v190
	v_add_f32_e32 v191, 1.0, v191
	v_add_f32_e32 v192, 1.0, v192
	v_add_f32_e32 v193, 1.0, v193
	v_rcp_f32_e32 v178, v178
	v_rcp_f32_e32 v179, v179
	v_rcp_f32_e32 v180, v180
	v_rcp_f32_e32 v181, v181
	v_rcp_f32_e32 v182, v182
	v_rcp_f32_e32 v183, v183
	v_rcp_f32_e32 v184, v184
	v_rcp_f32_e32 v185, v185
	v_rcp_f32_e32 v186, v186
	v_rcp_f32_e32 v187, v187
	v_rcp_f32_e32 v188, v188
	v_rcp_f32_e32 v189, v189
	v_rcp_f32_e32 v190, v190
	v_rcp_f32_e32 v191, v191
	v_rcp_f32_e32 v192, v192
	v_rcp_f32_e32 v193, v193
	v_mul_f32_e32 v178, v175, v178
	v_mul_f32_e32 v179, v175, v179
	v_mul_f32_e32 v180, v175, v180
	v_mul_f32_e32 v181, v175, v181
	v_mul_f32_e32 v182, v175, v182
	v_mul_f32_e32 v183, v175, v183
	v_mul_f32_e32 v184, v175, v184
	v_mul_f32_e32 v185, v175, v185
	v_exp_f32_e32 v96, v178
	v_exp_f32_e32 v97, v179
	v_exp_f32_e32 v98, v180
	v_exp_f32_e32 v99, v181
	v_exp_f32_e32 v100, v182
	v_exp_f32_e32 v101, v183
	v_exp_f32_e32 v102, v184
	v_exp_f32_e32 v103, v185
	s_nop 0
	v_fma_f32 v194, -v96, v96, 1.0
	v_fma_f32 v195, -v97, v97, 1.0
	v_fma_f32 v196, -v98, v98, 1.0
	v_fma_f32 v197, -v99, v99, 1.0
	v_fma_f32 v198, -v100, v100, 1.0
	v_fma_f32 v199, -v101, v101, 1.0
	v_fma_f32 v200, -v102, v102, 1.0
	v_fma_f32 v201, -v103, v103, 1.0
	v_max_f32_e32 v194, 0, v194
	v_max_f32_e32 v195, 0, v195
	v_max_f32_e32 v196, 0, v196
	v_max_f32_e32 v197, 0, v197
	v_max_f32_e32 v198, 0, v198
	v_max_f32_e32 v199, 0, v199
	v_max_f32_e32 v200, 0, v200
	v_max_f32_e32 v201, 0, v201
	v_sqrt_f32_e32 v194, v194
	v_sqrt_f32_e32 v195, v195
	v_sqrt_f32_e32 v196, v196
	v_sqrt_f32_e32 v197, v197
	v_sqrt_f32_e32 v198, v198
	v_sqrt_f32_e32 v199, v199
	v_sqrt_f32_e32 v200, v200
	v_sqrt_f32_e32 v201, v201
	s_waitcnt lgkmcnt(8)
	v_lshlrev_b32_e32 v144, 16, v144
	v_lshlrev_b32_e32 v145, 16, v145
	v_lshlrev_b32_e32 v146, 16, v146
	v_lshlrev_b32_e32 v147, 16, v147
	v_lshlrev_b32_e32 v148, 16, v148
	v_lshlrev_b32_e32 v149, 16, v149
	v_lshlrev_b32_e32 v150, 16, v150
	v_lshlrev_b32_e32 v151, 16, v151
	v_mul_f32_e32 v194, v194, v186
	v_mul_f32_e32 v195, v195, v187
	v_mul_f32_e32 v196, v196, v188
	v_mul_f32_e32 v197, v197, v189
	v_mul_f32_e32 v198, v198, v190
	v_mul_f32_e32 v199, v199, v191
	v_mul_f32_e32 v200, v200, v192
	v_mul_f32_e32 v201, v201, v193
	v_mul_f32_e32 v144, v194, v144
	v_mul_f32_e32 v145, v195, v145
	v_mul_f32_e32 v146, v196, v146
	v_mul_f32_e32 v147, v197, v147
	v_mul_f32_e32 v148, v198, v148
	v_mul_f32_e32 v149, v199, v149
	v_mul_f32_e32 v150, v200, v150
	v_mul_f32_e32 v151, v201, v151
	v_fma_f32 v178, v80, s53, v173
	v_fma_f32 v179, v81, s53, v173
	v_fma_f32 v180, v82, s53, v173
	v_fma_f32 v181, v83, s53, v173
	v_fma_f32 v182, v88, s53, v173
	v_fma_f32 v183, v89, s53, v173
	v_fma_f32 v184, v90, s53, v173
	v_fma_f32 v185, v91, s53, v173
	v_fma_f32 v186, v84, s53, v174
	v_fma_f32 v187, v85, s53, v174
	v_fma_f32 v188, v86, s53, v174
	v_fma_f32 v189, v87, s53, v174
	v_fma_f32 v190, v92, s53, v174
	v_fma_f32 v191, v93, s53, v174
	v_fma_f32 v192, v94, s53, v174
	v_fma_f32 v193, v95, s53, v174
	v_exp_f32_e32 v178, v178
	v_exp_f32_e32 v179, v179
	v_exp_f32_e32 v180, v180
	v_exp_f32_e32 v181, v181
	v_exp_f32_e32 v182, v182
	v_exp_f32_e32 v183, v183
	v_exp_f32_e32 v184, v184
	v_exp_f32_e32 v185, v185
	v_exp_f32_e32 v186, v186
	v_exp_f32_e32 v187, v187
	v_exp_f32_e32 v188, v188
	v_exp_f32_e32 v189, v189
	v_exp_f32_e32 v190, v190
	v_exp_f32_e32 v191, v191
	v_exp_f32_e32 v192, v192
	v_exp_f32_e32 v193, v193
	v_add_f32_e32 v178, 1.0, v178
	v_add_f32_e32 v179, 1.0, v179
	v_add_f32_e32 v180, 1.0, v180
	v_add_f32_e32 v181, 1.0, v181
	v_add_f32_e32 v182, 1.0, v182
	v_add_f32_e32 v183, 1.0, v183
	v_add_f32_e32 v184, 1.0, v184
	v_add_f32_e32 v185, 1.0, v185
	v_add_f32_e32 v186, 1.0, v186
	v_add_f32_e32 v187, 1.0, v187
	v_add_f32_e32 v188, 1.0, v188
	v_add_f32_e32 v189, 1.0, v189
	v_add_f32_e32 v190, 1.0, v190
	v_add_f32_e32 v191, 1.0, v191
	v_add_f32_e32 v192, 1.0, v192
	v_add_f32_e32 v193, 1.0, v193
	v_rcp_f32_e32 v178, v178
	v_rcp_f32_e32 v179, v179
	v_rcp_f32_e32 v180, v180
	v_rcp_f32_e32 v181, v181
	v_rcp_f32_e32 v182, v182
	v_rcp_f32_e32 v183, v183
	v_rcp_f32_e32 v184, v184
	v_rcp_f32_e32 v185, v185
	v_rcp_f32_e32 v186, v186
	v_rcp_f32_e32 v187, v187
	v_rcp_f32_e32 v188, v188
	v_rcp_f32_e32 v189, v189
	v_rcp_f32_e32 v190, v190
	v_rcp_f32_e32 v191, v191
	v_rcp_f32_e32 v192, v192
	v_rcp_f32_e32 v193, v193
	v_mul_f32_e32 v178, v175, v178
	v_mul_f32_e32 v179, v175, v179
	v_mul_f32_e32 v180, v175, v180
	v_mul_f32_e32 v181, v175, v181
	v_mul_f32_e32 v182, v175, v182
	v_mul_f32_e32 v183, v175, v183
	v_mul_f32_e32 v184, v175, v184
	v_mul_f32_e32 v185, v175, v185
	v_exp_f32_e32 v104, v178
	v_exp_f32_e32 v105, v179
	v_exp_f32_e32 v106, v180
	v_exp_f32_e32 v107, v181
	v_exp_f32_e32 v108, v182
	v_exp_f32_e32 v109, v183
	v_exp_f32_e32 v110, v184
	v_exp_f32_e32 v111, v185
	s_nop 0
	v_fma_f32 v194, -v104, v104, 1.0
	v_fma_f32 v195, -v105, v105, 1.0
	v_fma_f32 v196, -v106, v106, 1.0
	v_fma_f32 v197, -v107, v107, 1.0
	v_fma_f32 v198, -v108, v108, 1.0
	v_fma_f32 v199, -v109, v109, 1.0
	v_fma_f32 v200, -v110, v110, 1.0
	v_fma_f32 v201, -v111, v111, 1.0
	v_max_f32_e32 v194, 0, v194
	v_max_f32_e32 v195, 0, v195
	v_max_f32_e32 v196, 0, v196
	v_max_f32_e32 v197, 0, v197
	v_max_f32_e32 v198, 0, v198
	v_max_f32_e32 v199, 0, v199
	v_max_f32_e32 v200, 0, v200
	v_max_f32_e32 v201, 0, v201
	v_sqrt_f32_e32 v194, v194
	v_sqrt_f32_e32 v195, v195
	v_sqrt_f32_e32 v196, v196
	v_sqrt_f32_e32 v197, v197
	v_sqrt_f32_e32 v198, v198
	v_sqrt_f32_e32 v199, v199
	v_sqrt_f32_e32 v200, v200
	v_sqrt_f32_e32 v201, v201
	s_waitcnt lgkmcnt(0)
	v_lshlrev_b32_e32 v152, 16, v152
	v_lshlrev_b32_e32 v153, 16, v153
	v_lshlrev_b32_e32 v154, 16, v154
	v_lshlrev_b32_e32 v155, 16, v155
	v_lshlrev_b32_e32 v156, 16, v156
	v_lshlrev_b32_e32 v157, 16, v157
	v_lshlrev_b32_e32 v158, 16, v158
	v_lshlrev_b32_e32 v159, 16, v159
	v_mul_f32_e32 v194, v194, v186
	v_mul_f32_e32 v195, v195, v187
	v_mul_f32_e32 v196, v196, v188
	v_mul_f32_e32 v197, v197, v189
	v_mul_f32_e32 v198, v198, v190
	v_mul_f32_e32 v199, v199, v191
	v_mul_f32_e32 v200, v200, v192
	v_mul_f32_e32 v201, v201, v193
	v_mul_f32_e32 v152, v194, v152
	v_mul_f32_e32 v153, v195, v153
	v_mul_f32_e32 v154, v196, v154
	v_mul_f32_e32 v155, v197, v155
	v_mul_f32_e32 v156, v198, v156
	v_mul_f32_e32 v157, v199, v157
	v_mul_f32_e32 v158, v200, v158
	v_mul_f32_e32 v159, v201, v159
	v_fma_f32 v146, v98, v147, v146
	v_fma_f32 v150, v102, v151, v150
	v_fma_f32 v154, v106, v155, v154
	v_fma_f32 v158, v110, v159, v158
	v_mul_f32_e32 v98, v98, v99
	v_mul_f32_e32 v102, v102, v103
	v_mul_f32_e32 v106, v106, v107
	v_mul_f32_e32 v110, v110, v111
	v_fma_f32 v145, v97, v146, v145
	v_fma_f32 v149, v101, v150, v149
	v_fma_f32 v153, v105, v154, v153
	v_fma_f32 v157, v109, v158, v157
	v_mul_f32_e32 v97, v97, v98
	v_mul_f32_e32 v101, v101, v102
	v_mul_f32_e32 v105, v105, v106
	v_mul_f32_e32 v109, v109, v110
	v_fma_f32 v144, v96, v145, v144
	v_fma_f32 v148, v100, v149, v148
	v_fma_f32 v152, v104, v153, v152
	v_fma_f32 v156, v108, v157, v156
	v_mul_f32_e32 v96, v96, v97
	v_mul_f32_e32 v100, v100, v101
	v_mul_f32_e32 v104, v104, v105
	v_mul_f32_e32 v108, v108, v109
	ds_bpermute_b32 v178, v204, v96
	ds_bpermute_b32 v182, v204, v144
	ds_bpermute_b32 v179, v204, v100
	ds_bpermute_b32 v183, v204, v148
	ds_bpermute_b32 v180, v204, v104
	ds_bpermute_b32 v184, v204, v152
	ds_bpermute_b32 v181, v204, v108
	ds_bpermute_b32 v185, v204, v156
	s_waitcnt lgkmcnt(0)
	v_fma_f32 v186, v182, v96, v144
	v_cndmask_b32_e64 v178, 1.0, v178, s[34:35]
	v_fma_f32 v187, v183, v100, v148
	v_cndmask_b32_e64 v179, 1.0, v179, s[34:35]
	v_fma_f32 v188, v184, v104, v152
	v_cndmask_b32_e64 v180, 1.0, v180, s[34:35]
	v_fma_f32 v189, v185, v108, v156
	v_cndmask_b32_e64 v181, 1.0, v181, s[34:35]
	v_cndmask_b32_e64 v223, v144, v186, s[34:35]
	v_mul_f32_e32 v219, v96, v178
	v_cndmask_b32_e64 v224, v148, v187, s[34:35]
	v_mul_f32_e32 v220, v100, v179
	v_cndmask_b32_e64 v225, v152, v188, s[34:35]
	v_mul_f32_e32 v221, v104, v180
	v_cndmask_b32_e64 v226, v156, v189, s[34:35]
	v_mul_f32_e32 v222, v108, v181
	ds_bpermute_b32 v178, v205, v219
	ds_bpermute_b32 v182, v205, v223
	ds_bpermute_b32 v179, v205, v220
	ds_bpermute_b32 v183, v205, v224
	ds_bpermute_b32 v180, v205, v221
	ds_bpermute_b32 v184, v205, v225
	ds_bpermute_b32 v181, v205, v222
	ds_bpermute_b32 v185, v205, v226
	s_waitcnt lgkmcnt(0)
	v_fma_f32 v186, v182, v219, v223
	v_cndmask_b32_e64 v178, 1.0, v178, s[36:37]
	v_fma_f32 v187, v183, v220, v224
	v_cndmask_b32_e64 v179, 1.0, v179, s[36:37]
	v_fma_f32 v188, v184, v221, v225
	v_cndmask_b32_e64 v180, 1.0, v180, s[36:37]
	v_fma_f32 v189, v185, v222, v226
	v_cndmask_b32_e64 v181, 1.0, v181, s[36:37]
	v_cndmask_b32_e64 v223, v223, v186, s[36:37]
	v_mul_f32_e32 v219, v219, v178
	v_cndmask_b32_e64 v224, v224, v187, s[36:37]
	v_mul_f32_e32 v220, v220, v179
	v_cndmask_b32_e64 v225, v225, v188, s[36:37]
	v_mul_f32_e32 v221, v221, v180
	v_cndmask_b32_e64 v226, v226, v189, s[36:37]
	v_mul_f32_e32 v222, v222, v181
	ds_bpermute_b32 v227, v204, v219
	ds_bpermute_b32 v231, v204, v223
	ds_bpermute_b32 v235, v206, v219
	ds_bpermute_b32 v239, v206, v223
	ds_bpermute_b32 v228, v204, v220
	ds_bpermute_b32 v232, v204, v224
	ds_bpermute_b32 v236, v206, v220
	ds_bpermute_b32 v244, v206, v224
	ds_bpermute_b32 v229, v204, v221
	ds_bpermute_b32 v233, v204, v225
	ds_bpermute_b32 v237, v206, v221
	ds_bpermute_b32 v245, v206, v225
	ds_bpermute_b32 v230, v204, v222
	ds_bpermute_b32 v234, v204, v226
	ds_bpermute_b32 v238, v206, v222
	ds_bpermute_b32 v246, v206, v226
	s_waitcnt lgkmcnt(0)
	v_cndmask_b32_e64 v227, 1.0, v227, s[34:35]
	v_cndmask_b32_e64 v231, 0, v231, s[34:35]
	v_cndmask_b32_e64 v228, 1.0, v228, s[34:35]
	v_cndmask_b32_e64 v232, 0, v232, s[34:35]
	v_cndmask_b32_e64 v229, 1.0, v229, s[34:35]
	v_cndmask_b32_e64 v233, 0, v233, s[34:35]
	v_cndmask_b32_e64 v230, 1.0, v230, s[34:35]
	v_cndmask_b32_e64 v234, 0, v234, s[34:35]
	v_mov_b32_e32 v190, v238
	v_mov_b32_e32 v194, v246
	v_mov_b32_e32 v198, v190
	v_mov_b32_e32 v201, v194
	v_fma_f32 v194, v194, v237, v245
	v_mul_f32_e32 v190, v190, v237
	v_mov_b32_e32 v199, v190
	v_mov_b32_e32 v177, v194
	v_fma_f32 v194, v194, v236, v244
	v_mul_f32_e32 v190, v190, v236
	v_mov_b32_e32 v200, v190
	v_mov_b32_e32 v203, v194
	v_fma_f32 v194, v194, v235, v239
	v_mul_f32_e32 v190, v190, v235
	v_mov_b32_e32 v191, v194
	ds_write_b64 v207, v[190:191]
	s_waitcnt lgkmcnt(0)
	s_barrier
	ds_read_b64 v[178:179], v208 offset:512
	ds_read_b64 v[180:181], v208
	s_waitcnt lgkmcnt(0)
	v_fma_f32 v182, v176, v178, v179
	v_cndmask_b32_e64 v183, v176, v182, s[38:39]
	v_fma_f32 v176, v182, v180, v181
	s_add_i32 s13, s13, 1
	s_waitcnt vmcnt(0)
	s_barrier
	s_cmp_eq_u32 s13, 17
	s_cbranch_scc1 .Lmylru_nodma_6
	s_add_i32 s58, s13, 1
	s_cmp_lt_u32 s58, 2
	s_sub_i32 s50, 1, s58
	s_lshl_b32 s50, s50, 7
	s_lshl_b32 s51, s9, 8
	s_add_i32 s51, s51, 0x8000
	s_add_i32 s51, s51, s50
	s_sub_i32 s50, 17, s58
	s_lshl_b32 s50, s50, 7
	s_lshl_b32 s59, s9, 11
	s_add_i32 s59, s59, s50
	s_cmp_lt_u32 s58, 2
	s_cselect_b32 s59, s51, s59
	s_lshl_b32 s52, s59, 11
	s_add_u32 s46, s16, s52
	s_addc_u32 s47, s17, 0
	s_lshl_b32 s52, s6, 13
	s_mov_b32 m0, s52
	s_add_i32 s52, s52, 0x400
	global_load_lds_dwordx4 v211, s[46:47]
	s_mov_b32 m0, s52
	s_add_i32 s52, s52, 0x400
	global_load_lds_dwordx4 v212, s[46:47]
	s_mov_b32 m0, s52
	s_add_i32 s52, s52, 0x400
	global_load_lds_dwordx4 v213, s[46:47]
	s_mov_b32 m0, s52
	s_add_i32 s52, s52, 0x400
	global_load_lds_dwordx4 v214, s[46:47]
	s_mov_b32 m0, s52
	s_add_i32 s52, s52, 0x400
	global_load_lds_dwordx4 v215, s[46:47]
	s_mov_b32 m0, s52
	s_add_i32 s52, s52, 0x400
	global_load_lds_dwordx4 v216, s[46:47]
	s_mov_b32 m0, s52
	s_add_i32 s52, s52, 0x400
	global_load_lds_dwordx4 v217, s[46:47]
	s_mov_b32 m0, s52
	s_nop 0
	global_load_lds_dwordx4 v218, s[46:47]
.Lmylru_nodma_6:
	v_or_b32_e32 v163, 0x10000, v162
	ds_read_b128 v[96:99], v163
	ds_read_b128 v[100:103], v163 offset:8192
	ds_read_b128 v[104:107], v163 offset:16384
	ds_read_b128 v[108:111], v163 offset:24576
	v_xor_b32_e32 v164, 0x40, v163
	ds_read_b128 v[112:115], v164
	ds_read_b128 v[116:119], v164 offset:8192
	ds_read_b128 v[120:123], v164 offset:16384
	ds_read_b128 v[124:127], v164 offset:24576
	s_waitcnt lgkmcnt(7)
	v_mfma_f32_16x16x32_bf16 v[64:67], v[96:99], v[0:3], 0
	v_mfma_f32_16x16x32_bf16 v[68:71], v[96:99], v[32:35], 0
	v_xor_b32_e32 v164, 0x80, v163
	ds_read_b128 v[96:99], v164
	s_waitcnt lgkmcnt(7)
	v_mfma_f32_16x16x32_bf16 v[72:75], v[100:103], v[0:3], 0
	v_mfma_f32_16x16x32_bf16 v[76:79], v[100:103], v[32:35], 0
	ds_read_b128 v[100:103], v164 offset:8192
	s_waitcnt lgkmcnt(7)
	v_mfma_f32_16x16x32_bf16 v[80:83], v[104:107], v[0:3], 0
	v_mfma_f32_16x16x32_bf16 v[84:87], v[104:107], v[32:35], 0
	ds_read_b128 v[104:107], v164 offset:16384
	s_waitcnt lgkmcnt(7)
	v_mfma_f32_16x16x32_bf16 v[88:91], v[108:111], v[0:3], 0
	v_mfma_f32_16x16x32_bf16 v[92:95], v[108:111], v[32:35], 0
	ds_read_b128 v[108:111], v164 offset:24576
	s_waitcnt lgkmcnt(7)
	v_mfma_f32_16x16x32_bf16 v[64:67], v[112:115], v[4:7], v[64:67]
	v_mfma_f32_16x16x32_bf16 v[68:71], v[112:115], v[36:39], v[68:71]
	v_xor_b32_e32 v164, 0xc0, v163
	ds_read_b128 v[112:115], v164
	s_waitcnt lgkmcnt(7)
	v_mfma_f32_16x16x32_bf16 v[72:75], v[116:119], v[4:7], v[72:75]
	v_mfma_f32_16x16x32_bf16 v[76:79], v[116:119], v[36:39], v[76:79]
	ds_read_b128 v[116:119], v164 offset:8192
	s_waitcnt lgkmcnt(7)
	v_mfma_f32_16x16x32_bf16 v[80:83], v[120:123], v[4:7], v[80:83]
	v_mfma_f32_16x16x32_bf16 v[84:87], v[120:123], v[36:39], v[84:87]
	ds_read_b128 v[120:123], v164 offset:16384
	s_waitcnt lgkmcnt(7)
	v_mfma_f32_16x16x32_bf16 v[88:91], v[124:127], v[4:7], v[88:91]
	v_mfma_f32_16x16x32_bf16 v[92:95], v[124:127], v[36:39], v[92:95]
	ds_read_b128 v[124:127], v164 offset:24576
	s_waitcnt lgkmcnt(7)
	v_mfma_f32_16x16x32_bf16 v[64:67], v[96:99], v[8:11], v[64:67]
	v_mfma_f32_16x16x32_bf16 v[68:71], v[96:99], v[40:43], v[68:71]
	v_xor_b32_e32 v164, 0x100, v163
	ds_read_b128 v[96:99], v164
	s_waitcnt lgkmcnt(7)
	v_mfma_f32_16x16x32_bf16 v[72:75], v[100:103], v[8:11], v[72:75]
	v_mfma_f32_16x16x32_bf16 v[76:79], v[100:103], v[40:43], v[76:79]
	ds_read_b128 v[100:103], v164 offset:8192
	s_waitcnt lgkmcnt(7)
	v_mfma_f32_16x16x32_bf16 v[80:83], v[104:107], v[8:11], v[80:83]
	v_mfma_f32_16x16x32_bf16 v[84:87], v[104:107], v[40:43], v[84:87]
	ds_read_b128 v[104:107], v164 offset:16384
	s_waitcnt lgkmcnt(7)
	v_mfma_f32_16x16x32_bf16 v[88:91], v[108:111], v[8:11], v[88:91]
	v_mfma_f32_16x16x32_bf16 v[92:95], v[108:111], v[40:43], v[92:95]
	ds_read_b128 v[108:111], v164 offset:24576
	s_waitcnt lgkmcnt(7)
	v_mfma_f32_16x16x32_bf16 v[64:67], v[112:115], v[12:15], v[64:67]
	v_mfma_f32_16x16x32_bf16 v[68:71], v[112:115], v[44:47], v[68:71]
	v_xor_b32_e32 v164, 0x140, v163
	ds_read_b128 v[112:115], v164
	s_waitcnt lgkmcnt(7)
	v_mfma_f32_16x16x32_bf16 v[72:75], v[116:119], v[12:15], v[72:75]
	v_mfma_f32_16x16x32_bf16 v[76:79], v[116:119], v[44:47], v[76:79]
	ds_read_b128 v[116:119], v164 offset:8192
	s_waitcnt lgkmcnt(7)
	v_mfma_f32_16x16x32_bf16 v[80:83], v[120:123], v[12:15], v[80:83]
	v_mfma_f32_16x16x32_bf16 v[84:87], v[120:123], v[44:47], v[84:87]
	ds_read_b128 v[120:123], v164 offset:16384
	s_waitcnt lgkmcnt(7)
	v_mfma_f32_16x16x32_bf16 v[88:91], v[124:127], v[12:15], v[88:91]
	v_mfma_f32_16x16x32_bf16 v[92:95], v[124:127], v[44:47], v[92:95]
	ds_read_b128 v[124:127], v164 offset:24576
	s_waitcnt lgkmcnt(7)
	v_mfma_f32_16x16x32_bf16 v[64:67], v[96:99], v[16:19], v[64:67]
	v_mfma_f32_16x16x32_bf16 v[68:71], v[96:99], v[48:51], v[68:71]
	v_xor_b32_e32 v164, 0x180, v163
	ds_read_b128 v[96:99], v164
	s_waitcnt lgkmcnt(7)
	v_mfma_f32_16x16x32_bf16 v[72:75], v[100:103], v[16:19], v[72:75]
	v_mfma_f32_16x16x32_bf16 v[76:79], v[100:103], v[48:51], v[76:79]
	ds_read_b128 v[100:103], v164 offset:8192
	s_waitcnt lgkmcnt(7)
	v_mfma_f32_16x16x32_bf16 v[80:83], v[104:107], v[16:19], v[80:83]
	v_mfma_f32_16x16x32_bf16 v[84:87], v[104:107], v[48:51], v[84:87]
	ds_read_b128 v[104:107], v164 offset:16384
	s_waitcnt lgkmcnt(7)
	v_mfma_f32_16x16x32_bf16 v[88:91], v[108:111], v[16:19], v[88:91]
	v_mfma_f32_16x16x32_bf16 v[92:95], v[108:111], v[48:51], v[92:95]
	ds_read_b128 v[108:111], v164 offset:24576
	s_waitcnt lgkmcnt(7)
	v_mfma_f32_16x16x32_bf16 v[64:67], v[112:115], v[20:23], v[64:67]
	v_mfma_f32_16x16x32_bf16 v[68:71], v[112:115], v[52:55], v[68:71]
	v_xor_b32_e32 v164, 0x1c0, v163
	ds_read_b128 v[112:115], v164
	s_waitcnt lgkmcnt(7)
	v_mfma_f32_16x16x32_bf16 v[72:75], v[116:119], v[20:23], v[72:75]
	v_mfma_f32_16x16x32_bf16 v[76:79], v[116:119], v[52:55], v[76:79]
	ds_read_b128 v[116:119], v164 offset:8192
	s_waitcnt lgkmcnt(7)
	v_mfma_f32_16x16x32_bf16 v[80:83], v[120:123], v[20:23], v[80:83]
	v_mfma_f32_16x16x32_bf16 v[84:87], v[120:123], v[52:55], v[84:87]
	ds_read_b128 v[120:123], v164 offset:16384
	s_waitcnt lgkmcnt(7)
	v_mfma_f32_16x16x32_bf16 v[88:91], v[124:127], v[20:23], v[88:91]
	v_mfma_f32_16x16x32_bf16 v[92:95], v[124:127], v[52:55], v[92:95]
	ds_read_b128 v[124:127], v164 offset:24576
	s_waitcnt lgkmcnt(7)
	v_mfma_f32_16x16x32_bf16 v[64:67], v[96:99], v[24:27], v[64:67]
	v_mfma_f32_16x16x32_bf16 v[68:71], v[96:99], v[56:59], v[68:71]
	s_waitcnt lgkmcnt(6)
	v_mfma_f32_16x16x32_bf16 v[72:75], v[100:103], v[24:27], v[72:75]
	v_mfma_f32_16x16x32_bf16 v[76:79], v[100:103], v[56:59], v[76:79]
	s_waitcnt lgkmcnt(5)
	v_mfma_f32_16x16x32_bf16 v[80:83], v[104:107], v[24:27], v[80:83]
	v_mfma_f32_16x16x32_bf16 v[84:87], v[104:107], v[56:59], v[84:87]
	s_waitcnt lgkmcnt(4)
	v_mfma_f32_16x16x32_bf16 v[88:91], v[108:111], v[24:27], v[88:91]
	v_mfma_f32_16x16x32_bf16 v[92:95], v[108:111], v[56:59], v[92:95]
	s_waitcnt lgkmcnt(3)
	v_mfma_f32_16x16x32_bf16 v[64:67], v[112:115], v[28:31], v[64:67]
	v_mfma_f32_16x16x32_bf16 v[68:71], v[112:115], v[60:63], v[68:71]
	s_waitcnt lgkmcnt(2)
	v_mfma_f32_16x16x32_bf16 v[72:75], v[116:119], v[28:31], v[72:75]
	v_mfma_f32_16x16x32_bf16 v[76:79], v[116:119], v[60:63], v[76:79]
	s_waitcnt lgkmcnt(1)
	v_mfma_f32_16x16x32_bf16 v[80:83], v[120:123], v[28:31], v[80:83]
	v_mfma_f32_16x16x32_bf16 v[84:87], v[120:123], v[60:63], v[84:87]
	s_waitcnt lgkmcnt(0)
	v_mfma_f32_16x16x32_bf16 v[88:91], v[124:127], v[28:31], v[88:91]
	v_mfma_f32_16x16x32_bf16 v[92:95], v[124:127], v[60:63], v[92:95]
	v_or_b32_e32 v198, 0x10000, v165
	v_or_b32_e32 v199, 0x10000, v166
	v_or_b32_e32 v200, 0x10000, v167
	v_or_b32_e32 v201, 0x10000, v168
	ds_read_u16 v144, v198
	ds_read_u16 v145, v199
	ds_read_u16 v146, v200
	ds_read_u16 v147, v201
	ds_read_u16 v148, v198 offset:8192
	ds_read_u16 v149, v199 offset:8192
	ds_read_u16 v150, v200 offset:8192
	ds_read_u16 v151, v201 offset:8192
	ds_read_u16 v152, v198 offset:16384
	ds_read_u16 v153, v199 offset:16384
	ds_read_u16 v154, v200 offset:16384
	ds_read_u16 v155, v201 offset:16384
	ds_read_u16 v156, v198 offset:24576
	ds_read_u16 v157, v199 offset:24576
	ds_read_u16 v158, v200 offset:24576
	ds_read_u16 v159, v201 offset:24576
	s_nop 7
	v_fma_f32 v178, v64, s53, v173
	v_fma_f32 v179, v65, s53, v173
	v_fma_f32 v180, v66, s53, v173
	v_fma_f32 v181, v67, s53, v173
	v_fma_f32 v182, v72, s53, v173
	v_fma_f32 v183, v73, s53, v173
	v_fma_f32 v184, v74, s53, v173
	v_fma_f32 v185, v75, s53, v173
	v_fma_f32 v186, v68, s53, v174
	v_fma_f32 v187, v69, s53, v174
	v_fma_f32 v188, v70, s53, v174
	v_fma_f32 v189, v71, s53, v174
	v_fma_f32 v190, v76, s53, v174
	v_fma_f32 v191, v77, s53, v174
	v_fma_f32 v192, v78, s53, v174
	v_fma_f32 v193, v79, s53, v174
	v_exp_f32_e32 v178, v178
	v_exp_f32_e32 v179, v179
	v_exp_f32_e32 v180, v180
	v_exp_f32_e32 v181, v181
	v_exp_f32_e32 v182, v182
	v_exp_f32_e32 v183, v183
	v_exp_f32_e32 v184, v184
	v_exp_f32_e32 v185, v185
	v_exp_f32_e32 v186, v186
	v_exp_f32_e32 v187, v187
	v_exp_f32_e32 v188, v188
	v_exp_f32_e32 v189, v189
	v_exp_f32_e32 v190, v190
	v_exp_f32_e32 v191, v191
	v_exp_f32_e32 v192, v192
	v_exp_f32_e32 v193, v193
	v_add_f32_e32 v178, 1.0, v178
	v_add_f32_e32 v179, 1.0, v179
	v_add_f32_e32 v180, 1.0, v180
	v_add_f32_e32 v181, 1.0, v181
	v_add_f32_e32 v182, 1.0, v182
	v_add_f32_e32 v183, 1.0, v183
	v_add_f32_e32 v184, 1.0, v184
	v_add_f32_e32 v185, 1.0, v185
	v_add_f32_e32 v186, 1.0, v186
	v_add_f32_e32 v187, 1.0, v187
	v_add_f32_e32 v188, 1.0, v188
	v_add_f32_e32 v189, 1.0, v189
	v_add_f32_e32 v190, 1.0, v190
	v_add_f32_e32 v191, 1.0, v191
	v_add_f32_e32 v192, 1.0, v192
	v_add_f32_e32 v193, 1.0, v193
	v_rcp_f32_e32 v178, v178
	v_rcp_f32_e32 v179, v179
	v_rcp_f32_e32 v180, v180
	v_rcp_f32_e32 v181, v181
	v_rcp_f32_e32 v182, v182
	v_rcp_f32_e32 v183, v183
	v_rcp_f32_e32 v184, v184
	v_rcp_f32_e32 v185, v185
	v_rcp_f32_e32 v186, v186
	v_rcp_f32_e32 v187, v187
	v_rcp_f32_e32 v188, v188
	v_rcp_f32_e32 v189, v189
	v_rcp_f32_e32 v190, v190
	v_rcp_f32_e32 v191, v191
	v_rcp_f32_e32 v192, v192
	v_rcp_f32_e32 v193, v193
	v_mul_f32_e32 v178, v175, v178
	v_mul_f32_e32 v179, v175, v179
	v_mul_f32_e32 v180, v175, v180
	v_mul_f32_e32 v181, v175, v181
	v_mul_f32_e32 v182, v175, v182
	v_mul_f32_e32 v183, v175, v183
	v_mul_f32_e32 v184, v175, v184
	v_mul_f32_e32 v185, v175, v185
	v_exp_f32_e32 v96, v178
	v_exp_f32_e32 v97, v179
	v_exp_f32_e32 v98, v180
	v_exp_f32_e32 v99, v181
	v_exp_f32_e32 v100, v182
	v_exp_f32_e32 v101, v183
	v_exp_f32_e32 v102, v184
	v_exp_f32_e32 v103, v185
	s_nop 0
	v_fma_f32 v194, -v96, v96, 1.0
	v_fma_f32 v195, -v97, v97, 1.0
	v_fma_f32 v196, -v98, v98, 1.0
	v_fma_f32 v197, -v99, v99, 1.0
	v_fma_f32 v198, -v100, v100, 1.0
	v_fma_f32 v199, -v101, v101, 1.0
	v_fma_f32 v200, -v102, v102, 1.0
	v_fma_f32 v201, -v103, v103, 1.0
	v_max_f32_e32 v194, 0, v194
	v_max_f32_e32 v195, 0, v195
	v_max_f32_e32 v196, 0, v196
	v_max_f32_e32 v197, 0, v197
	v_max_f32_e32 v198, 0, v198
	v_max_f32_e32 v199, 0, v199
	v_max_f32_e32 v200, 0, v200
	v_max_f32_e32 v201, 0, v201
	v_sqrt_f32_e32 v194, v194
	v_sqrt_f32_e32 v195, v195
	v_sqrt_f32_e32 v196, v196
	v_sqrt_f32_e32 v197, v197
	v_sqrt_f32_e32 v198, v198
	v_sqrt_f32_e32 v199, v199
	v_sqrt_f32_e32 v200, v200
	v_sqrt_f32_e32 v201, v201
	s_waitcnt lgkmcnt(8)
	v_lshlrev_b32_e32 v144, 16, v144
	v_lshlrev_b32_e32 v145, 16, v145
	v_lshlrev_b32_e32 v146, 16, v146
	v_lshlrev_b32_e32 v147, 16, v147
	v_lshlrev_b32_e32 v148, 16, v148
	v_lshlrev_b32_e32 v149, 16, v149
	v_lshlrev_b32_e32 v150, 16, v150
	v_lshlrev_b32_e32 v151, 16, v151
	v_mul_f32_e32 v194, v194, v186
	v_mul_f32_e32 v195, v195, v187
	v_mul_f32_e32 v196, v196, v188
	v_mul_f32_e32 v197, v197, v189
	v_mul_f32_e32 v198, v198, v190
	v_mul_f32_e32 v199, v199, v191
	v_mul_f32_e32 v200, v200, v192
	v_mul_f32_e32 v201, v201, v193
	v_mul_f32_e32 v144, v194, v144
	v_mul_f32_e32 v145, v195, v145
	v_mul_f32_e32 v146, v196, v146
	v_mul_f32_e32 v147, v197, v147
	v_mul_f32_e32 v148, v198, v148
	v_mul_f32_e32 v149, v199, v149
	v_mul_f32_e32 v150, v200, v150
	v_mul_f32_e32 v151, v201, v151
	v_fma_f32 v178, v80, s53, v173
	v_fma_f32 v179, v81, s53, v173
	v_fma_f32 v180, v82, s53, v173
	v_fma_f32 v181, v83, s53, v173
	v_fma_f32 v182, v88, s53, v173
	v_fma_f32 v183, v89, s53, v173
	v_fma_f32 v184, v90, s53, v173
	v_fma_f32 v185, v91, s53, v173
	v_fma_f32 v186, v84, s53, v174
	v_fma_f32 v187, v85, s53, v174
	v_fma_f32 v188, v86, s53, v174
	v_fma_f32 v189, v87, s53, v174
	v_fma_f32 v190, v92, s53, v174
	v_fma_f32 v191, v93, s53, v174
	v_fma_f32 v192, v94, s53, v174
	v_fma_f32 v193, v95, s53, v174
	v_exp_f32_e32 v178, v178
	v_exp_f32_e32 v179, v179
	v_exp_f32_e32 v180, v180
	v_exp_f32_e32 v181, v181
	v_exp_f32_e32 v182, v182
	v_exp_f32_e32 v183, v183
	v_exp_f32_e32 v184, v184
	v_exp_f32_e32 v185, v185
	v_exp_f32_e32 v186, v186
	v_exp_f32_e32 v187, v187
	v_exp_f32_e32 v188, v188
	v_exp_f32_e32 v189, v189
	v_exp_f32_e32 v190, v190
	v_exp_f32_e32 v191, v191
	v_exp_f32_e32 v192, v192
	v_exp_f32_e32 v193, v193
	v_add_f32_e32 v178, 1.0, v178
	v_add_f32_e32 v179, 1.0, v179
	v_add_f32_e32 v180, 1.0, v180
	v_add_f32_e32 v181, 1.0, v181
	v_add_f32_e32 v182, 1.0, v182
	v_add_f32_e32 v183, 1.0, v183
	v_add_f32_e32 v184, 1.0, v184
	v_add_f32_e32 v185, 1.0, v185
	v_add_f32_e32 v186, 1.0, v186
	v_add_f32_e32 v187, 1.0, v187
	v_add_f32_e32 v188, 1.0, v188
	v_add_f32_e32 v189, 1.0, v189
	v_add_f32_e32 v190, 1.0, v190
	v_add_f32_e32 v191, 1.0, v191
	v_add_f32_e32 v192, 1.0, v192
	v_add_f32_e32 v193, 1.0, v193
	v_rcp_f32_e32 v178, v178
	v_rcp_f32_e32 v179, v179
	v_rcp_f32_e32 v180, v180
	v_rcp_f32_e32 v181, v181
	v_rcp_f32_e32 v182, v182
	v_rcp_f32_e32 v183, v183
	v_rcp_f32_e32 v184, v184
	v_rcp_f32_e32 v185, v185
	v_rcp_f32_e32 v186, v186
	v_rcp_f32_e32 v187, v187
	v_rcp_f32_e32 v188, v188
	v_rcp_f32_e32 v189, v189
	v_rcp_f32_e32 v190, v190
	v_rcp_f32_e32 v191, v191
	v_rcp_f32_e32 v192, v192
	v_rcp_f32_e32 v193, v193
	v_mul_f32_e32 v178, v175, v178
	v_mul_f32_e32 v179, v175, v179
	v_mul_f32_e32 v180, v175, v180
	v_mul_f32_e32 v181, v175, v181
	v_mul_f32_e32 v182, v175, v182
	v_mul_f32_e32 v183, v175, v183
	v_mul_f32_e32 v184, v175, v184
	v_mul_f32_e32 v185, v175, v185
	v_exp_f32_e32 v104, v178
	v_exp_f32_e32 v105, v179
	v_exp_f32_e32 v106, v180
	v_exp_f32_e32 v107, v181
	v_exp_f32_e32 v108, v182
	v_exp_f32_e32 v109, v183
	v_exp_f32_e32 v110, v184
	v_exp_f32_e32 v111, v185
	s_nop 0
	v_fma_f32 v194, -v104, v104, 1.0
	v_fma_f32 v195, -v105, v105, 1.0
	v_fma_f32 v196, -v106, v106, 1.0
	v_fma_f32 v197, -v107, v107, 1.0
	v_fma_f32 v198, -v108, v108, 1.0
	v_fma_f32 v199, -v109, v109, 1.0
	v_fma_f32 v200, -v110, v110, 1.0
	v_fma_f32 v201, -v111, v111, 1.0
	v_max_f32_e32 v194, 0, v194
	v_max_f32_e32 v195, 0, v195
	v_max_f32_e32 v196, 0, v196
	v_max_f32_e32 v197, 0, v197
	v_max_f32_e32 v198, 0, v198
	v_max_f32_e32 v199, 0, v199
	v_max_f32_e32 v200, 0, v200
	v_max_f32_e32 v201, 0, v201
	v_sqrt_f32_e32 v194, v194
	v_sqrt_f32_e32 v195, v195
	v_sqrt_f32_e32 v196, v196
	v_sqrt_f32_e32 v197, v197
	v_sqrt_f32_e32 v198, v198
	v_sqrt_f32_e32 v199, v199
	v_sqrt_f32_e32 v200, v200
	v_sqrt_f32_e32 v201, v201
	s_waitcnt lgkmcnt(0)
	v_lshlrev_b32_e32 v152, 16, v152
	v_lshlrev_b32_e32 v153, 16, v153
	v_lshlrev_b32_e32 v154, 16, v154
	v_lshlrev_b32_e32 v155, 16, v155
	v_lshlrev_b32_e32 v156, 16, v156
	v_lshlrev_b32_e32 v157, 16, v157
	v_lshlrev_b32_e32 v158, 16, v158
	v_lshlrev_b32_e32 v159, 16, v159
	v_mul_f32_e32 v194, v194, v186
	v_mul_f32_e32 v195, v195, v187
	v_mul_f32_e32 v196, v196, v188
	v_mul_f32_e32 v197, v197, v189
	v_mul_f32_e32 v198, v198, v190
	v_mul_f32_e32 v199, v199, v191
	v_mul_f32_e32 v200, v200, v192
	v_mul_f32_e32 v201, v201, v193
	v_mul_f32_e32 v152, v194, v152
	v_mul_f32_e32 v153, v195, v153
	v_mul_f32_e32 v154, v196, v154
	v_mul_f32_e32 v155, v197, v155
	v_mul_f32_e32 v156, v198, v156
	v_mul_f32_e32 v157, v199, v157
	v_mul_f32_e32 v158, v200, v158
	v_mul_f32_e32 v159, v201, v159
	v_fma_f32 v146, v98, v147, v146
	v_fma_f32 v150, v102, v151, v150
	v_fma_f32 v154, v106, v155, v154
	v_fma_f32 v158, v110, v159, v158
	v_mul_f32_e32 v98, v98, v99
	v_mul_f32_e32 v102, v102, v103
	v_mul_f32_e32 v106, v106, v107
	v_mul_f32_e32 v110, v110, v111
	v_fma_f32 v145, v97, v146, v145
	v_fma_f32 v149, v101, v150, v149
	v_fma_f32 v153, v105, v154, v153
	v_fma_f32 v157, v109, v158, v157
	v_mul_f32_e32 v97, v97, v98
	v_mul_f32_e32 v101, v101, v102
	v_mul_f32_e32 v105, v105, v106
	v_mul_f32_e32 v109, v109, v110
	v_fma_f32 v144, v96, v145, v144
	v_fma_f32 v148, v100, v149, v148
	v_fma_f32 v152, v104, v153, v152
	v_fma_f32 v156, v108, v157, v156
	v_mul_f32_e32 v96, v96, v97
	v_mul_f32_e32 v100, v100, v101
	v_mul_f32_e32 v104, v104, v105
	v_mul_f32_e32 v108, v108, v109
	ds_bpermute_b32 v178, v204, v96
	ds_bpermute_b32 v182, v204, v144
	ds_bpermute_b32 v179, v204, v100
	ds_bpermute_b32 v183, v204, v148
	ds_bpermute_b32 v180, v204, v104
	ds_bpermute_b32 v184, v204, v152
	ds_bpermute_b32 v181, v204, v108
	ds_bpermute_b32 v185, v204, v156
	s_waitcnt lgkmcnt(0)
	v_fma_f32 v186, v182, v96, v144
	v_cndmask_b32_e64 v178, 1.0, v178, s[34:35]
	v_fma_f32 v187, v183, v100, v148
	v_cndmask_b32_e64 v179, 1.0, v179, s[34:35]
	v_fma_f32 v188, v184, v104, v152
	v_cndmask_b32_e64 v180, 1.0, v180, s[34:35]
	v_fma_f32 v189, v185, v108, v156
	v_cndmask_b32_e64 v181, 1.0, v181, s[34:35]
	v_cndmask_b32_e64 v223, v144, v186, s[34:35]
	v_mul_f32_e32 v219, v96, v178
	v_cndmask_b32_e64 v224, v148, v187, s[34:35]
	v_mul_f32_e32 v220, v100, v179
	v_cndmask_b32_e64 v225, v152, v188, s[34:35]
	v_mul_f32_e32 v221, v104, v180
	v_cndmask_b32_e64 v226, v156, v189, s[34:35]
	v_mul_f32_e32 v222, v108, v181
	ds_bpermute_b32 v178, v205, v219
	ds_bpermute_b32 v182, v205, v223
	ds_bpermute_b32 v179, v205, v220
	ds_bpermute_b32 v183, v205, v224
	ds_bpermute_b32 v180, v205, v221
	ds_bpermute_b32 v184, v205, v225
	ds_bpermute_b32 v181, v205, v222
	ds_bpermute_b32 v185, v205, v226
	s_waitcnt lgkmcnt(0)
	v_fma_f32 v186, v182, v219, v223
	v_cndmask_b32_e64 v178, 1.0, v178, s[36:37]
	v_fma_f32 v187, v183, v220, v224
	v_cndmask_b32_e64 v179, 1.0, v179, s[36:37]
	v_fma_f32 v188, v184, v221, v225
	v_cndmask_b32_e64 v180, 1.0, v180, s[36:37]
	v_fma_f32 v189, v185, v222, v226
	v_cndmask_b32_e64 v181, 1.0, v181, s[36:37]
	v_cndmask_b32_e64 v223, v223, v186, s[36:37]
	v_mul_f32_e32 v219, v219, v178
	v_cndmask_b32_e64 v224, v224, v187, s[36:37]
	v_mul_f32_e32 v220, v220, v179
	v_cndmask_b32_e64 v225, v225, v188, s[36:37]
	v_mul_f32_e32 v221, v221, v180
	v_cndmask_b32_e64 v226, v226, v189, s[36:37]
	v_mul_f32_e32 v222, v222, v181
	ds_bpermute_b32 v227, v204, v219
	ds_bpermute_b32 v231, v204, v223
	ds_bpermute_b32 v235, v206, v219
	ds_bpermute_b32 v239, v206, v223
	ds_bpermute_b32 v228, v204, v220
	ds_bpermute_b32 v232, v204, v224
	ds_bpermute_b32 v236, v206, v220
	ds_bpermute_b32 v244, v206, v224
	ds_bpermute_b32 v229, v204, v221
	ds_bpermute_b32 v233, v204, v225
	ds_bpermute_b32 v237, v206, v221
	ds_bpermute_b32 v245, v206, v225
	ds_bpermute_b32 v230, v204, v222
	ds_bpermute_b32 v234, v204, v226
	ds_bpermute_b32 v238, v206, v222
	ds_bpermute_b32 v246, v206, v226
	s_waitcnt lgkmcnt(0)
	v_cndmask_b32_e64 v227, 1.0, v227, s[34:35]
	v_cndmask_b32_e64 v231, 0, v231, s[34:35]
	v_cndmask_b32_e64 v228, 1.0, v228, s[34:35]
	v_cndmask_b32_e64 v232, 0, v232, s[34:35]
	v_cndmask_b32_e64 v229, 1.0, v229, s[34:35]
	v_cndmask_b32_e64 v233, 0, v233, s[34:35]
	v_cndmask_b32_e64 v230, 1.0, v230, s[34:35]
	v_cndmask_b32_e64 v234, 0, v234, s[34:35]
	v_mov_b32_e32 v190, v238
	v_mov_b32_e32 v194, v246
	v_mov_b32_e32 v198, v190
	v_mov_b32_e32 v201, v194
	v_fma_f32 v194, v194, v237, v245
	v_mul_f32_e32 v190, v190, v237
	v_mov_b32_e32 v199, v190
	v_mov_b32_e32 v177, v194
	v_fma_f32 v194, v194, v236, v244
	v_mul_f32_e32 v190, v190, v236
	v_mov_b32_e32 v200, v190
	v_mov_b32_e32 v203, v194
	v_fma_f32 v194, v194, v235, v239
	v_mul_f32_e32 v190, v190, v235
	v_mov_b32_e32 v191, v194
	ds_write_b64 v207, v[190:191] offset:1024
	s_waitcnt lgkmcnt(0)
	s_barrier
	ds_read_b64 v[178:179], v208 offset:1536
	ds_read_b64 v[180:181], v208 offset:1024
	s_waitcnt lgkmcnt(0)
	v_fma_f32 v182, v176, v178, v179
	v_cndmask_b32_e64 v183, v176, v182, s[38:39]
	v_fma_f32 v176, v182, v180, v181
	s_add_i32 s13, s13, 1
	s_mov_b32 s60, 8
.Lmylru_loop_1:
	s_waitcnt vmcnt(0)
	s_barrier
	s_cmp_eq_u32 s13, 2
	s_cbranch_scc1 .Lmylru_nf_7
	ds_read_b128 v[178:181], v170
	ds_read_b128 v[182:185], v170 offset:1024
	s_waitcnt lgkmcnt(0)
	global_store_dwordx4 v171, v[178:181], s[62:63]
	global_store_dwordx4 v172, v[182:185], s[62:63]
.Lmylru_nf_7:
	s_sub_i32 s54, 17, s13
	s_lshl_b32 s55, s54, 14
	s_lshl_b32 s56, s6, 11
	s_add_i32 s55, s55, s56
	s_add_u32 s44, s22, s55
	s_addc_u32 s45, s23, 0
	s_cmp_lt_u32 s13, 2
	s_sub_i32 s50, 1, s13
	s_lshl_b32 s50, s50, 7
	s_lshl_b32 s51, s9, 8
	s_add_i32 s51, s51, 0x8000
	s_add_i32 s51, s51, s50
	s_sub_i32 s50, 17, s13
	s_lshl_b32 s50, s50, 7
	s_lshl_b32 s57, s9, 11
	s_add_i32 s57, s57, s50
	s_cmp_lt_u32 s13, 2
	s_cselect_b32 s57, s51, s57
	s_lshl_b32 s57, s57, 11
	s_add_u32 s40, s18, s57
	s_addc_u32 s41, s19, 0
	s_add_u32 s42, s20, s57
	s_addc_u32 s43, s21, 0
	global_load_dword v247, v209, s[44:45]
	global_load_dword v248, v209, s[44:45] offset:256
	global_load_dword v249, v209, s[44:45] offset:512
	global_load_dword v250, v209, s[44:45] offset:768
	global_load_dword v251, v209, s[44:45] offset:1024
	global_load_dword v252, v209, s[44:45] offset:1280
	global_load_dword v253, v209, s[44:45] offset:1536
	global_load_dword v254, v209, s[44:45] offset:1792
	v_add_u32_e32 v182, 0x0, v210
	v_add_u32_e32 v183, 0x1000, v182
	global_load_ushort v128, v182, s[40:41]
	global_load_ushort v129, v182, s[40:41] offset:2048
	global_load_ushort v130, v183, s[40:41]
	global_load_ushort v131, v183, s[40:41] offset:2048
	v_add_u32_e32 v182, 0x8000, v210
	v_add_u32_e32 v183, 0x1000, v182
	global_load_ushort v132, v182, s[40:41]
	global_load_ushort v133, v182, s[40:41] offset:2048
	global_load_ushort v134, v183, s[40:41]
	global_load_ushort v135, v183, s[40:41] offset:2048
	v_add_u32_e32 v182, 0x10000, v210
	v_add_u32_e32 v183, 0x1000, v182
	global_load_ushort v136, v182, s[40:41]
	global_load_ushort v137, v182, s[40:41] offset:2048
	global_load_ushort v138, v183, s[40:41]
	global_load_ushort v139, v183, s[40:41] offset:2048
	v_add_u32_e32 v182, 0x18000, v210
	v_add_u32_e32 v183, 0x1000, v182
	global_load_ushort v140, v182, s[40:41]
	global_load_ushort v141, v182, s[40:41] offset:2048
	global_load_ushort v142, v183, s[40:41]
	global_load_ushort v143, v183, s[40:41] offset:2048
	s_cmp_eq_u32 s13, 17
	s_cbranch_scc1 .Lmylru_nodma_7
	s_add_i32 s58, s13, 1
	s_cmp_lt_u32 s58, 2
	s_sub_i32 s50, 1, s58
	s_lshl_b32 s50, s50, 7
	s_lshl_b32 s51, s9, 8
	s_add_i32 s51, s51, 0x8000
	s_add_i32 s51, s51, s50
	s_sub_i32 s50, 17, s58
	s_lshl_b32 s50, s50, 7
	s_lshl_b32 s59, s9, 11
	s_add_i32 s59, s59, s50
	s_cmp_lt_u32 s58, 2
	s_cselect_b32 s59, s51, s59
	s_lshl_b32 s52, s59, 11
	s_add_u32 s46, s16, s52
	s_addc_u32 s47, s17, 0
	s_lshl_b32 s52, s6, 13
	s_add_i32 s52, s52, 0x10000
	s_mov_b32 m0, s52
	s_add_i32 s52, s52, 0x400
	global_load_lds_dwordx4 v211, s[46:47]
	s_mov_b32 m0, s52
	s_add_i32 s52, s52, 0x400
	global_load_lds_dwordx4 v212, s[46:47]
	s_mov_b32 m0, s52
	s_add_i32 s52, s52, 0x400
	global_load_lds_dwordx4 v213, s[46:47]
	s_mov_b32 m0, s52
	s_add_i32 s52, s52, 0x400
	global_load_lds_dwordx4 v214, s[46:47]
	s_mov_b32 m0, s52
	s_add_i32 s52, s52, 0x400
	global_load_lds_dwordx4 v215, s[46:47]
	s_mov_b32 m0, s52
	s_add_i32 s52, s52, 0x400
	global_load_lds_dwordx4 v216, s[46:47]
	s_mov_b32 m0, s52
	s_add_i32 s52, s52, 0x400
	global_load_lds_dwordx4 v217, s[46:47]
	s_mov_b32 m0, s52
	s_nop 0
	global_load_lds_dwordx4 v218, s[46:47]
.Lmylru_nodma_7:
	v_mov_b32_e32 v163, v162
	ds_read_b128 v[96:99], v163
	ds_read_b128 v[100:103], v163 offset:8192
	ds_read_b128 v[104:107], v163 offset:16384
	ds_read_b128 v[108:111], v163 offset:24576
	v_xor_b32_e32 v164, 0x40, v163
	ds_read_b128 v[112:115], v164
	ds_read_b128 v[116:119], v164 offset:8192
	ds_read_b128 v[120:123], v164 offset:16384
	ds_read_b128 v[124:127], v164 offset:24576
	s_waitcnt lgkmcnt(7)
	v_mfma_f32_16x16x32_bf16 v[64:67], v[96:99], v[0:3], 0
	v_mfma_f32_16x16x32_bf16 v[68:71], v[96:99], v[32:35], 0
	v_xor_b32_e32 v164, 0x80, v163
	ds_read_b128 v[96:99], v164
	s_waitcnt lgkmcnt(7)
	v_mfma_f32_16x16x32_bf16 v[72:75], v[100:103], v[0:3], 0
	v_mfma_f32_16x16x32_bf16 v[76:79], v[100:103], v[32:35], 0
	ds_read_b128 v[100:103], v164 offset:8192
	s_waitcnt lgkmcnt(7)
	v_mfma_f32_16x16x32_bf16 v[80:83], v[104:107], v[0:3], 0
	v_mfma_f32_16x16x32_bf16 v[84:87], v[104:107], v[32:35], 0
	ds_read_b128 v[104:107], v164 offset:16384
	s_waitcnt lgkmcnt(7)
	v_mfma_f32_16x16x32_bf16 v[88:91], v[108:111], v[0:3], 0
	v_mfma_f32_16x16x32_bf16 v[92:95], v[108:111], v[32:35], 0
	ds_read_b128 v[108:111], v164 offset:24576
	s_waitcnt lgkmcnt(7)
	v_mfma_f32_16x16x32_bf16 v[64:67], v[112:115], v[4:7], v[64:67]
	v_mfma_f32_16x16x32_bf16 v[68:71], v[112:115], v[36:39], v[68:71]
	v_xor_b32_e32 v164, 0xc0, v163
	ds_read_b128 v[112:115], v164
	s_waitcnt lgkmcnt(7)
	v_mfma_f32_16x16x32_bf16 v[72:75], v[116:119], v[4:7], v[72:75]
	v_mfma_f32_16x16x32_bf16 v[76:79], v[116:119], v[36:39], v[76:79]
	ds_read_b128 v[116:119], v164 offset:8192
	s_waitcnt lgkmcnt(7)
	v_mfma_f32_16x16x32_bf16 v[80:83], v[120:123], v[4:7], v[80:83]
	v_mfma_f32_16x16x32_bf16 v[84:87], v[120:123], v[36:39], v[84:87]
	ds_read_b128 v[120:123], v164 offset:16384
	s_waitcnt lgkmcnt(7)
	v_mfma_f32_16x16x32_bf16 v[88:91], v[124:127], v[4:7], v[88:91]
	v_mfma_f32_16x16x32_bf16 v[92:95], v[124:127], v[36:39], v[92:95]
	ds_read_b128 v[124:127], v164 offset:24576
	s_waitcnt lgkmcnt(7)
	v_mfma_f32_16x16x32_bf16 v[64:67], v[96:99], v[8:11], v[64:67]
	v_mfma_f32_16x16x32_bf16 v[68:71], v[96:99], v[40:43], v[68:71]
	v_xor_b32_e32 v164, 0x100, v163
	ds_read_b128 v[96:99], v164
	s_waitcnt lgkmcnt(7)
	v_mfma_f32_16x16x32_bf16 v[72:75], v[100:103], v[8:11], v[72:75]
	v_mfma_f32_16x16x32_bf16 v[76:79], v[100:103], v[40:43], v[76:79]
	ds_read_b128 v[100:103], v164 offset:8192
	s_waitcnt lgkmcnt(7)
	v_mfma_f32_16x16x32_bf16 v[80:83], v[104:107], v[8:11], v[80:83]
	v_mfma_f32_16x16x32_bf16 v[84:87], v[104:107], v[40:43], v[84:87]
	ds_read_b128 v[104:107], v164 offset:16384
	s_waitcnt lgkmcnt(7)
	v_mfma_f32_16x16x32_bf16 v[88:91], v[108:111], v[8:11], v[88:91]
	v_mfma_f32_16x16x32_bf16 v[92:95], v[108:111], v[40:43], v[92:95]
	ds_read_b128 v[108:111], v164 offset:24576
	s_waitcnt lgkmcnt(7)
	v_mfma_f32_16x16x32_bf16 v[64:67], v[112:115], v[12:15], v[64:67]
	v_mfma_f32_16x16x32_bf16 v[68:71], v[112:115], v[44:47], v[68:71]
	v_xor_b32_e32 v164, 0x140, v163
	ds_read_b128 v[112:115], v164
	s_waitcnt lgkmcnt(7)
	v_mfma_f32_16x16x32_bf16 v[72:75], v[116:119], v[12:15], v[72:75]
	v_mfma_f32_16x16x32_bf16 v[76:79], v[116:119], v[44:47], v[76:79]
	ds_read_b128 v[116:119], v164 offset:8192
	s_waitcnt lgkmcnt(7)
	v_mfma_f32_16x16x32_bf16 v[80:83], v[120:123], v[12:15], v[80:83]
	v_mfma_f32_16x16x32_bf16 v[84:87], v[120:123], v[44:47], v[84:87]
	ds_read_b128 v[120:123], v164 offset:16384
	s_waitcnt lgkmcnt(7)
	v_mfma_f32_16x16x32_bf16 v[88:91], v[124:127], v[12:15], v[88:91]
	v_mfma_f32_16x16x32_bf16 v[92:95], v[124:127], v[44:47], v[92:95]
	ds_read_b128 v[124:127], v164 offset:24576
	s_waitcnt lgkmcnt(7)
	v_mfma_f32_16x16x32_bf16 v[64:67], v[96:99], v[16:19], v[64:67]
	v_mfma_f32_16x16x32_bf16 v[68:71], v[96:99], v[48:51], v[68:71]
	v_xor_b32_e32 v164, 0x180, v163
	ds_read_b128 v[96:99], v164
	s_waitcnt lgkmcnt(7)
	v_mfma_f32_16x16x32_bf16 v[72:75], v[100:103], v[16:19], v[72:75]
	v_mfma_f32_16x16x32_bf16 v[76:79], v[100:103], v[48:51], v[76:79]
	ds_read_b128 v[100:103], v164 offset:8192
	s_waitcnt lgkmcnt(7)
	v_mfma_f32_16x16x32_bf16 v[80:83], v[104:107], v[16:19], v[80:83]
	v_mfma_f32_16x16x32_bf16 v[84:87], v[104:107], v[48:51], v[84:87]
	ds_read_b128 v[104:107], v164 offset:16384
	s_waitcnt lgkmcnt(7)
	v_mfma_f32_16x16x32_bf16 v[88:91], v[108:111], v[16:19], v[88:91]
	v_mfma_f32_16x16x32_bf16 v[92:95], v[108:111], v[48:51], v[92:95]
	ds_read_b128 v[108:111], v164 offset:24576
	s_waitcnt lgkmcnt(7)
	v_mfma_f32_16x16x32_bf16 v[64:67], v[112:115], v[20:23], v[64:67]
	v_mfma_f32_16x16x32_bf16 v[68:71], v[112:115], v[52:55], v[68:71]
	v_xor_b32_e32 v164, 0x1c0, v163
	ds_read_b128 v[112:115], v164
	s_waitcnt lgkmcnt(7)
	v_mfma_f32_16x16x32_bf16 v[72:75], v[116:119], v[20:23], v[72:75]
	v_mfma_f32_16x16x32_bf16 v[76:79], v[116:119], v[52:55], v[76:79]
	ds_read_b128 v[116:119], v164 offset:8192
	s_waitcnt lgkmcnt(7)
	v_mfma_f32_16x16x32_bf16 v[80:83], v[120:123], v[20:23], v[80:83]
	v_mfma_f32_16x16x32_bf16 v[84:87], v[120:123], v[52:55], v[84:87]
	ds_read_b128 v[120:123], v164 offset:16384
	s_waitcnt lgkmcnt(7)
	v_mfma_f32_16x16x32_bf16 v[88:91], v[124:127], v[20:23], v[88:91]
	v_mfma_f32_16x16x32_bf16 v[92:95], v[124:127], v[52:55], v[92:95]
	ds_read_b128 v[124:127], v164 offset:24576
	s_waitcnt lgkmcnt(7)
	v_mfma_f32_16x16x32_bf16 v[64:67], v[96:99], v[24:27], v[64:67]
	v_mfma_f32_16x16x32_bf16 v[68:71], v[96:99], v[56:59], v[68:71]
	s_waitcnt lgkmcnt(6)
	v_mfma_f32_16x16x32_bf16 v[72:75], v[100:103], v[24:27], v[72:75]
	v_mfma_f32_16x16x32_bf16 v[76:79], v[100:103], v[56:59], v[76:79]
	s_waitcnt lgkmcnt(5)
	v_mfma_f32_16x16x32_bf16 v[80:83], v[104:107], v[24:27], v[80:83]
	v_mfma_f32_16x16x32_bf16 v[84:87], v[104:107], v[56:59], v[84:87]
	s_waitcnt lgkmcnt(4)
	v_mfma_f32_16x16x32_bf16 v[88:91], v[108:111], v[24:27], v[88:91]
	v_mfma_f32_16x16x32_bf16 v[92:95], v[108:111], v[56:59], v[92:95]
	s_waitcnt lgkmcnt(3)
	v_mfma_f32_16x16x32_bf16 v[64:67], v[112:115], v[28:31], v[64:67]
	v_mfma_f32_16x16x32_bf16 v[68:71], v[112:115], v[60:63], v[68:71]
	s_waitcnt lgkmcnt(2)
	v_mfma_f32_16x16x32_bf16 v[72:75], v[116:119], v[28:31], v[72:75]
	v_mfma_f32_16x16x32_bf16 v[76:79], v[116:119], v[60:63], v[76:79]
	s_waitcnt lgkmcnt(1)
	v_mfma_f32_16x16x32_bf16 v[80:83], v[120:123], v[28:31], v[80:83]
	v_mfma_f32_16x16x32_bf16 v[84:87], v[120:123], v[60:63], v[84:87]
	s_waitcnt lgkmcnt(0)
	v_mfma_f32_16x16x32_bf16 v[88:91], v[124:127], v[28:31], v[88:91]
	v_mfma_f32_16x16x32_bf16 v[92:95], v[124:127], v[60:63], v[92:95]
	v_mov_b32_e32 v198, v165
	v_mov_b32_e32 v199, v166
	v_mov_b32_e32 v200, v167
	v_mov_b32_e32 v201, v168
	ds_read_u16 v144, v198
	ds_read_u16 v145, v199
	ds_read_u16 v146, v200
	ds_read_u16 v147, v201
	ds_read_u16 v148, v198 offset:8192
	ds_read_u16 v149, v199 offset:8192
	ds_read_u16 v150, v200 offset:8192
	ds_read_u16 v151, v201 offset:8192
	ds_read_u16 v152, v198 offset:16384
	ds_read_u16 v153, v199 offset:16384
	ds_read_u16 v154, v200 offset:16384
	ds_read_u16 v155, v201 offset:16384
	ds_read_u16 v156, v198 offset:24576
	ds_read_u16 v157, v199 offset:24576
	ds_read_u16 v158, v200 offset:24576
	ds_read_u16 v159, v201 offset:24576
	s_nop 7
	v_fma_f32 v178, v64, s53, v173
	v_fma_f32 v179, v65, s53, v173
	v_fma_f32 v180, v66, s53, v173
	v_fma_f32 v181, v67, s53, v173
	v_fma_f32 v182, v72, s53, v173
	v_fma_f32 v183, v73, s53, v173
	v_fma_f32 v184, v74, s53, v173
	v_fma_f32 v185, v75, s53, v173
	v_fma_f32 v186, v68, s53, v174
	v_fma_f32 v187, v69, s53, v174
	v_fma_f32 v188, v70, s53, v174
	v_fma_f32 v189, v71, s53, v174
	v_fma_f32 v190, v76, s53, v174
	v_fma_f32 v191, v77, s53, v174
	v_fma_f32 v192, v78, s53, v174
	v_fma_f32 v193, v79, s53, v174
	v_exp_f32_e32 v178, v178
	v_exp_f32_e32 v179, v179
	v_exp_f32_e32 v180, v180
	v_exp_f32_e32 v181, v181
	v_exp_f32_e32 v182, v182
	v_exp_f32_e32 v183, v183
	v_exp_f32_e32 v184, v184
	v_exp_f32_e32 v185, v185
	v_exp_f32_e32 v186, v186
	v_exp_f32_e32 v187, v187
	v_exp_f32_e32 v188, v188
	v_exp_f32_e32 v189, v189
	v_exp_f32_e32 v190, v190
	v_exp_f32_e32 v191, v191
	v_exp_f32_e32 v192, v192
	v_exp_f32_e32 v193, v193
	v_add_f32_e32 v178, 1.0, v178
	v_add_f32_e32 v179, 1.0, v179
	v_add_f32_e32 v180, 1.0, v180
	v_add_f32_e32 v181, 1.0, v181
	v_add_f32_e32 v182, 1.0, v182
	v_add_f32_e32 v183, 1.0, v183
	v_add_f32_e32 v184, 1.0, v184
	v_add_f32_e32 v185, 1.0, v185
	v_add_f32_e32 v186, 1.0, v186
	v_add_f32_e32 v187, 1.0, v187
	v_add_f32_e32 v188, 1.0, v188
	v_add_f32_e32 v189, 1.0, v189
	v_add_f32_e32 v190, 1.0, v190
	v_add_f32_e32 v191, 1.0, v191
	v_add_f32_e32 v192, 1.0, v192
	v_add_f32_e32 v193, 1.0, v193
	v_rcp_f32_e32 v178, v178
	v_rcp_f32_e32 v179, v179
	v_rcp_f32_e32 v180, v180
	v_rcp_f32_e32 v181, v181
	v_rcp_f32_e32 v182, v182
	v_rcp_f32_e32 v183, v183
	v_rcp_f32_e32 v184, v184
	v_rcp_f32_e32 v185, v185
	v_rcp_f32_e32 v186, v186
	v_rcp_f32_e32 v187, v187
	v_rcp_f32_e32 v188, v188
	v_rcp_f32_e32 v189, v189
	v_rcp_f32_e32 v190, v190
	v_rcp_f32_e32 v191, v191
	v_rcp_f32_e32 v192, v192
	v_rcp_f32_e32 v193, v193
	v_mul_f32_e32 v178, v175, v178
	v_mul_f32_e32 v179, v175, v179
	v_mul_f32_e32 v180, v175, v180
	v_mul_f32_e32 v181, v175, v181
	v_mul_f32_e32 v182, v175, v182
	v_mul_f32_e32 v183, v175, v183
	v_mul_f32_e32 v184, v175, v184
	v_mul_f32_e32 v185, v175, v185
	v_exp_f32_e32 v96, v178
	v_exp_f32_e32 v97, v179
	v_exp_f32_e32 v98, v180
	v_exp_f32_e32 v99, v181
	v_exp_f32_e32 v100, v182
	v_exp_f32_e32 v101, v183
	v_exp_f32_e32 v102, v184
	v_exp_f32_e32 v103, v185
	s_nop 0
	v_fma_f32 v194, -v96, v96, 1.0
	v_fma_f32 v195, -v97, v97, 1.0
	v_fma_f32 v196, -v98, v98, 1.0
	v_fma_f32 v197, -v99, v99, 1.0
	v_fma_f32 v198, -v100, v100, 1.0
	v_fma_f32 v199, -v101, v101, 1.0
	v_fma_f32 v200, -v102, v102, 1.0
	v_fma_f32 v201, -v103, v103, 1.0
	v_max_f32_e32 v194, 0, v194
	v_max_f32_e32 v195, 0, v195
	v_max_f32_e32 v196, 0, v196
	v_max_f32_e32 v197, 0, v197
	v_max_f32_e32 v198, 0, v198
	v_max_f32_e32 v199, 0, v199
	v_max_f32_e32 v200, 0, v200
	v_max_f32_e32 v201, 0, v201
	v_sqrt_f32_e32 v194, v194
	v_sqrt_f32_e32 v195, v195
	v_sqrt_f32_e32 v196, v196
	v_sqrt_f32_e32 v197, v197
	v_sqrt_f32_e32 v198, v198
	v_sqrt_f32_e32 v199, v199
	v_sqrt_f32_e32 v200, v200
	v_sqrt_f32_e32 v201, v201
	s_waitcnt lgkmcnt(8)
	v_lshlrev_b32_e32 v144, 16, v144
	v_lshlrev_b32_e32 v145, 16, v145
	v_lshlrev_b32_e32 v146, 16, v146
	v_lshlrev_b32_e32 v147, 16, v147
	v_lshlrev_b32_e32 v148, 16, v148
	v_lshlrev_b32_e32 v149, 16, v149
	v_lshlrev_b32_e32 v150, 16, v150
	v_lshlrev_b32_e32 v151, 16, v151
	v_mul_f32_e32 v194, v194, v186
	v_mul_f32_e32 v195, v195, v187
	v_mul_f32_e32 v196, v196, v188
	v_mul_f32_e32 v197, v197, v189
	v_mul_f32_e32 v198, v198, v190
	v_mul_f32_e32 v199, v199, v191
	v_mul_f32_e32 v200, v200, v192
	v_mul_f32_e32 v201, v201, v193
	v_mul_f32_e32 v144, v194, v144
	v_mul_f32_e32 v145, v195, v145
	v_mul_f32_e32 v146, v196, v146
	v_mul_f32_e32 v147, v197, v147
	v_mul_f32_e32 v148, v198, v148
	v_mul_f32_e32 v149, v199, v149
	v_mul_f32_e32 v150, v200, v150
	v_mul_f32_e32 v151, v201, v151
	v_fma_f32 v178, v80, s53, v173
	v_fma_f32 v179, v81, s53, v173
	v_fma_f32 v180, v82, s53, v173
	v_fma_f32 v181, v83, s53, v173
	v_fma_f32 v182, v88, s53, v173
	v_fma_f32 v183, v89, s53, v173
	v_fma_f32 v184, v90, s53, v173
	v_fma_f32 v185, v91, s53, v173
	v_fma_f32 v186, v84, s53, v174
	v_fma_f32 v187, v85, s53, v174
	v_fma_f32 v188, v86, s53, v174
	v_fma_f32 v189, v87, s53, v174
	v_fma_f32 v190, v92, s53, v174
	v_fma_f32 v191, v93, s53, v174
	v_fma_f32 v192, v94, s53, v174
	v_fma_f32 v193, v95, s53, v174
	v_exp_f32_e32 v178, v178
	v_exp_f32_e32 v179, v179
	v_exp_f32_e32 v180, v180
	v_exp_f32_e32 v181, v181
	v_exp_f32_e32 v182, v182
	v_exp_f32_e32 v183, v183
	v_exp_f32_e32 v184, v184
	v_exp_f32_e32 v185, v185
	v_exp_f32_e32 v186, v186
	v_exp_f32_e32 v187, v187
	v_exp_f32_e32 v188, v188
	v_exp_f32_e32 v189, v189
	v_exp_f32_e32 v190, v190
	v_exp_f32_e32 v191, v191
	v_exp_f32_e32 v192, v192
	v_exp_f32_e32 v193, v193
	v_add_f32_e32 v178, 1.0, v178
	v_add_f32_e32 v179, 1.0, v179
	v_add_f32_e32 v180, 1.0, v180
	v_add_f32_e32 v181, 1.0, v181
	v_add_f32_e32 v182, 1.0, v182
	v_add_f32_e32 v183, 1.0, v183
	v_add_f32_e32 v184, 1.0, v184
	v_add_f32_e32 v185, 1.0, v185
	v_add_f32_e32 v186, 1.0, v186
	v_add_f32_e32 v187, 1.0, v187
	v_add_f32_e32 v188, 1.0, v188
	v_add_f32_e32 v189, 1.0, v189
	v_add_f32_e32 v190, 1.0, v190
	v_add_f32_e32 v191, 1.0, v191
	v_add_f32_e32 v192, 1.0, v192
	v_add_f32_e32 v193, 1.0, v193
	v_rcp_f32_e32 v178, v178
	v_rcp_f32_e32 v179, v179
	v_rcp_f32_e32 v180, v180
	v_rcp_f32_e32 v181, v181
	v_rcp_f32_e32 v182, v182
	v_rcp_f32_e32 v183, v183
	v_rcp_f32_e32 v184, v184
	v_rcp_f32_e32 v185, v185
	v_rcp_f32_e32 v186, v186
	v_rcp_f32_e32 v187, v187
	v_rcp_f32_e32 v188, v188
	v_rcp_f32_e32 v189, v189
	v_rcp_f32_e32 v190, v190
	v_rcp_f32_e32 v191, v191
	v_rcp_f32_e32 v192, v192
	v_rcp_f32_e32 v193, v193
	v_mul_f32_e32 v178, v175, v178
	v_mul_f32_e32 v179, v175, v179
	v_mul_f32_e32 v180, v175, v180
	v_mul_f32_e32 v181, v175, v181
	v_mul_f32_e32 v182, v175, v182
	v_mul_f32_e32 v183, v175, v183
	v_mul_f32_e32 v184, v175, v184
	v_mul_f32_e32 v185, v175, v185
	v_exp_f32_e32 v104, v178
	v_exp_f32_e32 v105, v179
	v_exp_f32_e32 v106, v180
	v_exp_f32_e32 v107, v181
	v_exp_f32_e32 v108, v182
	v_exp_f32_e32 v109, v183
	v_exp_f32_e32 v110, v184
	v_exp_f32_e32 v111, v185
	s_nop 0
	v_fma_f32 v194, -v104, v104, 1.0
	v_fma_f32 v195, -v105, v105, 1.0
	v_fma_f32 v196, -v106, v106, 1.0
	v_fma_f32 v197, -v107, v107, 1.0
	v_fma_f32 v198, -v108, v108, 1.0
	v_fma_f32 v199, -v109, v109, 1.0
	v_fma_f32 v200, -v110, v110, 1.0
	v_fma_f32 v201, -v111, v111, 1.0
	v_max_f32_e32 v194, 0, v194
	v_max_f32_e32 v195, 0, v195
	v_max_f32_e32 v196, 0, v196
	v_max_f32_e32 v197, 0, v197
	v_max_f32_e32 v198, 0, v198
	v_max_f32_e32 v199, 0, v199
	v_max_f32_e32 v200, 0, v200
	v_max_f32_e32 v201, 0, v201
	v_sqrt_f32_e32 v194, v194
	v_sqrt_f32_e32 v195, v195
	v_sqrt_f32_e32 v196, v196
	v_sqrt_f32_e32 v197, v197
	v_sqrt_f32_e32 v198, v198
	v_sqrt_f32_e32 v199, v199
	v_sqrt_f32_e32 v200, v200
	v_sqrt_f32_e32 v201, v201
	s_waitcnt lgkmcnt(0)
	v_lshlrev_b32_e32 v152, 16, v152
	v_lshlrev_b32_e32 v153, 16, v153
	v_lshlrev_b32_e32 v154, 16, v154
	v_lshlrev_b32_e32 v155, 16, v155
	v_lshlrev_b32_e32 v156, 16, v156
	v_lshlrev_b32_e32 v157, 16, v157
	v_lshlrev_b32_e32 v158, 16, v158
	v_lshlrev_b32_e32 v159, 16, v159
	v_mul_f32_e32 v194, v194, v186
	v_mul_f32_e32 v195, v195, v187
	v_mul_f32_e32 v196, v196, v188
	v_mul_f32_e32 v197, v197, v189
	v_mul_f32_e32 v198, v198, v190
	v_mul_f32_e32 v199, v199, v191
	v_mul_f32_e32 v200, v200, v192
	v_mul_f32_e32 v201, v201, v193
	v_mul_f32_e32 v152, v194, v152
	v_mul_f32_e32 v153, v195, v153
	v_mul_f32_e32 v154, v196, v154
	v_mul_f32_e32 v155, v197, v155
	v_mul_f32_e32 v156, v198, v156
	v_mul_f32_e32 v157, v199, v157
	v_mul_f32_e32 v158, v200, v158
	v_mul_f32_e32 v159, v201, v159
	v_fma_f32 v146, v98, v147, v146
	v_fma_f32 v150, v102, v151, v150
	v_fma_f32 v154, v106, v155, v154
	v_fma_f32 v158, v110, v159, v158
	v_mul_f32_e32 v98, v98, v99
	v_mul_f32_e32 v102, v102, v103
	v_mul_f32_e32 v106, v106, v107
	v_mul_f32_e32 v110, v110, v111
	v_fma_f32 v145, v97, v146, v145
	v_fma_f32 v149, v101, v150, v149
	v_fma_f32 v153, v105, v154, v153
	v_fma_f32 v157, v109, v158, v157
	v_mul_f32_e32 v97, v97, v98
	v_mul_f32_e32 v101, v101, v102
	v_mul_f32_e32 v105, v105, v106
	v_mul_f32_e32 v109, v109, v110
	v_fma_f32 v144, v96, v145, v144
	v_fma_f32 v148, v100, v149, v148
	v_fma_f32 v152, v104, v153, v152
	v_fma_f32 v156, v108, v157, v156
	v_mul_f32_e32 v96, v96, v97
	v_mul_f32_e32 v100, v100, v101
	v_mul_f32_e32 v104, v104, v105
	v_mul_f32_e32 v108, v108, v109
	ds_bpermute_b32 v178, v204, v96
	ds_bpermute_b32 v182, v204, v144
	ds_bpermute_b32 v179, v204, v100
	ds_bpermute_b32 v183, v204, v148
	ds_bpermute_b32 v180, v204, v104
	ds_bpermute_b32 v184, v204, v152
	ds_bpermute_b32 v181, v204, v108
	ds_bpermute_b32 v185, v204, v156
	s_waitcnt lgkmcnt(0)
	v_fma_f32 v186, v182, v96, v144
	v_cndmask_b32_e64 v178, 1.0, v178, s[34:35]
	v_fma_f32 v187, v183, v100, v148
	v_cndmask_b32_e64 v179, 1.0, v179, s[34:35]
	v_fma_f32 v188, v184, v104, v152
	v_cndmask_b32_e64 v180, 1.0, v180, s[34:35]
	v_fma_f32 v189, v185, v108, v156
	v_cndmask_b32_e64 v181, 1.0, v181, s[34:35]
	v_cndmask_b32_e64 v223, v144, v186, s[34:35]
	v_mul_f32_e32 v219, v96, v178
	v_cndmask_b32_e64 v224, v148, v187, s[34:35]
	v_mul_f32_e32 v220, v100, v179
	v_cndmask_b32_e64 v225, v152, v188, s[34:35]
	v_mul_f32_e32 v221, v104, v180
	v_cndmask_b32_e64 v226, v156, v189, s[34:35]
	v_mul_f32_e32 v222, v108, v181
	ds_bpermute_b32 v178, v205, v219
	ds_bpermute_b32 v182, v205, v223
	ds_bpermute_b32 v179, v205, v220
	ds_bpermute_b32 v183, v205, v224
	ds_bpermute_b32 v180, v205, v221
	ds_bpermute_b32 v184, v205, v225
	ds_bpermute_b32 v181, v205, v222
	ds_bpermute_b32 v185, v205, v226
	s_waitcnt lgkmcnt(0)
	v_fma_f32 v186, v182, v219, v223
	v_cndmask_b32_e64 v178, 1.0, v178, s[36:37]
	v_fma_f32 v187, v183, v220, v224
	v_cndmask_b32_e64 v179, 1.0, v179, s[36:37]
	v_fma_f32 v188, v184, v221, v225
	v_cndmask_b32_e64 v180, 1.0, v180, s[36:37]
	v_fma_f32 v189, v185, v222, v226
	v_cndmask_b32_e64 v181, 1.0, v181, s[36:37]
	v_cndmask_b32_e64 v223, v223, v186, s[36:37]
	v_mul_f32_e32 v219, v219, v178
	v_cndmask_b32_e64 v224, v224, v187, s[36:37]
	v_mul_f32_e32 v220, v220, v179
	v_cndmask_b32_e64 v225, v225, v188, s[36:37]
	v_mul_f32_e32 v221, v221, v180
	v_cndmask_b32_e64 v226, v226, v189, s[36:37]
	v_mul_f32_e32 v222, v222, v181
	ds_bpermute_b32 v227, v204, v219
	ds_bpermute_b32 v231, v204, v223
	ds_bpermute_b32 v235, v206, v219
	ds_bpermute_b32 v239, v206, v223
	ds_bpermute_b32 v228, v204, v220
	ds_bpermute_b32 v232, v204, v224
	ds_bpermute_b32 v236, v206, v220
	ds_bpermute_b32 v244, v206, v224
	ds_bpermute_b32 v229, v204, v221
	ds_bpermute_b32 v233, v204, v225
	ds_bpermute_b32 v237, v206, v221
	ds_bpermute_b32 v245, v206, v225
	ds_bpermute_b32 v230, v204, v222
	ds_bpermute_b32 v234, v204, v226
	ds_bpermute_b32 v238, v206, v222
	ds_bpermute_b32 v246, v206, v226
	s_waitcnt lgkmcnt(0)
	v_cndmask_b32_e64 v227, 1.0, v227, s[34:35]
	v_cndmask_b32_e64 v231, 0, v231, s[34:35]
	v_cndmask_b32_e64 v228, 1.0, v228, s[34:35]
	v_cndmask_b32_e64 v232, 0, v232, s[34:35]
	v_cndmask_b32_e64 v229, 1.0, v229, s[34:35]
	v_cndmask_b32_e64 v233, 0, v233, s[34:35]
	v_cndmask_b32_e64 v230, 1.0, v230, s[34:35]
	v_cndmask_b32_e64 v234, 0, v234, s[34:35]
	v_mov_b32_e32 v190, v238
	v_mov_b32_e32 v194, v246
	v_mov_b32_e32 v198, v190
	v_mov_b32_e32 v201, v194
	v_fma_f32 v194, v194, v237, v245
	v_mul_f32_e32 v190, v190, v237
	v_mov_b32_e32 v199, v190
	v_mov_b32_e32 v177, v194
	v_fma_f32 v194, v194, v236, v244
	v_mul_f32_e32 v190, v190, v236
	v_mov_b32_e32 v200, v190
	v_mov_b32_e32 v203, v194
	v_fma_f32 v194, v194, v235, v239
	v_mul_f32_e32 v190, v190, v235
	v_mov_b32_e32 v191, v194
	ds_write_b64 v207, v[190:191]
	s_waitcnt lgkmcnt(0)
	s_barrier
	ds_read_b64 v[178:179], v208 offset:512
	ds_read_b64 v[180:181], v208
	s_waitcnt lgkmcnt(0)
	v_fma_f32 v182, v176, v178, v179
	v_cndmask_b32_e64 v183, v176, v182, s[38:39]
	v_fma_f32 v176, v182, v180, v181
	v_fma_f32 v184, v183, v200, v203
	v_fma_f32 v185, v183, v199, v177
	v_fma_f32 v186, v183, v198, v201
	v_mov_b32_e32 v187, v183
	v_fma_f32 v184, v184, v227, v231
	v_fma_f32 v185, v185, v228, v232
	v_fma_f32 v186, v186, v229, v233
	v_fma_f32 v187, v187, v230, v234
	v_fma_f32 v144, v184, v96, v144
	v_fma_f32 v148, v185, v100, v148
	v_fma_f32 v152, v186, v104, v152
	v_fma_f32 v156, v187, v108, v156
	v_fma_f32 v145, v184, v97, v145
	v_fma_f32 v149, v185, v101, v149
	v_fma_f32 v153, v186, v105, v153
	v_fma_f32 v157, v187, v109, v157
	v_fma_f32 v146, v184, v98, v146
	v_fma_f32 v150, v185, v102, v150
	v_fma_f32 v154, v186, v106, v154
	v_fma_f32 v158, v187, v110, v158
	v_fma_f32 v147, v184, v99, v147
	v_fma_f32 v151, v185, v103, v151
	v_fma_f32 v155, v186, v107, v155
	v_fma_f32 v159, v187, v111, v159
	s_cmp_eq_u32 s13, 17
	s_cbranch_scc1 .Lmylru_w0_7
	s_waitcnt vmcnt(8)
	s_branch .Lmylru_w1_7

.Lmylru_w1_7:
	v_lshlrev_b32_e32 v178, 16, v247
	v_add_f32_e32 v144, v144, v178
	v_lshlrev_b32_e32 v128, 16, v128
	v_mul_f32_e32 v144, v144, v128
	v_cvt_pk_bf16_f32 v144, v144, v144
	v_and_b32_e32 v179, 0xffff0000, v247
	v_add_f32_e32 v145, v145, v179
	v_lshlrev_b32_e32 v129, 16, v129
	v_mul_f32_e32 v145, v145, v129
	v_cvt_pk_bf16_f32 v145, v145, v145
	v_lshlrev_b32_e32 v180, 16, v248
	v_add_f32_e32 v146, v146, v180
	v_lshlrev_b32_e32 v130, 16, v130
	v_mul_f32_e32 v146, v146, v130
	v_cvt_pk_bf16_f32 v146, v146, v146
	v_and_b32_e32 v181, 0xffff0000, v248
	v_add_f32_e32 v147, v147, v181
	v_lshlrev_b32_e32 v131, 16, v131
	v_mul_f32_e32 v147, v147, v131
	v_cvt_pk_bf16_f32 v147, v147, v147
	v_lshlrev_b32_e32 v178, 16, v249
	v_add_f32_e32 v148, v148, v178
	v_lshlrev_b32_e32 v132, 16, v132
	v_mul_f32_e32 v148, v148, v132
	v_cvt_pk_bf16_f32 v148, v148, v148
	v_and_b32_e32 v179, 0xffff0000, v249
	v_add_f32_e32 v149, v149, v179
	v_lshlrev_b32_e32 v133, 16, v133
	v_mul_f32_e32 v149, v149, v133
	v_cvt_pk_bf16_f32 v149, v149, v149
	v_lshlrev_b32_e32 v180, 16, v250
	v_add_f32_e32 v150, v150, v180
	v_lshlrev_b32_e32 v134, 16, v134
	v_mul_f32_e32 v150, v150, v134
	v_cvt_pk_bf16_f32 v150, v150, v150
	v_and_b32_e32 v181, 0xffff0000, v250
	v_add_f32_e32 v151, v151, v181
	v_lshlrev_b32_e32 v135, 16, v135
	v_mul_f32_e32 v151, v151, v135
	v_cvt_pk_bf16_f32 v151, v151, v151
	v_lshlrev_b32_e32 v178, 16, v251
	v_add_f32_e32 v152, v152, v178
	v_lshlrev_b32_e32 v136, 16, v136
	v_mul_f32_e32 v152, v152, v136
	v_cvt_pk_bf16_f32 v152, v152, v152
	v_and_b32_e32 v179, 0xffff0000, v251
	v_add_f32_e32 v153, v153, v179
	v_lshlrev_b32_e32 v137, 16, v137
	v_mul_f32_e32 v153, v153, v137
	v_cvt_pk_bf16_f32 v153, v153, v153
	v_lshlrev_b32_e32 v180, 16, v252
	v_add_f32_e32 v154, v154, v180
	v_lshlrev_b32_e32 v138, 16, v138
	v_mul_f32_e32 v154, v154, v138
	v_cvt_pk_bf16_f32 v154, v154, v154
	v_and_b32_e32 v181, 0xffff0000, v252
	v_add_f32_e32 v155, v155, v181
	v_lshlrev_b32_e32 v139, 16, v139
	v_mul_f32_e32 v155, v155, v139
	v_cvt_pk_bf16_f32 v155, v155, v155
	v_lshlrev_b32_e32 v178, 16, v253
	v_add_f32_e32 v156, v156, v178
	v_lshlrev_b32_e32 v140, 16, v140
	v_mul_f32_e32 v156, v156, v140
	v_cvt_pk_bf16_f32 v156, v156, v156
	v_and_b32_e32 v179, 0xffff0000, v253
	v_add_f32_e32 v157, v157, v179
	v_lshlrev_b32_e32 v141, 16, v141
	v_mul_f32_e32 v157, v157, v141
	v_cvt_pk_bf16_f32 v157, v157, v157
	v_lshlrev_b32_e32 v180, 16, v254
	v_add_f32_e32 v158, v158, v180
	v_lshlrev_b32_e32 v142, 16, v142
	v_mul_f32_e32 v158, v158, v142
	v_cvt_pk_bf16_f32 v158, v158, v158
	v_and_b32_e32 v181, 0xffff0000, v254
	v_add_f32_e32 v159, v159, v181
	v_lshlrev_b32_e32 v143, 16, v143
	v_mul_f32_e32 v159, v159, v143
	v_cvt_pk_bf16_f32 v159, v159, v159
	ds_write_b16 v169, v144
	ds_write_b16 v169, v145 offset:128
	ds_write_b16 v169, v146 offset:256
	ds_write_b16 v169, v147 offset:384
	ds_write_b16 v169, v148 offset:2048
	ds_write_b16 v169, v149 offset:2176
	ds_write_b16 v169, v150 offset:2304
	ds_write_b16 v169, v151 offset:2432
	ds_write_b16 v169, v152 offset:4096
	ds_write_b16 v169, v153 offset:4224
	ds_write_b16 v169, v154 offset:4352
	ds_write_b16 v169, v155 offset:4480
	ds_write_b16 v169, v156 offset:6144
	ds_write_b16 v169, v157 offset:6272
	ds_write_b16 v169, v158 offset:6400
	ds_write_b16 v169, v159 offset:6528
	s_mov_b64 s[62:63], s[42:43]
	s_add_i32 s13, s13, 1
	s_waitcnt vmcnt(0)
	s_barrier
	s_cmp_eq_u32 s13, 2
	s_cbranch_scc1 .Lmylru_nf_8
	ds_read_b128 v[178:181], v170
	ds_read_b128 v[182:185], v170 offset:1024
	s_waitcnt lgkmcnt(0)
	global_store_dwordx4 v171, v[178:181], s[62:63]
	global_store_dwordx4 v172, v[182:185], s[62:63]
.Lmylru_nf_8:
	s_sub_i32 s54, 17, s13
	s_lshl_b32 s55, s54, 14
	s_lshl_b32 s56, s6, 11
	s_add_i32 s55, s55, s56
	s_add_u32 s44, s22, s55
	s_addc_u32 s45, s23, 0
	s_cmp_lt_u32 s13, 2
	s_sub_i32 s50, 1, s13
	s_lshl_b32 s50, s50, 7
	s_lshl_b32 s51, s9, 8
	s_add_i32 s51, s51, 0x8000
	s_add_i32 s51, s51, s50
	s_sub_i32 s50, 17, s13
	s_lshl_b32 s50, s50, 7
	s_lshl_b32 s57, s9, 11
	s_add_i32 s57, s57, s50
	s_cmp_lt_u32 s13, 2
	s_cselect_b32 s57, s51, s57
	s_lshl_b32 s57, s57, 11
	s_add_u32 s40, s18, s57
	s_addc_u32 s41, s19, 0
	s_add_u32 s42, s20, s57
	s_addc_u32 s43, s21, 0
	global_load_dword v247, v209, s[44:45]
	global_load_dword v248, v209, s[44:45] offset:256
	global_load_dword v249, v209, s[44:45] offset:512
	global_load_dword v250, v209, s[44:45] offset:768
	global_load_dword v251, v209, s[44:45] offset:1024
	global_load_dword v252, v209, s[44:45] offset:1280
	global_load_dword v253, v209, s[44:45] offset:1536
	global_load_dword v254, v209, s[44:45] offset:1792
	v_add_u32_e32 v182, 0x0, v210
	v_add_u32_e32 v183, 0x1000, v182
	global_load_ushort v128, v182, s[40:41]
	global_load_ushort v129, v182, s[40:41] offset:2048
	global_load_ushort v130, v183, s[40:41]
	global_load_ushort v131, v183, s[40:41] offset:2048
	v_add_u32_e32 v182, 0x8000, v210
	v_add_u32_e32 v183, 0x1000, v182
	global_load_ushort v132, v182, s[40:41]
	global_load_ushort v133, v182, s[40:41] offset:2048
	global_load_ushort v134, v183, s[40:41]
	global_load_ushort v135, v183, s[40:41] offset:2048
	v_add_u32_e32 v182, 0x10000, v210
	v_add_u32_e32 v183, 0x1000, v182
	global_load_ushort v136, v182, s[40:41]
	global_load_ushort v137, v182, s[40:41] offset:2048
	global_load_ushort v138, v183, s[40:41]
	global_load_ushort v139, v183, s[40:41] offset:2048
	v_add_u32_e32 v182, 0x18000, v210
	v_add_u32_e32 v183, 0x1000, v182
	global_load_ushort v140, v182, s[40:41]
	global_load_ushort v141, v182, s[40:41] offset:2048
	global_load_ushort v142, v183, s[40:41]
	global_load_ushort v143, v183, s[40:41] offset:2048
	s_cmp_eq_u32 s13, 17
	s_cbranch_scc1 .Lmylru_nodma_8
	s_add_i32 s58, s13, 1
	s_cmp_lt_u32 s58, 2
	s_sub_i32 s50, 1, s58
	s_lshl_b32 s50, s50, 7
	s_lshl_b32 s51, s9, 8
	s_add_i32 s51, s51, 0x8000
	s_add_i32 s51, s51, s50
	s_sub_i32 s50, 17, s58
	s_lshl_b32 s50, s50, 7
	s_lshl_b32 s59, s9, 11
	s_add_i32 s59, s59, s50
	s_cmp_lt_u32 s58, 2
	s_cselect_b32 s59, s51, s59
	s_lshl_b32 s52, s59, 11
	s_add_u32 s46, s16, s52
	s_addc_u32 s47, s17, 0
	s_lshl_b32 s52, s6, 13
	s_mov_b32 m0, s52
	s_add_i32 s52, s52, 0x400
	global_load_lds_dwordx4 v211, s[46:47]
	s_mov_b32 m0, s52
	s_add_i32 s52, s52, 0x400
	global_load_lds_dwordx4 v212, s[46:47]
	s_mov_b32 m0, s52
	s_add_i32 s52, s52, 0x400
	global_load_lds_dwordx4 v213, s[46:47]
	s_mov_b32 m0, s52
	s_add_i32 s52, s52, 0x400
	global_load_lds_dwordx4 v214, s[46:47]
	s_mov_b32 m0, s52
	s_add_i32 s52, s52, 0x400
	global_load_lds_dwordx4 v215, s[46:47]
	s_mov_b32 m0, s52
	s_add_i32 s52, s52, 0x400
	global_load_lds_dwordx4 v216, s[46:47]
	s_mov_b32 m0, s52
	s_add_i32 s52, s52, 0x400
	global_load_lds_dwordx4 v217, s[46:47]
	s_mov_b32 m0, s52
	s_nop 0
	global_load_lds_dwordx4 v218, s[46:47]
.Lmylru_nodma_8:
	v_or_b32_e32 v163, 0x10000, v162
	ds_read_b128 v[96:99], v163
	ds_read_b128 v[100:103], v163 offset:8192
	ds_read_b128 v[104:107], v163 offset:16384
	ds_read_b128 v[108:111], v163 offset:24576
	v_xor_b32_e32 v164, 0x40, v163
	ds_read_b128 v[112:115], v164
	ds_read_b128 v[116:119], v164 offset:8192
	ds_read_b128 v[120:123], v164 offset:16384
	ds_read_b128 v[124:127], v164 offset:24576
	s_waitcnt lgkmcnt(7)
	v_mfma_f32_16x16x32_bf16 v[64:67], v[96:99], v[0:3], 0
	v_mfma_f32_16x16x32_bf16 v[68:71], v[96:99], v[32:35], 0
	v_xor_b32_e32 v164, 0x80, v163
	ds_read_b128 v[96:99], v164
	s_waitcnt lgkmcnt(7)
	v_mfma_f32_16x16x32_bf16 v[72:75], v[100:103], v[0:3], 0
	v_mfma_f32_16x16x32_bf16 v[76:79], v[100:103], v[32:35], 0
	ds_read_b128 v[100:103], v164 offset:8192
	s_waitcnt lgkmcnt(7)
	v_mfma_f32_16x16x32_bf16 v[80:83], v[104:107], v[0:3], 0
	v_mfma_f32_16x16x32_bf16 v[84:87], v[104:107], v[32:35], 0
	ds_read_b128 v[104:107], v164 offset:16384
	s_waitcnt lgkmcnt(7)
	v_mfma_f32_16x16x32_bf16 v[88:91], v[108:111], v[0:3], 0
	v_mfma_f32_16x16x32_bf16 v[92:95], v[108:111], v[32:35], 0
	ds_read_b128 v[108:111], v164 offset:24576
	s_waitcnt lgkmcnt(7)
	v_mfma_f32_16x16x32_bf16 v[64:67], v[112:115], v[4:7], v[64:67]
	v_mfma_f32_16x16x32_bf16 v[68:71], v[112:115], v[36:39], v[68:71]
	v_xor_b32_e32 v164, 0xc0, v163
	ds_read_b128 v[112:115], v164
	s_waitcnt lgkmcnt(7)
	v_mfma_f32_16x16x32_bf16 v[72:75], v[116:119], v[4:7], v[72:75]
	v_mfma_f32_16x16x32_bf16 v[76:79], v[116:119], v[36:39], v[76:79]
	ds_read_b128 v[116:119], v164 offset:8192
	s_waitcnt lgkmcnt(7)
	v_mfma_f32_16x16x32_bf16 v[80:83], v[120:123], v[4:7], v[80:83]
	v_mfma_f32_16x16x32_bf16 v[84:87], v[120:123], v[36:39], v[84:87]
	ds_read_b128 v[120:123], v164 offset:16384
	s_waitcnt lgkmcnt(7)
	v_mfma_f32_16x16x32_bf16 v[88:91], v[124:127], v[4:7], v[88:91]
	v_mfma_f32_16x16x32_bf16 v[92:95], v[124:127], v[36:39], v[92:95]
	ds_read_b128 v[124:127], v164 offset:24576
	s_waitcnt lgkmcnt(7)
	v_mfma_f32_16x16x32_bf16 v[64:67], v[96:99], v[8:11], v[64:67]
	v_mfma_f32_16x16x32_bf16 v[68:71], v[96:99], v[40:43], v[68:71]
	v_xor_b32_e32 v164, 0x100, v163
	ds_read_b128 v[96:99], v164
	s_waitcnt lgkmcnt(7)
	v_mfma_f32_16x16x32_bf16 v[72:75], v[100:103], v[8:11], v[72:75]
	v_mfma_f32_16x16x32_bf16 v[76:79], v[100:103], v[40:43], v[76:79]
	ds_read_b128 v[100:103], v164 offset:8192
	s_waitcnt lgkmcnt(7)
	v_mfma_f32_16x16x32_bf16 v[80:83], v[104:107], v[8:11], v[80:83]
	v_mfma_f32_16x16x32_bf16 v[84:87], v[104:107], v[40:43], v[84:87]
	ds_read_b128 v[104:107], v164 offset:16384
	s_waitcnt lgkmcnt(7)
	v_mfma_f32_16x16x32_bf16 v[88:91], v[108:111], v[8:11], v[88:91]
	v_mfma_f32_16x16x32_bf16 v[92:95], v[108:111], v[40:43], v[92:95]
	ds_read_b128 v[108:111], v164 offset:24576
	s_waitcnt lgkmcnt(7)
	v_mfma_f32_16x16x32_bf16 v[64:67], v[112:115], v[12:15], v[64:67]
	v_mfma_f32_16x16x32_bf16 v[68:71], v[112:115], v[44:47], v[68:71]
	v_xor_b32_e32 v164, 0x140, v163
	ds_read_b128 v[112:115], v164
	s_waitcnt lgkmcnt(7)
	v_mfma_f32_16x16x32_bf16 v[72:75], v[116:119], v[12:15], v[72:75]
	v_mfma_f32_16x16x32_bf16 v[76:79], v[116:119], v[44:47], v[76:79]
	ds_read_b128 v[116:119], v164 offset:8192
	s_waitcnt lgkmcnt(7)
	v_mfma_f32_16x16x32_bf16 v[80:83], v[120:123], v[12:15], v[80:83]
	v_mfma_f32_16x16x32_bf16 v[84:87], v[120:123], v[44:47], v[84:87]
	ds_read_b128 v[120:123], v164 offset:16384
	s_waitcnt lgkmcnt(7)
	v_mfma_f32_16x16x32_bf16 v[88:91], v[124:127], v[12:15], v[88:91]
	v_mfma_f32_16x16x32_bf16 v[92:95], v[124:127], v[44:47], v[92:95]
	ds_read_b128 v[124:127], v164 offset:24576
	s_waitcnt lgkmcnt(7)
	v_mfma_f32_16x16x32_bf16 v[64:67], v[96:99], v[16:19], v[64:67]
	v_mfma_f32_16x16x32_bf16 v[68:71], v[96:99], v[48:51], v[68:71]
	v_xor_b32_e32 v164, 0x180, v163
	ds_read_b128 v[96:99], v164
	s_waitcnt lgkmcnt(7)
	v_mfma_f32_16x16x32_bf16 v[72:75], v[100:103], v[16:19], v[72:75]
	v_mfma_f32_16x16x32_bf16 v[76:79], v[100:103], v[48:51], v[76:79]
	ds_read_b128 v[100:103], v164 offset:8192
	s_waitcnt lgkmcnt(7)
	v_mfma_f32_16x16x32_bf16 v[80:83], v[104:107], v[16:19], v[80:83]
	v_mfma_f32_16x16x32_bf16 v[84:87], v[104:107], v[48:51], v[84:87]
	ds_read_b128 v[104:107], v164 offset:16384
	s_waitcnt lgkmcnt(7)
	v_mfma_f32_16x16x32_bf16 v[88:91], v[108:111], v[16:19], v[88:91]
	v_mfma_f32_16x16x32_bf16 v[92:95], v[108:111], v[48:51], v[92:95]
	ds_read_b128 v[108:111], v164 offset:24576
	s_waitcnt lgkmcnt(7)
	v_mfma_f32_16x16x32_bf16 v[64:67], v[112:115], v[20:23], v[64:67]
	v_mfma_f32_16x16x32_bf16 v[68:71], v[112:115], v[52:55], v[68:71]
	v_xor_b32_e32 v164, 0x1c0, v163
	ds_read_b128 v[112:115], v164
	s_waitcnt lgkmcnt(7)
	v_mfma_f32_16x16x32_bf16 v[72:75], v[116:119], v[20:23], v[72:75]
	v_mfma_f32_16x16x32_bf16 v[76:79], v[116:119], v[52:55], v[76:79]
	ds_read_b128 v[116:119], v164 offset:8192
	s_waitcnt lgkmcnt(7)
	v_mfma_f32_16x16x32_bf16 v[80:83], v[120:123], v[20:23], v[80:83]
	v_mfma_f32_16x16x32_bf16 v[84:87], v[120:123], v[52:55], v[84:87]
	ds_read_b128 v[120:123], v164 offset:16384
	s_waitcnt lgkmcnt(7)
	v_mfma_f32_16x16x32_bf16 v[88:91], v[124:127], v[20:23], v[88:91]
	v_mfma_f32_16x16x32_bf16 v[92:95], v[124:127], v[52:55], v[92:95]
	ds_read_b128 v[124:127], v164 offset:24576
	s_waitcnt lgkmcnt(7)
	v_mfma_f32_16x16x32_bf16 v[64:67], v[96:99], v[24:27], v[64:67]
	v_mfma_f32_16x16x32_bf16 v[68:71], v[96:99], v[56:59], v[68:71]
	s_waitcnt lgkmcnt(6)
	v_mfma_f32_16x16x32_bf16 v[72:75], v[100:103], v[24:27], v[72:75]
	v_mfma_f32_16x16x32_bf16 v[76:79], v[100:103], v[56:59], v[76:79]
	s_waitcnt lgkmcnt(5)
	v_mfma_f32_16x16x32_bf16 v[80:83], v[104:107], v[24:27], v[80:83]
	v_mfma_f32_16x16x32_bf16 v[84:87], v[104:107], v[56:59], v[84:87]
	s_waitcnt lgkmcnt(4)
	v_mfma_f32_16x16x32_bf16 v[88:91], v[108:111], v[24:27], v[88:91]
	v_mfma_f32_16x16x32_bf16 v[92:95], v[108:111], v[56:59], v[92:95]
	s_waitcnt lgkmcnt(3)
	v_mfma_f32_16x16x32_bf16 v[64:67], v[112:115], v[28:31], v[64:67]
	v_mfma_f32_16x16x32_bf16 v[68:71], v[112:115], v[60:63], v[68:71]
	s_waitcnt lgkmcnt(2)
	v_mfma_f32_16x16x32_bf16 v[72:75], v[116:119], v[28:31], v[72:75]
	v_mfma_f32_16x16x32_bf16 v[76:79], v[116:119], v[60:63], v[76:79]
	s_waitcnt lgkmcnt(1)
	v_mfma_f32_16x16x32_bf16 v[80:83], v[120:123], v[28:31], v[80:83]
	v_mfma_f32_16x16x32_bf16 v[84:87], v[120:123], v[60:63], v[84:87]
	s_waitcnt lgkmcnt(0)
	v_mfma_f32_16x16x32_bf16 v[88:91], v[124:127], v[28:31], v[88:91]
	v_mfma_f32_16x16x32_bf16 v[92:95], v[124:127], v[60:63], v[92:95]
	v_or_b32_e32 v198, 0x10000, v165
	v_or_b32_e32 v199, 0x10000, v166
	v_or_b32_e32 v200, 0x10000, v167
	v_or_b32_e32 v201, 0x10000, v168
	ds_read_u16 v144, v198
	ds_read_u16 v145, v199
	ds_read_u16 v146, v200
	ds_read_u16 v147, v201
	ds_read_u16 v148, v198 offset:8192
	ds_read_u16 v149, v199 offset:8192
	ds_read_u16 v150, v200 offset:8192
	ds_read_u16 v151, v201 offset:8192
	ds_read_u16 v152, v198 offset:16384
	ds_read_u16 v153, v199 offset:16384
	ds_read_u16 v154, v200 offset:16384
	ds_read_u16 v155, v201 offset:16384
	ds_read_u16 v156, v198 offset:24576
	ds_read_u16 v157, v199 offset:24576
	ds_read_u16 v158, v200 offset:24576
	ds_read_u16 v159, v201 offset:24576
	s_nop 7
	v_fma_f32 v178, v64, s53, v173
	v_fma_f32 v179, v65, s53, v173
	v_fma_f32 v180, v66, s53, v173
	v_fma_f32 v181, v67, s53, v173
	v_fma_f32 v182, v72, s53, v173
	v_fma_f32 v183, v73, s53, v173
	v_fma_f32 v184, v74, s53, v173
	v_fma_f32 v185, v75, s53, v173
	v_fma_f32 v186, v68, s53, v174
	v_fma_f32 v187, v69, s53, v174
	v_fma_f32 v188, v70, s53, v174
	v_fma_f32 v189, v71, s53, v174
	v_fma_f32 v190, v76, s53, v174
	v_fma_f32 v191, v77, s53, v174
	v_fma_f32 v192, v78, s53, v174
	v_fma_f32 v193, v79, s53, v174
	v_exp_f32_e32 v178, v178
	v_exp_f32_e32 v179, v179
	v_exp_f32_e32 v180, v180
	v_exp_f32_e32 v181, v181
	v_exp_f32_e32 v182, v182
	v_exp_f32_e32 v183, v183
	v_exp_f32_e32 v184, v184
	v_exp_f32_e32 v185, v185
	v_exp_f32_e32 v186, v186
	v_exp_f32_e32 v187, v187
	v_exp_f32_e32 v188, v188
	v_exp_f32_e32 v189, v189
	v_exp_f32_e32 v190, v190
	v_exp_f32_e32 v191, v191
	v_exp_f32_e32 v192, v192
	v_exp_f32_e32 v193, v193
	v_add_f32_e32 v178, 1.0, v178
	v_add_f32_e32 v179, 1.0, v179
	v_add_f32_e32 v180, 1.0, v180
	v_add_f32_e32 v181, 1.0, v181
	v_add_f32_e32 v182, 1.0, v182
	v_add_f32_e32 v183, 1.0, v183
	v_add_f32_e32 v184, 1.0, v184
	v_add_f32_e32 v185, 1.0, v185
	v_add_f32_e32 v186, 1.0, v186
	v_add_f32_e32 v187, 1.0, v187
	v_add_f32_e32 v188, 1.0, v188
	v_add_f32_e32 v189, 1.0, v189
	v_add_f32_e32 v190, 1.0, v190
	v_add_f32_e32 v191, 1.0, v191
	v_add_f32_e32 v192, 1.0, v192
	v_add_f32_e32 v193, 1.0, v193
	v_rcp_f32_e32 v178, v178
	v_rcp_f32_e32 v179, v179
	v_rcp_f32_e32 v180, v180
	v_rcp_f32_e32 v181, v181
	v_rcp_f32_e32 v182, v182
	v_rcp_f32_e32 v183, v183
	v_rcp_f32_e32 v184, v184
	v_rcp_f32_e32 v185, v185
	v_rcp_f32_e32 v186, v186
	v_rcp_f32_e32 v187, v187
	v_rcp_f32_e32 v188, v188
	v_rcp_f32_e32 v189, v189
	v_rcp_f32_e32 v190, v190
	v_rcp_f32_e32 v191, v191
	v_rcp_f32_e32 v192, v192
	v_rcp_f32_e32 v193, v193
	v_mul_f32_e32 v178, v175, v178
	v_mul_f32_e32 v179, v175, v179
	v_mul_f32_e32 v180, v175, v180
	v_mul_f32_e32 v181, v175, v181
	v_mul_f32_e32 v182, v175, v182
	v_mul_f32_e32 v183, v175, v183
	v_mul_f32_e32 v184, v175, v184
	v_mul_f32_e32 v185, v175, v185
	v_exp_f32_e32 v96, v178
	v_exp_f32_e32 v97, v179
	v_exp_f32_e32 v98, v180
	v_exp_f32_e32 v99, v181
	v_exp_f32_e32 v100, v182
	v_exp_f32_e32 v101, v183
	v_exp_f32_e32 v102, v184
	v_exp_f32_e32 v103, v185
	s_nop 0
	v_fma_f32 v194, -v96, v96, 1.0
	v_fma_f32 v195, -v97, v97, 1.0
	v_fma_f32 v196, -v98, v98, 1.0
	v_fma_f32 v197, -v99, v99, 1.0
	v_fma_f32 v198, -v100, v100, 1.0
	v_fma_f32 v199, -v101, v101, 1.0
	v_fma_f32 v200, -v102, v102, 1.0
	v_fma_f32 v201, -v103, v103, 1.0
	v_max_f32_e32 v194, 0, v194
	v_max_f32_e32 v195, 0, v195
	v_max_f32_e32 v196, 0, v196
	v_max_f32_e32 v197, 0, v197
	v_max_f32_e32 v198, 0, v198
	v_max_f32_e32 v199, 0, v199
	v_max_f32_e32 v200, 0, v200
	v_max_f32_e32 v201, 0, v201
	v_sqrt_f32_e32 v194, v194
	v_sqrt_f32_e32 v195, v195
	v_sqrt_f32_e32 v196, v196
	v_sqrt_f32_e32 v197, v197
	v_sqrt_f32_e32 v198, v198
	v_sqrt_f32_e32 v199, v199
	v_sqrt_f32_e32 v200, v200
	v_sqrt_f32_e32 v201, v201
	s_waitcnt lgkmcnt(8)
	v_lshlrev_b32_e32 v144, 16, v144
	v_lshlrev_b32_e32 v145, 16, v145
	v_lshlrev_b32_e32 v146, 16, v146
	v_lshlrev_b32_e32 v147, 16, v147
	v_lshlrev_b32_e32 v148, 16, v148
	v_lshlrev_b32_e32 v149, 16, v149
	v_lshlrev_b32_e32 v150, 16, v150
	v_lshlrev_b32_e32 v151, 16, v151
	v_mul_f32_e32 v194, v194, v186
	v_mul_f32_e32 v195, v195, v187
	v_mul_f32_e32 v196, v196, v188
	v_mul_f32_e32 v197, v197, v189
	v_mul_f32_e32 v198, v198, v190
	v_mul_f32_e32 v199, v199, v191
	v_mul_f32_e32 v200, v200, v192
	v_mul_f32_e32 v201, v201, v193
	v_mul_f32_e32 v144, v194, v144
	v_mul_f32_e32 v145, v195, v145
	v_mul_f32_e32 v146, v196, v146
	v_mul_f32_e32 v147, v197, v147
	v_mul_f32_e32 v148, v198, v148
	v_mul_f32_e32 v149, v199, v149
	v_mul_f32_e32 v150, v200, v150
	v_mul_f32_e32 v151, v201, v151
	v_fma_f32 v178, v80, s53, v173
	v_fma_f32 v179, v81, s53, v173
	v_fma_f32 v180, v82, s53, v173
	v_fma_f32 v181, v83, s53, v173
	v_fma_f32 v182, v88, s53, v173
	v_fma_f32 v183, v89, s53, v173
	v_fma_f32 v184, v90, s53, v173
	v_fma_f32 v185, v91, s53, v173
	v_fma_f32 v186, v84, s53, v174
	v_fma_f32 v187, v85, s53, v174
	v_fma_f32 v188, v86, s53, v174
	v_fma_f32 v189, v87, s53, v174
	v_fma_f32 v190, v92, s53, v174
	v_fma_f32 v191, v93, s53, v174
	v_fma_f32 v192, v94, s53, v174
	v_fma_f32 v193, v95, s53, v174
	v_exp_f32_e32 v178, v178
	v_exp_f32_e32 v179, v179
	v_exp_f32_e32 v180, v180
	v_exp_f32_e32 v181, v181
	v_exp_f32_e32 v182, v182
	v_exp_f32_e32 v183, v183
	v_exp_f32_e32 v184, v184
	v_exp_f32_e32 v185, v185
	v_exp_f32_e32 v186, v186
	v_exp_f32_e32 v187, v187
	v_exp_f32_e32 v188, v188
	v_exp_f32_e32 v189, v189
	v_exp_f32_e32 v190, v190
	v_exp_f32_e32 v191, v191
	v_exp_f32_e32 v192, v192
	v_exp_f32_e32 v193, v193
	v_add_f32_e32 v178, 1.0, v178
	v_add_f32_e32 v179, 1.0, v179
	v_add_f32_e32 v180, 1.0, v180
	v_add_f32_e32 v181, 1.0, v181
	v_add_f32_e32 v182, 1.0, v182
	v_add_f32_e32 v183, 1.0, v183
	v_add_f32_e32 v184, 1.0, v184
	v_add_f32_e32 v185, 1.0, v185
	v_add_f32_e32 v186, 1.0, v186
	v_add_f32_e32 v187, 1.0, v187
	v_add_f32_e32 v188, 1.0, v188
	v_add_f32_e32 v189, 1.0, v189
	v_add_f32_e32 v190, 1.0, v190
	v_add_f32_e32 v191, 1.0, v191
	v_add_f32_e32 v192, 1.0, v192
	v_add_f32_e32 v193, 1.0, v193
	v_rcp_f32_e32 v178, v178
	v_rcp_f32_e32 v179, v179
	v_rcp_f32_e32 v180, v180
	v_rcp_f32_e32 v181, v181
	v_rcp_f32_e32 v182, v182
	v_rcp_f32_e32 v183, v183
	v_rcp_f32_e32 v184, v184
	v_rcp_f32_e32 v185, v185
	v_rcp_f32_e32 v186, v186
	v_rcp_f32_e32 v187, v187
	v_rcp_f32_e32 v188, v188
	v_rcp_f32_e32 v189, v189
	v_rcp_f32_e32 v190, v190
	v_rcp_f32_e32 v191, v191
	v_rcp_f32_e32 v192, v192
	v_rcp_f32_e32 v193, v193
	v_mul_f32_e32 v178, v175, v178
	v_mul_f32_e32 v179, v175, v179
	v_mul_f32_e32 v180, v175, v180
	v_mul_f32_e32 v181, v175, v181
	v_mul_f32_e32 v182, v175, v182
	v_mul_f32_e32 v183, v175, v183
	v_mul_f32_e32 v184, v175, v184
	v_mul_f32_e32 v185, v175, v185
	v_exp_f32_e32 v104, v178
	v_exp_f32_e32 v105, v179
	v_exp_f32_e32 v106, v180
	v_exp_f32_e32 v107, v181
	v_exp_f32_e32 v108, v182
	v_exp_f32_e32 v109, v183
	v_exp_f32_e32 v110, v184
	v_exp_f32_e32 v111, v185
	s_nop 0
	v_fma_f32 v194, -v104, v104, 1.0
	v_fma_f32 v195, -v105, v105, 1.0
	v_fma_f32 v196, -v106, v106, 1.0
	v_fma_f32 v197, -v107, v107, 1.0
	v_fma_f32 v198, -v108, v108, 1.0
	v_fma_f32 v199, -v109, v109, 1.0
	v_fma_f32 v200, -v110, v110, 1.0
	v_fma_f32 v201, -v111, v111, 1.0
	v_max_f32_e32 v194, 0, v194
	v_max_f32_e32 v195, 0, v195
	v_max_f32_e32 v196, 0, v196
	v_max_f32_e32 v197, 0, v197
	v_max_f32_e32 v198, 0, v198
	v_max_f32_e32 v199, 0, v199
	v_max_f32_e32 v200, 0, v200
	v_max_f32_e32 v201, 0, v201
	v_sqrt_f32_e32 v194, v194
	v_sqrt_f32_e32 v195, v195
	v_sqrt_f32_e32 v196, v196
	v_sqrt_f32_e32 v197, v197
	v_sqrt_f32_e32 v198, v198
	v_sqrt_f32_e32 v199, v199
	v_sqrt_f32_e32 v200, v200
	v_sqrt_f32_e32 v201, v201
	s_waitcnt lgkmcnt(0)
	v_lshlrev_b32_e32 v152, 16, v152
	v_lshlrev_b32_e32 v153, 16, v153
	v_lshlrev_b32_e32 v154, 16, v154
	v_lshlrev_b32_e32 v155, 16, v155
	v_lshlrev_b32_e32 v156, 16, v156
	v_lshlrev_b32_e32 v157, 16, v157
	v_lshlrev_b32_e32 v158, 16, v158
	v_lshlrev_b32_e32 v159, 16, v159
	v_mul_f32_e32 v194, v194, v186
	v_mul_f32_e32 v195, v195, v187
	v_mul_f32_e32 v196, v196, v188
	v_mul_f32_e32 v197, v197, v189
	v_mul_f32_e32 v198, v198, v190
	v_mul_f32_e32 v199, v199, v191
	v_mul_f32_e32 v200, v200, v192
	v_mul_f32_e32 v201, v201, v193
	v_mul_f32_e32 v152, v194, v152
	v_mul_f32_e32 v153, v195, v153
	v_mul_f32_e32 v154, v196, v154
	v_mul_f32_e32 v155, v197, v155
	v_mul_f32_e32 v156, v198, v156
	v_mul_f32_e32 v157, v199, v157
	v_mul_f32_e32 v158, v200, v158
	v_mul_f32_e32 v159, v201, v159
	v_fma_f32 v146, v98, v147, v146
	v_fma_f32 v150, v102, v151, v150
	v_fma_f32 v154, v106, v155, v154
	v_fma_f32 v158, v110, v159, v158
	v_mul_f32_e32 v98, v98, v99
	v_mul_f32_e32 v102, v102, v103
	v_mul_f32_e32 v106, v106, v107
	v_mul_f32_e32 v110, v110, v111
	v_fma_f32 v145, v97, v146, v145
	v_fma_f32 v149, v101, v150, v149
	v_fma_f32 v153, v105, v154, v153
	v_fma_f32 v157, v109, v158, v157
	v_mul_f32_e32 v97, v97, v98
	v_mul_f32_e32 v101, v101, v102
	v_mul_f32_e32 v105, v105, v106
	v_mul_f32_e32 v109, v109, v110
	v_fma_f32 v144, v96, v145, v144
	v_fma_f32 v148, v100, v149, v148
	v_fma_f32 v152, v104, v153, v152
	v_fma_f32 v156, v108, v157, v156
	v_mul_f32_e32 v96, v96, v97
	v_mul_f32_e32 v100, v100, v101
	v_mul_f32_e32 v104, v104, v105
	v_mul_f32_e32 v108, v108, v109
	ds_bpermute_b32 v178, v204, v96
	ds_bpermute_b32 v182, v204, v144
	ds_bpermute_b32 v179, v204, v100
	ds_bpermute_b32 v183, v204, v148
	ds_bpermute_b32 v180, v204, v104
	ds_bpermute_b32 v184, v204, v152
	ds_bpermute_b32 v181, v204, v108
	ds_bpermute_b32 v185, v204, v156
	s_waitcnt lgkmcnt(0)
	v_fma_f32 v186, v182, v96, v144
	v_cndmask_b32_e64 v178, 1.0, v178, s[34:35]
	v_fma_f32 v187, v183, v100, v148
	v_cndmask_b32_e64 v179, 1.0, v179, s[34:35]
	v_fma_f32 v188, v184, v104, v152
	v_cndmask_b32_e64 v180, 1.0, v180, s[34:35]
	v_fma_f32 v189, v185, v108, v156
	v_cndmask_b32_e64 v181, 1.0, v181, s[34:35]
	v_cndmask_b32_e64 v223, v144, v186, s[34:35]
	v_mul_f32_e32 v219, v96, v178
	v_cndmask_b32_e64 v224, v148, v187, s[34:35]
	v_mul_f32_e32 v220, v100, v179
	v_cndmask_b32_e64 v225, v152, v188, s[34:35]
	v_mul_f32_e32 v221, v104, v180
	v_cndmask_b32_e64 v226, v156, v189, s[34:35]
	v_mul_f32_e32 v222, v108, v181
	ds_bpermute_b32 v178, v205, v219
	ds_bpermute_b32 v182, v205, v223
	ds_bpermute_b32 v179, v205, v220
	ds_bpermute_b32 v183, v205, v224
	ds_bpermute_b32 v180, v205, v221
	ds_bpermute_b32 v184, v205, v225
	ds_bpermute_b32 v181, v205, v222
	ds_bpermute_b32 v185, v205, v226
	s_waitcnt lgkmcnt(0)
	v_fma_f32 v186, v182, v219, v223
	v_cndmask_b32_e64 v178, 1.0, v178, s[36:37]
	v_fma_f32 v187, v183, v220, v224
	v_cndmask_b32_e64 v179, 1.0, v179, s[36:37]
	v_fma_f32 v188, v184, v221, v225
	v_cndmask_b32_e64 v180, 1.0, v180, s[36:37]
	v_fma_f32 v189, v185, v222, v226
	v_cndmask_b32_e64 v181, 1.0, v181, s[36:37]
	v_cndmask_b32_e64 v223, v223, v186, s[36:37]
	v_mul_f32_e32 v219, v219, v178
	v_cndmask_b32_e64 v224, v224, v187, s[36:37]
	v_mul_f32_e32 v220, v220, v179
	v_cndmask_b32_e64 v225, v225, v188, s[36:37]
	v_mul_f32_e32 v221, v221, v180
	v_cndmask_b32_e64 v226, v226, v189, s[36:37]
	v_mul_f32_e32 v222, v222, v181
	ds_bpermute_b32 v227, v204, v219
	ds_bpermute_b32 v231, v204, v223
	ds_bpermute_b32 v235, v206, v219
	ds_bpermute_b32 v239, v206, v223
	ds_bpermute_b32 v228, v204, v220
	ds_bpermute_b32 v232, v204, v224
	ds_bpermute_b32 v236, v206, v220
	ds_bpermute_b32 v244, v206, v224
	ds_bpermute_b32 v229, v204, v221
	ds_bpermute_b32 v233, v204, v225
	ds_bpermute_b32 v237, v206, v221
	ds_bpermute_b32 v245, v206, v225
	ds_bpermute_b32 v230, v204, v222
	ds_bpermute_b32 v234, v204, v226
	ds_bpermute_b32 v238, v206, v222
	ds_bpermute_b32 v246, v206, v226
	s_waitcnt lgkmcnt(0)
	v_cndmask_b32_e64 v227, 1.0, v227, s[34:35]
	v_cndmask_b32_e64 v231, 0, v231, s[34:35]
	v_cndmask_b32_e64 v228, 1.0, v228, s[34:35]
	v_cndmask_b32_e64 v232, 0, v232, s[34:35]
	v_cndmask_b32_e64 v229, 1.0, v229, s[34:35]
	v_cndmask_b32_e64 v233, 0, v233, s[34:35]
	v_cndmask_b32_e64 v230, 1.0, v230, s[34:35]
	v_cndmask_b32_e64 v234, 0, v234, s[34:35]
	v_mov_b32_e32 v190, v238
	v_mov_b32_e32 v194, v246
	v_mov_b32_e32 v198, v190
	v_mov_b32_e32 v201, v194
	v_fma_f32 v194, v194, v237, v245
	v_mul_f32_e32 v190, v190, v237
	v_mov_b32_e32 v199, v190
	v_mov_b32_e32 v177, v194
	v_fma_f32 v194, v194, v236, v244
	v_mul_f32_e32 v190, v190, v236
	v_mov_b32_e32 v200, v190
	v_mov_b32_e32 v203, v194
	v_fma_f32 v194, v194, v235, v239
	v_mul_f32_e32 v190, v190, v235
	v_mov_b32_e32 v191, v194
	ds_write_b64 v207, v[190:191] offset:1024
	s_waitcnt lgkmcnt(0)
	s_barrier
	ds_read_b64 v[178:179], v208 offset:1536
	ds_read_b64 v[180:181], v208 offset:1024
	s_waitcnt lgkmcnt(0)
	v_fma_f32 v182, v176, v178, v179
	v_cndmask_b32_e64 v183, v176, v182, s[38:39]
	v_fma_f32 v176, v182, v180, v181
	v_fma_f32 v184, v183, v200, v203
	v_fma_f32 v185, v183, v199, v177
	v_fma_f32 v186, v183, v198, v201
	v_mov_b32_e32 v187, v183
	v_fma_f32 v184, v184, v227, v231
	v_fma_f32 v185, v185, v228, v232
	v_fma_f32 v186, v186, v229, v233
	v_fma_f32 v187, v187, v230, v234
	v_fma_f32 v144, v184, v96, v144
	v_fma_f32 v148, v185, v100, v148
	v_fma_f32 v152, v186, v104, v152
	v_fma_f32 v156, v187, v108, v156
	v_fma_f32 v145, v184, v97, v145
	v_fma_f32 v149, v185, v101, v149
	v_fma_f32 v153, v186, v105, v153
	v_fma_f32 v157, v187, v109, v157
	v_fma_f32 v146, v184, v98, v146
	v_fma_f32 v150, v185, v102, v150
	v_fma_f32 v154, v186, v106, v154
	v_fma_f32 v158, v187, v110, v158
	v_fma_f32 v147, v184, v99, v147
	v_fma_f32 v151, v185, v103, v151
	v_fma_f32 v155, v186, v107, v155
	v_fma_f32 v159, v187, v111, v159
	s_cmp_eq_u32 s13, 17
	s_cbranch_scc1 .Lmylru_w0_8
	s_waitcnt vmcnt(8)
	s_branch .Lmylru_w1_8

.Lmylru_w1_8:
	v_lshlrev_b32_e32 v178, 16, v247
	v_add_f32_e32 v144, v144, v178
	v_lshlrev_b32_e32 v128, 16, v128
	v_mul_f32_e32 v144, v144, v128
	v_cvt_pk_bf16_f32 v144, v144, v144
	v_and_b32_e32 v179, 0xffff0000, v247
	v_add_f32_e32 v145, v145, v179
	v_lshlrev_b32_e32 v129, 16, v129
	v_mul_f32_e32 v145, v145, v129
	v_cvt_pk_bf16_f32 v145, v145, v145
	v_lshlrev_b32_e32 v180, 16, v248
	v_add_f32_e32 v146, v146, v180
	v_lshlrev_b32_e32 v130, 16, v130
	v_mul_f32_e32 v146, v146, v130
	v_cvt_pk_bf16_f32 v146, v146, v146
	v_and_b32_e32 v181, 0xffff0000, v248
	v_add_f32_e32 v147, v147, v181
	v_lshlrev_b32_e32 v131, 16, v131
	v_mul_f32_e32 v147, v147, v131
	v_cvt_pk_bf16_f32 v147, v147, v147
	v_lshlrev_b32_e32 v178, 16, v249
	v_add_f32_e32 v148, v148, v178
	v_lshlrev_b32_e32 v132, 16, v132
	v_mul_f32_e32 v148, v148, v132
	v_cvt_pk_bf16_f32 v148, v148, v148
	v_and_b32_e32 v179, 0xffff0000, v249
	v_add_f32_e32 v149, v149, v179
	v_lshlrev_b32_e32 v133, 16, v133
	v_mul_f32_e32 v149, v149, v133
	v_cvt_pk_bf16_f32 v149, v149, v149
	v_lshlrev_b32_e32 v180, 16, v250
	v_add_f32_e32 v150, v150, v180
	v_lshlrev_b32_e32 v134, 16, v134
	v_mul_f32_e32 v150, v150, v134
	v_cvt_pk_bf16_f32 v150, v150, v150
	v_and_b32_e32 v181, 0xffff0000, v250
	v_add_f32_e32 v151, v151, v181
	v_lshlrev_b32_e32 v135, 16, v135
	v_mul_f32_e32 v151, v151, v135
	v_cvt_pk_bf16_f32 v151, v151, v151
	v_lshlrev_b32_e32 v178, 16, v251
	v_add_f32_e32 v152, v152, v178
	v_lshlrev_b32_e32 v136, 16, v136
	v_mul_f32_e32 v152, v152, v136
	v_cvt_pk_bf16_f32 v152, v152, v152
	v_and_b32_e32 v179, 0xffff0000, v251
	v_add_f32_e32 v153, v153, v179
	v_lshlrev_b32_e32 v137, 16, v137
	v_mul_f32_e32 v153, v153, v137
	v_cvt_pk_bf16_f32 v153, v153, v153
	v_lshlrev_b32_e32 v180, 16, v252
	v_add_f32_e32 v154, v154, v180
	v_lshlrev_b32_e32 v138, 16, v138
	v_mul_f32_e32 v154, v154, v138
	v_cvt_pk_bf16_f32 v154, v154, v154
	v_and_b32_e32 v181, 0xffff0000, v252
	v_add_f32_e32 v155, v155, v181
	v_lshlrev_b32_e32 v139, 16, v139
	v_mul_f32_e32 v155, v155, v139
	v_cvt_pk_bf16_f32 v155, v155, v155
	v_lshlrev_b32_e32 v178, 16, v253
	v_add_f32_e32 v156, v156, v178
	v_lshlrev_b32_e32 v140, 16, v140
	v_mul_f32_e32 v156, v156, v140
	v_cvt_pk_bf16_f32 v156, v156, v156
	v_and_b32_e32 v179, 0xffff0000, v253
	v_add_f32_e32 v157, v157, v179
	v_lshlrev_b32_e32 v141, 16, v141
	v_mul_f32_e32 v157, v157, v141
	v_cvt_pk_bf16_f32 v157, v157, v157
	v_lshlrev_b32_e32 v180, 16, v254
	v_add_f32_e32 v158, v158, v180
	v_lshlrev_b32_e32 v142, 16, v142
	v_mul_f32_e32 v158, v158, v142
	v_cvt_pk_bf16_f32 v158, v158, v158
	v_and_b32_e32 v181, 0xffff0000, v254
	v_add_f32_e32 v159, v159, v181
	v_lshlrev_b32_e32 v143, 16, v143
	v_mul_f32_e32 v159, v159, v143
	v_cvt_pk_bf16_f32 v159, v159, v159
	ds_write_b16 v169, v144
	ds_write_b16 v169, v145 offset:128
	ds_write_b16 v169, v146 offset:256
	ds_write_b16 v169, v147 offset:384
	ds_write_b16 v169, v148 offset:2048
	ds_write_b16 v169, v149 offset:2176
	ds_write_b16 v169, v150 offset:2304
	ds_write_b16 v169, v151 offset:2432
	ds_write_b16 v169, v152 offset:4096
	ds_write_b16 v169, v153 offset:4224
	ds_write_b16 v169, v154 offset:4352
	ds_write_b16 v169, v155 offset:4480
	ds_write_b16 v169, v156 offset:6144
	ds_write_b16 v169, v157 offset:6272
	ds_write_b16 v169, v158 offset:6400
	ds_write_b16 v169, v159 offset:6528
	s_mov_b64 s[62:63], s[42:43]
	s_add_i32 s13, s13, 1
	s_add_i32 s60, s60, -1
	s_cmp_lg_u32 s60, 0
	s_cbranch_scc1 .Lmylru_loop_1
	s_waitcnt lgkmcnt(0)
	s_barrier
	ds_read_b128 v[178:181], v170
	ds_read_b128 v[182:185], v170 offset:1024
	s_waitcnt lgkmcnt(0)
	global_store_dwordx4 v171, v[178:181], s[62:63]
	global_store_dwordx4 v172, v[182:185], s[62:63]
	s_waitcnt vmcnt(0) lgkmcnt(0)
